# v34 + lever 7: wave_sum butterflies in P1/P6/P9 via DPP movs + v_permlane16/32_swap instead of ds_bpermute (bit-identical order)
# speedup vs baseline: 1.0065x; 1.0043x over previous
; __device__ __forceinline__ void p1_ln_mod(Frame& F) {
;     ...
;         const f32x4* xr = (const f32x4*)src + F.lane; f32x4 v[8]; float s = 0.f;
; #pragma unroll
;         for (int j = 0; j < 8; ++j) { v[j] = xr[64 * j]; s += (v[j][0] + v[j][1]) + (v[j][2] + v[j][3]); }
;         const float mean = wave_sum(s) * (1.f / DM); float s2 = 0.f;
; #pragma unroll
;         for (int j = 0; j < 8; ++j) { v[j] = v[j] - mean; s2 += (v[j][0] * v[j][0] + v[j][1] * v[j][1]) + (v[j][2] * v[j][2] + v[j][3] * v[j][3]); }
;         const float rstd = 1.f / sqrtf(wave_sum(s2) * (1.f / DM) + LN_EPS);
.LBB0_189:
	global_load_dwordx4 v[30:33], v34, s[0:1] nt
	global_load_dwordx4 v[26:29], v34, s[0:1] offset:1024 nt
	global_load_dwordx4 v[22:25], v34, s[0:1] offset:2048 nt
	global_load_dwordx4 v[18:21], v34, s[0:1] offset:3072 nt
	v_lshl_add_u64 v[2:3], s[0:1], 0, v[34:35]
	v_add_co_u32_e32 v2, vcc, s42, v2
	s_ashr_i32 s13, s12, 31
	s_nop 0
	v_addc_co_u32_e32 v3, vcc, 0, v3, vcc
	global_load_dwordx4 v[14:17], v[2:3], off nt
	global_load_dwordx4 v[10:13], v[2:3], off offset:1024 nt
	global_load_dwordx4 v[6:9], v[2:3], off offset:2048 nt
	s_nop 0
	global_load_dwordx4 v[2:5], v[2:3], off offset:3072 nt
	s_lshl_b64 s[38:39], s[12:13], 11
	s_lshl_b64 s[0:1], s[12:13], 12
	s_add_u32 s24, s20, 0x2000
	s_addc_u32 s25, s21, 0
	s_add_i32 s12, s12, s3
	s_cmpk_lt_i32 s12, 0x2200
	s_waitcnt vmcnt(7)
	v_mov_b32_e32 v56, v30
	s_waitcnt vmcnt(6)
	v_mov_b32_e32 v57, v26
	v_mov_b32_e32 v58, v31
	v_mov_b32_e32 v59, v27
	v_mov_b32_e32 v60, v32
	v_mov_b32_e32 v61, v28
	v_mov_b32_e32 v62, v33
	v_mov_b32_e32 v63, v29
	s_waitcnt vmcnt(5)
	v_mov_b32_e32 v64, v23
	v_mov_b32_e32 v65, v24
	v_mov_b32_e32 v66, v22
	v_mov_b32_e32 v67, v25
	v_pk_add_f32 v[56:57], v[56:57], v[58:59]
	v_pk_add_f32 v[58:59], v[60:61], v[62:63]
	v_pk_add_f32 v[60:61], v[64:65], v[66:67]
	v_pk_add_f32 v[56:57], v[56:57], v[58:59]
	v_pk_add_f32 v[58:59], v[60:61], v[60:61] op_sel:[0,1] op_sel_hi:[1,0]
	v_add_f32_e32 v56, 0, v56
	s_waitcnt vmcnt(4)
	v_add_f32_e32 v68, v18, v19
	v_add_f32_e32 v70, v20, v21
	s_waitcnt vmcnt(3)
	v_mov_b32_e32 v61, v14
	v_mov_b32_e32 v69, v16
	v_mov_b32_e32 v71, v17
	v_mov_b32_e32 v59, v15
	v_add_f32_e32 v60, v56, v57
	s_waitcnt vmcnt(2)
	v_mov_b32_e32 v62, v11
	v_mov_b32_e32 v63, v12
	v_mov_b32_e32 v64, v10
	v_mov_b32_e32 v65, v13
	v_pk_add_f32 v[68:69], v[68:69], v[70:71]
	v_pk_add_f32 v[58:59], v[60:61], v[58:59]
	v_pk_add_f32 v[62:63], v[62:63], v[64:65]
	v_pk_add_f32 v[58:59], v[58:59], v[68:69]
	v_pk_add_f32 v[56:57], v[62:63], v[62:63] op_sel:[0,1] op_sel_hi:[1,0]
	v_pk_add_f32 v[58:59], v[58:59], v[58:59] op_sel:[0,1] op_sel_hi:[1,0]
	s_waitcnt vmcnt(1)
	v_add_f32_e32 v66, v6, v7
	v_add_f32_e32 v72, v8, v9
	s_waitcnt vmcnt(0)
	v_mov_b32_e32 v67, v4
	v_mov_b32_e32 v73, v5
	v_mov_b32_e32 v57, v3
	v_mov_b32_e32 v59, v2
	v_pk_add_f32 v[64:65], v[66:67], v[72:73]
	v_pk_add_f32 v[56:57], v[58:59], v[56:57]
	s_nop 0
	v_pk_add_f32 v[56:57], v[56:57], v[64:65]
	s_nop 0
	v_add_f32_e32 v56, v56, v57
	s_nop 1
	v_mov_b32_dpp v57, v56 quad_perm:[1,0,3,2] row_mask:0xf bank_mask:0xf
	s_waitcnt lgkmcnt(0)
	v_add_f32_e32 v56, v56, v57
	s_nop 1
	v_mov_b32_dpp v57, v56 quad_perm:[2,3,0,1] row_mask:0xf bank_mask:0xf
	s_waitcnt lgkmcnt(0)
	v_add_f32_e32 v56, v56, v57
	s_nop 1
	v_mov_b32_dpp v57, v56 row_shl:4 row_mask:0xf bank_mask:0x5
	s_nop 1
	v_mov_b32_dpp v57, v56 row_shr:4 row_mask:0xf bank_mask:0xa
	s_waitcnt lgkmcnt(0)
	v_add_f32_e32 v56, v56, v57
	s_nop 1
	v_mov_b32_dpp v57, v56 row_ror:8 row_mask:0xf bank_mask:0xf
	s_waitcnt lgkmcnt(0)
	v_add_f32_e32 v56, v56, v57
	v_mov_b32_e32 v57, v56
	s_nop 1
	v_permlane16_swap_b32_e32 v57, v56
	s_waitcnt lgkmcnt(0)
	v_add_f32_e32 v56, v56, v57
	v_mov_b32_e32 v57, v56
	s_nop 1
	v_permlane32_swap_b32_e32 v57, v56
	s_waitcnt lgkmcnt(0)
	v_add_f32_e32 v78, v56, v57
	v_fmamk_f32 v33, v78, 0xba000000, v33
	v_fmamk_f32 v31, v78, 0xba000000, v31
	v_fmamk_f32 v65, v78, 0xba000000, v29
	v_fmamk_f32 v27, v78, 0xba000000, v27
	v_fmamk_f32 v67, v78, 0xba000000, v23
	v_fmamk_f32 v66, v78, 0xba000000, v22
	v_fmamk_f32 v25, v78, 0xba000000, v25
	v_fmac_f32_e32 v24, 0xba000000, v78
	v_fmamk_f32 v68, v78, 0xba000000, v18
	v_fmac_f32_e32 v20, 0xba000000, v78
	v_fmamk_f32 v11, v78, 0xba000000, v11
	v_fmamk_f32 v10, v78, 0xba000000, v10
	v_fmamk_f32 v13, v78, 0xba000000, v13
	v_fmac_f32_e32 v12, 0xba000000, v78
	v_fmamk_f32 v32, v78, 0xba000000, v32
	v_fmac_f32_e32 v30, 0xba000000, v78
	v_fmamk_f32 v64, v78, 0xba000000, v28
	v_fmac_f32_e32 v26, 0xba000000, v78
	v_fmamk_f32 v69, v78, 0xba000000, v19
	v_fmamk_f32 v21, v78, 0xba000000, v21
	v_mov_b32_e32 v22, v31
	v_mov_b32_e32 v23, v27
	v_mov_b32_e32 v56, v33
	v_mov_b32_e32 v57, v65
	v_pk_mul_f32 v[58:59], v[24:25], v[24:25]
	v_pk_mul_f32 v[60:61], v[66:67], v[66:67]
	v_mul_f32_e32 v62, v68, v68
	v_mul_f32_e32 v70, v20, v20
	v_pk_mul_f32 v[72:73], v[12:13], v[12:13]
	v_pk_mul_f32 v[74:75], v[10:11], v[10:11]
	v_fmamk_f32 v19, v78, 0xba000000, v17
	v_fmamk_f32 v18, v78, 0xba000000, v16
	v_fmamk_f32 v15, v78, 0xba000000, v15
	v_fmac_f32_e32 v14, 0xba000000, v78
	v_mov_b32_e32 v16, v30
	v_mov_b32_e32 v17, v26
	v_mov_b32_e32 v28, v32
	v_mov_b32_e32 v29, v64
	v_pk_mul_f32 v[22:23], v[22:23], v[22:23]
	v_pk_mul_f32 v[56:57], v[56:57], v[56:57]
	v_pk_mov_b32 v[76:77], v[60:61], v[58:59] op_sel:[1,0]
	v_mov_b32_e32 v61, v59
	v_pk_fma_f32 v[58:59], v[68:69], v[68:69], v[62:63] op_sel_hi:[1,1,0]
	v_pk_fma_f32 v[62:63], v[20:21], v[20:21], v[70:71] op_sel_hi:[1,1,0]
	v_pk_mov_b32 v[70:71], v[74:75], v[72:73] op_sel:[1,0]
	v_mov_b32_e32 v75, v73
	v_pk_fma_f32 v[16:17], v[16:17], v[16:17], v[22:23]
	v_pk_fma_f32 v[22:23], v[28:29], v[28:29], v[56:57]
	v_pk_add_f32 v[28:29], v[76:77], v[60:61]
	v_mul_f32_e32 v58, v14, v14
	v_mul_f32_e32 v62, v15, v15
	v_pk_add_f32 v[56:57], v[70:71], v[74:75]
	v_pk_add_f32 v[16:17], v[16:17], v[22:23]
	v_pk_add_f32 v[22:23], v[28:29], v[28:29] op_sel_hi:[0,1]
	v_pk_add_f32 v[28:29], v[58:59], v[62:63]
	v_pk_add_f32 v[70:71], v[56:57], v[56:57] op_sel_hi:[0,1]
	global_load_dwordx4 v[56:59], v34, s[20:21]
	global_load_dwordx4 v[60:63], v34, s[24:25]
	v_pk_add_f32 v[16:17], v[16:17], v[16:17] op_sel_hi:[0,1]
	v_mul_f32_e32 v22, v18, v18
	v_mul_f32_e32 v16, v19, v19
	v_pk_add_f32 v[16:17], v[22:23], v[16:17]
	v_fmac_f32_e32 v8, 0xba000000, v78
	v_pk_add_f32 v[16:17], v[28:29], v[16:17]
	v_fmamk_f32 v9, v78, 0xba000000, v9
	v_pk_add_f32 v[22:23], v[16:17], v[16:17] op_sel_hi:[0,1]
	v_fmamk_f32 v16, v78, 0xba000000, v6
	v_fmamk_f32 v17, v78, 0xba000000, v7
	v_mul_f32_e32 v6, v16, v16
	v_pk_fma_f32 v[6:7], v[16:17], v[16:17], v[6:7] op_sel_hi:[1,1,0]
	v_fmamk_f32 v5, v78, 0xba000000, v5
	v_mul_f32_e32 v6, v8, v8
	v_pk_fma_f32 v[28:29], v[8:9], v[8:9], v[6:7] op_sel_hi:[1,1,0]
	v_fmamk_f32 v4, v78, 0xba000000, v4
	v_fmamk_f32 v3, v78, 0xba000000, v3
	v_fmac_f32_e32 v2, 0xba000000, v78
	v_mul_f32_e32 v6, v2, v2
	v_mul_f32_e32 v28, v3, v3
	v_mul_f32_e32 v70, v4, v4
	v_mul_f32_e32 v22, v5, v5
	v_pk_add_f32 v[6:7], v[6:7], v[28:29]
	v_pk_add_f32 v[22:23], v[70:71], v[22:23]
	s_nop 0
	v_pk_add_f32 v[6:7], v[6:7], v[22:23]
	s_nop 0
	v_add_f32_e32 v6, v6, v7
	s_nop 1
	v_mov_b32_dpp v7, v6 quad_perm:[1,0,3,2] row_mask:0xf bank_mask:0xf
	s_waitcnt lgkmcnt(0)
; __device__ __forceinline__ unsigned cvt_pk_bf16(float lo, float hi) { unsigned r; asm volatile("v_cvt_pk_bf16_f32 %0, %1, %2" : "=v"(r) : "v"(lo), "v"(hi)); return r; }
; __device__ __forceinline__ unsigned pk4_fp8(float a, float b, float c, float d) { int w = 0; w = __builtin_amdgcn_cvt_pk_fp8_f32(a, b, w, false); w = __builtin_amdgcn_cvt_pk_fp8_f32(c, d, w, true); return (unsigned)w; }
; __device__ __forceinline__ void p1_ln_mod(Frame& F) {
;     ...
;         const float mean = wave_sum(s) * (1.f / DM); float s2 = 0.f;
; #pragma unroll
;         for (int j = 0; j < 8; ++j) { v[j] = v[j] - mean; s2 += (v[j][0] * v[j][0] + v[j][1] * v[j][1]) + (v[j][2] * v[j][2] + v[j][3] * v[j][3]); }
;         const float rstd = 1.f / sqrtf(wave_sum(s2) * (1.f / DM) + LN_EPS);
;         u32x2* o8 = (u32x2*)((bf16_t*)(F.ws + WS_U) + (size_t)m * DM) + F.lane;
; #pragma unroll
;         for (int j = 0; j < 8; ++j) { const f32x4 sh = ((const f32x4*)md)[F.lane + 64 * j], sc = ((const f32x4*)(md + 2048))[F.lane + 64 * j];
;             const f32x4 y = v[j] * rstd * (sc + 1.0f) + sh; u32x2 w; w.x = cvt_pk_bf16(y[0], y[1]); w.y = cvt_pk_bf16(y[2], y[3]); o8[64 * j] = w;
;             ((unsigned*)(F.ws + WS_UF8 + (size_t)m * DM))[F.lane + 64 * j] = pk4_fp8(y[0], y[1], y[2], y[3]); }
	v_add_f32_e32 v6, v6, v7
	s_nop 1
	v_mov_b32_dpp v7, v6 quad_perm:[2,3,0,1] row_mask:0xf bank_mask:0xf
	s_waitcnt lgkmcnt(0)
	v_add_f32_e32 v6, v6, v7
	s_nop 1
	v_mov_b32_dpp v7, v6 row_shl:4 row_mask:0xf bank_mask:0x5
	s_nop 1
	v_mov_b32_dpp v7, v6 row_shr:4 row_mask:0xf bank_mask:0xa
	s_waitcnt lgkmcnt(0)
	v_add_f32_e32 v6, v6, v7
	s_nop 1
	v_mov_b32_dpp v7, v6 row_ror:8 row_mask:0xf bank_mask:0xf
	s_waitcnt lgkmcnt(0)
	v_add_f32_e32 v6, v6, v7
	v_mov_b32_e32 v7, v6
	s_nop 1
	v_permlane16_swap_b32_e32 v7, v6
	s_waitcnt lgkmcnt(0)
	v_add_f32_e32 v6, v6, v7
	v_mov_b32_e32 v7, v6
	s_nop 1
	v_permlane32_swap_b32_e32 v7, v6
	s_waitcnt lgkmcnt(0)
	v_add_f32_e32 v6, v6, v7
	v_fmamk_f32 v6, v6, 0x3a000000, v47
	v_mul_f32_e32 v7, 0x4f800000, v6
	v_cmp_gt_f32_e32 vcc, s43, v6
	s_nop 1
	v_cndmask_b32_e32 v22, v6, v7, vcc
	v_sqrt_f32_e32 v23, v22
	v_lshl_add_u64 v[6:7], v[36:37], 0, s[0:1]
	v_add_u32_e32 v28, -1, v23
	v_add_u32_e32 v29, 1, v23
	v_fma_f32 v70, -v28, v23, v22
	v_fma_f32 v71, -v29, v23, v22
	v_cmp_ge_f32_e64 s[0:1], 0, v70
	s_nop 1
	v_cndmask_b32_e64 v23, v23, v28, s[0:1]
	v_cmp_lt_f32_e64 s[0:1], 0, v71
	s_nop 1
	v_cndmask_b32_e64 v23, v23, v29, s[0:1]
	v_mul_f32_e32 v28, 0x37800000, v23
	v_cndmask_b32_e32 v23, v23, v28, vcc
	v_cmp_class_f32_e32 vcc, v22, v48
	s_waitcnt vmcnt(0)
	v_pk_add_f32 v[28:29], v[60:61], 1.0 op_sel_hi:[1,0]
	v_cndmask_b32_e32 v22, v23, v22, vcc
	v_div_scale_f32 v23, s[0:1], v22, v22, 1.0
	v_rcp_f32_e32 v70, v23
	v_div_scale_f32 v60, vcc, 1.0, v22, 1.0
	v_fma_f32 v61, -v23, v70, 1.0
	v_fmac_f32_e32 v70, v61, v70
	v_mul_f32_e32 v61, v60, v70
	v_fma_f32 v71, -v23, v61, v60
	v_fmac_f32_e32 v61, v71, v70
	v_fma_f32 v23, -v23, v61, v60
	v_div_fmas_f32 v23, v23, v70, v61
	v_div_fixup_f32 v22, v23, v22, 1.0
	v_pk_mul_f32 v[30:31], v[30:31], v[22:23] op_sel_hi:[1,0]
	v_pk_mul_f32 v[32:33], v[32:33], v[22:23] op_sel_hi:[1,0]
	v_pk_fma_f32 v[28:29], v[28:29], v[30:31], v[56:57]
	v_mov_b32_e32 v23, 0
	v_cvt_pk_fp8_f32 v23, v28, v29
	v_pk_add_f32 v[30:31], v[62:63], 1.0 op_sel_hi:[1,0]
	v_cvt_pk_bf16_f32 v28, v28, v29
	s_nop 0
	v_pk_fma_f32 v[30:31], v[30:31], v[32:33], v[58:59]
	v_lshl_add_u64 v[32:33], v[38:39], 0, s[38:39]
	v_cvt_pk_fp8_f32 v23, v30, v31 op_sel:[0,0,1]
	v_cvt_pk_bf16_f32 v29, v30, v31
	global_store_dwordx2 v[6:7], v[28:29], off
	v_lshl_add_u64 v[28:29], v[40:41], 0, s[38:39]
	global_store_dword v[28:29], v23, off
	global_load_dwordx4 v[28:31], v49, s[24:25]
	s_nop 0
	global_load_dwordx4 v[56:59], v34, s[20:21] offset:1024
	v_mov_b32_e32 v23, 0
	v_pk_mul_f32 v[26:27], v[26:27], v[22:23] op_sel_hi:[1,0]
	v_add_co_u32_e32 v60, vcc, s44, v32
	s_waitcnt vmcnt(1)
	v_pk_add_f32 v[28:29], v[28:29], 1.0 op_sel_hi:[1,0]
	s_waitcnt vmcnt(0)
	v_pk_fma_f32 v[26:27], v[28:29], v[26:27], v[56:57]
	v_pk_add_f32 v[30:31], v[30:31], 1.0 op_sel_hi:[1,0]
	v_cvt_pk_fp8_f32 v23, v26, v27
	v_cvt_pk_bf16_f32 v26, v26, v27
	v_addc_co_u32_e32 v61, vcc, 0, v33, vcc
	v_pk_mul_f32 v[28:29], v[64:65], v[22:23] op_sel_hi:[1,0]
	s_nop 0
	v_pk_fma_f32 v[28:29], v[30:31], v[28:29], v[58:59]
	s_nop 0
	v_cvt_pk_fp8_f32 v23, v28, v29 op_sel:[0,0,1]
	v_cvt_pk_bf16_f32 v27, v28, v29
	global_store_dwordx2 v[6:7], v[26:27], off offset:512
	global_store_dword v[60:61], v23, off offset:256
	global_load_dwordx4 v[26:29], v50, s[24:25]
	s_nop 0
	global_load_dwordx4 v[30:33], v34, s[20:21] offset:2048
	v_mov_b32_e32 v23, 0
	v_pk_mul_f32 v[56:57], v[66:67], v[22:23] op_sel_hi:[1,0]
	s_waitcnt vmcnt(1)
	v_pk_add_f32 v[26:27], v[26:27], 1.0 op_sel_hi:[1,0]
	s_waitcnt vmcnt(0)
	v_pk_fma_f32 v[26:27], v[56:57], v[26:27], v[30:31]
	v_pk_add_f32 v[28:29], v[28:29], 1.0 op_sel_hi:[1,0]
	v_cvt_pk_fp8_f32 v23, v26, v27
	v_cvt_pk_bf16_f32 v26, v26, v27
	v_pk_mul_f32 v[24:25], v[24:25], v[22:23] op_sel_hi:[1,0]
	s_nop 0
	v_pk_fma_f32 v[24:25], v[24:25], v[28:29], v[32:33]
	s_nop 0
	v_cvt_pk_fp8_f32 v23, v24, v25 op_sel:[0,0,1]
	v_cvt_pk_bf16_f32 v27, v24, v25
	global_store_dwordx2 v[6:7], v[26:27], off offset:1024
	global_store_dword v[60:61], v23, off offset:512
	global_load_dwordx4 v[24:27], v51, s[24:25]
	s_nop 0
	global_load_dwordx4 v[28:31], v34, s[20:21] offset:3072
	v_mov_b32_e32 v23, 0
	v_pk_mul_f32 v[32:33], v[68:69], v[22:23] op_sel_hi:[1,0]
	s_waitcnt vmcnt(1)
; __device__ __forceinline__ unsigned cvt_pk_bf16(float lo, float hi) { unsigned r; asm volatile("v_cvt_pk_bf16_f32 %0, %1, %2" : "=v"(r) : "v"(lo), "v"(hi)); return r; }
; __device__ __forceinline__ unsigned pk4_fp8(float a, float b, float c, float d) { int w = 0; w = __builtin_amdgcn_cvt_pk_fp8_f32(a, b, w, false); w = __builtin_amdgcn_cvt_pk_fp8_f32(c, d, w, true); return (unsigned)w; }
; __device__ __forceinline__ void p1_ln_mod(Frame& F) {
;     ...
; #pragma unroll
;         for (int j = 0; j < 8; ++j) { const f32x4 sh = ((const f32x4*)md)[F.lane + 64 * j], sc = ((const f32x4*)(md + 2048))[F.lane + 64 * j];
;             const f32x4 y = v[j] * rstd * (sc + 1.0f) + sh; u32x2 w; w.x = cvt_pk_bf16(y[0], y[1]); w.y = cvt_pk_bf16(y[2], y[3]); o8[64 * j] = w;
;             ((unsigned*)(F.ws + WS_UF8 + (size_t)m * DM))[F.lane + 64 * j] = pk4_fp8(y[0], y[1], y[2], y[3]); }
	v_pk_add_f32 v[24:25], v[24:25], 1.0 op_sel_hi:[1,0]
	s_waitcnt vmcnt(0)
	v_pk_fma_f32 v[24:25], v[32:33], v[24:25], v[28:29]
	v_pk_add_f32 v[26:27], v[26:27], 1.0 op_sel_hi:[1,0]
	v_cvt_pk_fp8_f32 v23, v24, v25
	v_cvt_pk_bf16_f32 v24, v24, v25
	v_pk_mul_f32 v[20:21], v[20:21], v[22:23] op_sel_hi:[1,0]
	s_nop 0
	v_pk_fma_f32 v[20:21], v[20:21], v[26:27], v[30:31]
	s_nop 0
	v_cvt_pk_fp8_f32 v23, v20, v21 op_sel:[0,0,1]
	v_cvt_pk_bf16_f32 v25, v20, v21
	global_store_dwordx2 v[6:7], v[24:25], off offset:1536
	global_store_dword v[60:61], v23, off offset:768
	global_load_dwordx4 v[24:27], v52, s[24:25]
	s_nop 0
	global_load_dwordx4 v[28:31], v52, s[20:21]
	v_mov_b32_e32 v23, 0
	v_pk_mul_f32 v[14:15], v[14:15], v[22:23] op_sel_hi:[1,0]
	s_waitcnt vmcnt(1)
	v_pk_add_f32 v[20:21], v[24:25], 1.0 op_sel_hi:[1,0]
	s_waitcnt vmcnt(0)
	v_pk_fma_f32 v[14:15], v[14:15], v[20:21], v[28:29]
	v_pk_add_f32 v[20:21], v[26:27], 1.0 op_sel_hi:[1,0]
	v_cvt_pk_fp8_f32 v23, v14, v15
	v_cvt_pk_bf16_f32 v14, v14, v15
	v_pk_mul_f32 v[18:19], v[18:19], v[22:23] op_sel_hi:[1,0]
	s_nop 0
	v_pk_fma_f32 v[18:19], v[18:19], v[20:21], v[30:31]
	s_nop 0
	v_cvt_pk_fp8_f32 v23, v18, v19 op_sel:[0,0,1]
	v_cvt_pk_bf16_f32 v15, v18, v19
	global_store_dwordx2 v[6:7], v[14:15], off offset:2048
	global_store_dword v[60:61], v23, off offset:1024
	global_load_dwordx4 v[18:21], v53, s[24:25]
	global_load_dwordx4 v[24:27], v53, s[20:21]
	v_mov_b32_e32 v23, 0
	v_pk_mul_f32 v[10:11], v[10:11], v[22:23] op_sel_hi:[1,0]
	s_waitcnt vmcnt(1)
	v_pk_add_f32 v[14:15], v[18:19], 1.0 op_sel_hi:[1,0]
	s_waitcnt vmcnt(0)
	v_pk_fma_f32 v[10:11], v[10:11], v[14:15], v[24:25]
	v_pk_add_f32 v[14:15], v[20:21], 1.0 op_sel_hi:[1,0]
	v_cvt_pk_fp8_f32 v23, v10, v11
	v_cvt_pk_bf16_f32 v10, v10, v11
	v_pk_mul_f32 v[12:13], v[12:13], v[22:23] op_sel_hi:[1,0]
	s_nop 0
	v_pk_fma_f32 v[12:13], v[12:13], v[14:15], v[26:27]
	s_nop 0
	v_cvt_pk_fp8_f32 v23, v12, v13 op_sel:[0,0,1]
	v_cvt_pk_bf16_f32 v11, v12, v13
	global_store_dwordx2 v[6:7], v[10:11], off offset:2560
	global_store_dword v[60:61], v23, off offset:1280
	global_load_dwordx4 v[10:13], v54, s[24:25]
	s_nop 0
	global_load_dwordx4 v[18:21], v54, s[20:21]
	v_mov_b32_e32 v23, 0
	v_pk_mul_f32 v[14:15], v[16:17], v[22:23] op_sel_hi:[1,0]
	s_waitcnt vmcnt(1)
	v_pk_add_f32 v[10:11], v[10:11], 1.0 op_sel_hi:[1,0]
	s_waitcnt vmcnt(0)
	v_pk_fma_f32 v[10:11], v[14:15], v[10:11], v[18:19]
	v_pk_add_f32 v[12:13], v[12:13], 1.0 op_sel_hi:[1,0]
	v_cvt_pk_fp8_f32 v23, v10, v11
	v_cvt_pk_bf16_f32 v10, v10, v11
	v_pk_mul_f32 v[8:9], v[8:9], v[22:23] op_sel_hi:[1,0]
	s_nop 0
	v_pk_fma_f32 v[8:9], v[8:9], v[12:13], v[20:21]
	s_nop 0
	v_cvt_pk_fp8_f32 v23, v8, v9 op_sel:[0,0,1]
	v_cvt_pk_bf16_f32 v11, v8, v9
	global_store_dwordx2 v[6:7], v[10:11], off offset:3072
	global_store_dword v[60:61], v23, off offset:1536
	global_load_dwordx4 v[8:11], v55, s[24:25]
	s_nop 0
	global_load_dwordx4 v[12:15], v55, s[20:21]
	v_pk_mul_f32 v[2:3], v[2:3], v[22:23] op_sel_hi:[1,0]
	v_pk_mul_f32 v[4:5], v[4:5], v[22:23] op_sel_hi:[1,0]
	s_waitcnt vmcnt(1)
	v_pk_add_f32 v[8:9], v[8:9], 1.0 op_sel_hi:[1,0]
	s_waitcnt vmcnt(0)
	v_pk_fma_f32 v[2:3], v[2:3], v[8:9], v[12:13]
	v_mov_b32_e32 v8, 0
	v_cvt_pk_fp8_f32 v8, v2, v3
	v_pk_add_f32 v[10:11], v[10:11], 1.0 op_sel_hi:[1,0]
	v_cvt_pk_bf16_f32 v2, v2, v3
	s_nop 0
	v_pk_fma_f32 v[4:5], v[4:5], v[10:11], v[14:15]
	s_nop 0
	v_cvt_pk_fp8_f32 v8, v4, v5 op_sel:[0,0,1]
	v_cvt_pk_bf16_f32 v3, v4, v5
	global_store_dwordx2 v[6:7], v[2:3], off offset:3584
	global_store_dword v[60:61], v8, off offset:1792
	s_cbranch_scc0 .LBB0_194

; __device__ __forceinline__ float bf_lo(unsigned w) { return __uint_as_float(w << 16); }
; __device__ __forceinline__ float bf_hi(unsigned w) { return __uint_as_float(w & 0xffff0000u); }
; __device__ __forceinline__ void p6_router(Frame& F) {
;     const int t0 = blockIdx.x * 32; if (t0 >= NTOK) return;
;     const float* mod = (const float*)(F.ws + WS_MOD);
;     const int b = t0 >> 12, lane = F.lane, wave = F.wave, tid = F.tid;
;     const bf16_t* ZB = (const bf16_t*)(F.ws + WS_Z); bf16_t* X1 = (bf16_t*)(F.ws + WS_X1);
;     unsigned* U2F = (unsigned*)(F.ws + WS_U2F);
;     const bf16_t* WRH = (const bf16_t*)(F.ws + WS_WRT); const bf16_t* WRL = WRH + 65536;
;     const int fr = lane & 15, fq = lane >> 4;
;     f32x4 acc[2][2];
;     {
;         u32x2 zr[2][8];
; #pragma unroll
;         for (int q = 0; q < 2; ++q)
; #pragma unroll
;             for (int j = 0; j < 8; ++j) zr[q][j] = ((const u32x2*)(ZB + (size_t)(t0 + wave * 4 + q) * DM))[lane + 64 * j];
;         auto pass = [&](const int rp, f32x4 (&accp)[2]) __attribute__((always_inline)) {
;             const int ta = t0 + wave * 4 + 2 * rp;
;             f32x4 pw[8], pb[8];
;             int lop = lane; asm volatile("" : "+v"(lop));
; #pragma unroll
;             for (int j = 0; j < 8; ++j) { pw[j] = ((const f32x4*)F.in[I_LN1W])[lop + 64 * j]; pb[j] = ((const f32x4*)F.in[I_LN1B])[lop + 64 * j]; }
; #pragma unroll
;             for (int q = 0; q < 2; ++q) {
;                 const int t = ta + q; f32x4 v[8]; float s = 0.f;
; #pragma unroll
;                 for (int j = 0; j < 8; ++j) { const u32x2 zb = zr[q][j]; v[j] = (f32x4){bf_lo(zb.x), bf_hi(zb.x), bf_lo(zb.y), bf_hi(zb.y)}; s += (v[j][0] + v[j][1]) + (v[j][2] + v[j][3]); }
;                 float mean = wave_sum(s) * (1.f / DM), s2 = 0.f;
.LBB0_756:
	s_cmp_lt_i32 s34, 7
	s_cselect_b64 s[12:13], -1, 0
	s_and_b64 s[0:1], s[12:13], s[0:1]
	s_andn2_b64 vcc, exec, s[0:1]
	s_cbranch_vccnz .LBB0_931
	s_lshl_b32 s3, s2, 5
	s_cmpk_gt_i32 s3, 0x1fff
	s_cbranch_scc1 .LBB0_931
	s_add_u32 s6, s82, 0x4a600000
	s_addc_u32 s7, s83, 0
	s_add_u32 s42, s82, 0x4e600000
	v_readlane_b32 s46, v255, 8
	s_addc_u32 s43, s83, 0
	s_lshl_b32 s0, s46, 2
	s_add_i32 s4, s0, s3
	s_ashr_i32 s5, s4, 31
	s_lshl_b64 s[16:17], s[4:5], 12
	s_add_u32 s0, s6, s16
	s_addc_u32 s1, s7, s17
	v_lshlrev_b32_e32 v146, 3, v170
	global_load_dwordx2 v[2:3], v146, s[0:1] offset:512
	global_load_dwordx2 v[4:5], v146, s[0:1]
	global_load_dwordx2 v[6:7], v146, s[0:1] offset:1024
	global_load_dwordx2 v[8:9], v146, s[0:1] offset:1536
	global_load_dwordx2 v[10:11], v146, s[0:1] offset:2048
	global_load_dwordx2 v[12:13], v146, s[0:1] offset:2560
	global_load_dwordx2 v[14:15], v146, s[0:1] offset:3072
	global_load_dwordx2 v[16:17], v146, s[0:1] offset:3584
	v_mbcnt_lo_u32_b32 v1, -1, 0
	v_mbcnt_hi_u32_b32 v19, -1, v1
	v_and_b32_e32 v1, 64, v19
	v_xor_b32_e32 v20, 1, v19
	v_add_u32_e32 v26, 64, v1
	v_cmp_lt_i32_e32 vcc, v20, v26
	v_xor_b32_e32 v21, 2, v19
	v_xor_b32_e32 v22, 4, v19
	v_cndmask_b32_e32 v1, v19, v20, vcc
	v_lshlrev_b32_e32 v1, 2, v1
	v_cmp_lt_i32_e32 vcc, v21, v26
	v_xor_b32_e32 v23, 8, v19
	v_xor_b32_e32 v24, 16, v19
	v_cndmask_b32_e32 v20, v19, v21, vcc
	v_lshlrev_b32_e32 v142, 2, v20
	v_cmp_lt_i32_e32 vcc, v22, v26
	v_xor_b32_e32 v25, 32, v19
	s_or_b32 s24, s4, 1
	v_cndmask_b32_e32 v21, v19, v22, vcc
	v_lshlrev_b32_e32 v143, 2, v21
	v_cmp_lt_i32_e32 vcc, v23, v26
	s_ashr_i32 s25, s24, 31
	s_lshl_b64 s[36:37], s[24:25], 12
	v_cndmask_b32_e32 v22, v19, v23, vcc
	v_lshlrev_b32_e32 v144, 2, v22
	v_cmp_lt_i32_e32 vcc, v24, v26
	s_add_u32 s0, s6, s36
	v_mov_b32_e32 v18, v170
	v_cndmask_b32_e32 v23, v19, v24, vcc
	v_lshlrev_b32_e32 v145, 2, v23
	v_cmp_lt_i32_e32 vcc, v25, v26
	s_addc_u32 s1, s7, s37
	global_load_dwordx2 v[86:87], v146, s[0:1]
	global_load_dwordx2 v[88:89], v146, s[0:1] offset:512
	global_load_dwordx2 v[84:85], v146, s[0:1] offset:1024
	global_load_dwordx2 v[82:83], v146, s[0:1] offset:1536
	global_load_dwordx2 v[80:81], v146, s[0:1] offset:2048
	global_load_dwordx2 v[78:79], v146, s[0:1] offset:2560
	global_load_dwordx2 v[76:77], v146, s[0:1] offset:3072
	global_load_dwordx2 v[74:75], v146, s[0:1] offset:3584
	s_movk_i32 s41, 0x1000
	v_mov_b32_e32 v148, 0x358637bd
	s_mov_b32 s45, 0xf800000
	v_mov_b32_e32 v149, 0x260
	s_ashr_i32 s20, s3, 12
	s_add_u32 s40, s82, 0x2c000000
	s_addc_u32 s44, s83, 0
	v_lshlrev_b32_e32 v150, 2, v170
	v_and_b32_e32 v151, 15, v0
	v_lshrrev_b32_e32 v154, 4, v170
	s_waitcnt vmcnt(0)
	v_lshlrev_b32_e32 v111, 16, v2
	v_lshlrev_b32_e32 v110, 16, v4
	v_and_b32_e32 v113, 0xffff0000, v2
	v_and_b32_e32 v112, 0xffff0000, v4
	v_lshlrev_b32_e32 v107, 16, v3
	v_lshlrev_b32_e32 v106, 16, v5
	v_and_b32_e32 v109, 0xffff0000, v3
	v_and_b32_e32 v108, 0xffff0000, v5
	v_lshlrev_b32_e32 v105, 16, v7
	v_lshlrev_b32_e32 v104, 16, v6
	v_and_b32_e32 v7, 0xffff0000, v7
	v_and_b32_e32 v6, 0xffff0000, v6
	v_pk_add_f32 v[2:3], v[110:111], v[112:113]
	v_pk_add_f32 v[4:5], v[106:107], v[108:109]
	v_lshlrev_b32_e32 v117, 16, v10
	v_and_b32_e32 v69, 0xffff0000, v10
	v_lshlrev_b32_e32 v101, 16, v11
	v_and_b32_e32 v67, 0xffff0000, v11
	v_pk_add_f32 v[10:11], v[104:105], v[6:7]
	v_pk_add_f32 v[2:3], v[2:3], v[4:5]
	v_lshlrev_b32_e32 v70, 16, v8
	v_and_b32_e32 v71, 0xffff0000, v8
	v_lshlrev_b32_e32 v72, 16, v9
	v_and_b32_e32 v73, 0xffff0000, v9
	v_pk_add_f32 v[4:5], v[10:11], v[10:11] op_sel:[0,1] op_sel_hi:[1,0]
	v_add_f32_e32 v2, 0, v2
	v_add_f32_e32 v100, v70, v71
	v_add_f32_e32 v66, v72, v73
	v_mov_b32_e32 v5, v69
	v_add_f32_e32 v116, v2, v3
	v_lshlrev_b32_e32 v99, 16, v13
	v_lshlrev_b32_e32 v98, 16, v12
	v_and_b32_e32 v9, 0xffff0000, v13
	v_and_b32_e32 v8, 0xffff0000, v12
	v_pk_add_f32 v[10:11], v[100:101], v[66:67]
	v_pk_add_f32 v[2:3], v[116:117], v[4:5]
	v_pk_add_f32 v[12:13], v[98:99], v[8:9]
	v_pk_add_f32 v[2:3], v[2:3], v[10:11]
	v_lshlrev_b32_e32 v94, 16, v14
	v_and_b32_e32 v95, 0xffff0000, v14
	v_lshlrev_b32_e32 v96, 16, v15
	v_and_b32_e32 v97, 0xffff0000, v15
	v_lshlrev_b32_e32 v92, 16, v16
	v_and_b32_e32 v93, 0xffff0000, v16
	v_pk_add_f32 v[12:13], v[12:13], v[12:13] op_sel:[0,1] op_sel_hi:[1,0]
	v_pk_add_f32 v[2:3], v[2:3], v[2:3] op_sel:[0,1] op_sel_hi:[1,0]
	v_lshlrev_b32_e32 v103, 16, v17
	v_and_b32_e32 v91, 0xffff0000, v17
	v_add_f32_e32 v102, v94, v95
	v_add_f32_e32 v90, v96, v97
	v_mov_b32_e32 v13, v93
	v_mov_b32_e32 v3, v92
	v_pk_add_f32 v[14:15], v[102:103], v[90:91]
	v_pk_add_f32 v[2:3], v[2:3], v[12:13]
	v_cndmask_b32_e32 v4, v19, v25, vcc
	v_pk_add_f32 v[2:3], v[2:3], v[14:15]
	v_lshlrev_b32_e32 v147, 2, v4
	v_add_f32_e32 v2, v2, v3
	s_nop 1
	v_mov_b32_dpp v3, v2 quad_perm:[1,0,3,2] row_mask:0xf bank_mask:0xf
	v_ashrrev_i32_e32 v19, 31, v18
	v_and_b32_e32 v135, 0xffff0000, v79
	v_and_b32_e32 v134, 0xffff0000, v78
	s_waitcnt lgkmcnt(0)
	v_add_f32_e32 v2, v2, v3
	s_nop 1
	v_mov_b32_dpp v3, v2 quad_perm:[2,3,0,1] row_mask:0xf bank_mask:0xf
	s_waitcnt lgkmcnt(0)
	v_add_f32_e32 v2, v2, v3
	s_nop 1
	v_mov_b32_dpp v3, v2 row_shl:4 row_mask:0xf bank_mask:0x5
	s_nop 1
	v_mov_b32_dpp v3, v2 row_shr:4 row_mask:0xf bank_mask:0xa
	s_waitcnt lgkmcnt(0)
	v_add_f32_e32 v2, v2, v3
	s_nop 1
	v_mov_b32_dpp v3, v2 row_ror:8 row_mask:0xf bank_mask:0xf
	s_waitcnt lgkmcnt(0)
	v_add_f32_e32 v2, v2, v3
	v_mov_b32_e32 v3, v2
	s_nop 1
	v_permlane16_swap_b32_e32 v3, v2
	s_waitcnt lgkmcnt(0)
; __device__ __forceinline__ float bf_lo(unsigned w) { return __uint_as_float(w << 16); }
; __device__ __forceinline__ float bf_hi(unsigned w) { return __uint_as_float(w & 0xffff0000u); }
; __device__ __forceinline__ void p6_router(Frame& F) {
;     ...
;             for (int j = 0; j < 8; ++j) { pw[j] = ((const f32x4*)F.in[I_LN1W])[lop + 64 * j]; pb[j] = ((const f32x4*)F.in[I_LN1B])[lop + 64 * j]; }
; #pragma unroll
;             for (int q = 0; q < 2; ++q) {
;                 const int t = ta + q; f32x4 v[8]; float s = 0.f;
; #pragma unroll
;                 for (int j = 0; j < 8; ++j) { const u32x2 zb = zr[q][j]; v[j] = (f32x4){bf_lo(zb.x), bf_hi(zb.x), bf_lo(zb.y), bf_hi(zb.y)}; s += (v[j][0] + v[j][1]) + (v[j][2] + v[j][3]); }
;                 float mean = wave_sum(s) * (1.f / DM), s2 = 0.f;
; #pragma unroll
;                 for (int j = 0; j < 8; ++j) { v[j] = v[j] - mean; s2 += (v[j][0] * v[j][0] + v[j][1] * v[j][1]) + (v[j][2] * v[j][2] + v[j][3] * v[j][3]); }
;                 float rstd = 1.f / sqrtf(wave_sum(s2) * (1.f / DM) + LN_EPS);
	v_add_f32_e32 v14, v2, v3
	v_mov_b32_e32 v15, v14
	s_nop 1
	v_permlane32_swap_b32_e32 v15, v14
	v_lshlrev_b64 v[2:3], 4, v[18:19]
	v_lshl_add_u64 v[10:11], s[8:9], 0, v[2:3]
	v_lshl_add_u64 v[12:13], s[10:11], 0, v[2:3]
	global_load_dwordx4 v[2:5], v[10:11], off
	s_waitcnt lgkmcnt(0)
	v_add_f32_e32 v20, v14, v15
	v_fmac_f32_e32 v108, 0xba000000, v20
	v_fmac_f32_e32 v112, 0xba000000, v20
	v_fmac_f32_e32 v109, 0xba000000, v20
	v_fmac_f32_e32 v113, 0xba000000, v20
	v_fmac_f32_e32 v106, 0xba000000, v20
	v_fmac_f32_e32 v110, 0xba000000, v20
	v_fmac_f32_e32 v107, 0xba000000, v20
	v_fmac_f32_e32 v111, 0xba000000, v20
	v_pk_mul_f32 v[14:15], v[112:113], v[112:113]
	v_pk_mul_f32 v[16:17], v[108:109], v[108:109]
	v_fmac_f32_e32 v6, 0xba000000, v20
	v_fmac_f32_e32 v7, 0xba000000, v20
	v_fmac_f32_e32 v105, 0xba000000, v20
	v_pk_fma_f32 v[14:15], v[110:111], v[110:111], v[14:15]
	v_pk_fma_f32 v[16:17], v[106:107], v[106:107], v[16:17]
	v_fmac_f32_e32 v104, 0xba000000, v20
	v_mov_b32_e32 v120, v105
	v_mov_b32_e32 v121, v7
	v_mov_b32_e32 v105, v6
	v_pk_add_f32 v[14:15], v[14:15], v[16:17]
	v_pk_mul_f32 v[16:17], v[120:121], v[120:121]
	v_pk_mul_f32 v[6:7], v[104:105], v[104:105]
	v_fmac_f32_e32 v70, 0xba000000, v20
	v_pk_mov_b32 v[18:19], v[6:7], v[16:17] op_sel:[1,0]
	v_mov_b32_e32 v7, v17
	v_pk_add_f32 v[6:7], v[18:19], v[6:7]
	v_fmac_f32_e32 v71, 0xba000000, v20
	v_pk_add_f32 v[6:7], v[6:7], v[6:7] op_sel_hi:[0,1]
	v_fmac_f32_e32 v72, 0xba000000, v20
	v_mul_f32_e32 v6, v70, v70
	v_fmac_f32_e32 v73, 0xba000000, v20
	v_pk_fma_f32 v[16:17], v[70:71], v[70:71], v[6:7] op_sel_hi:[1,1,0]
	v_mul_f32_e32 v6, v72, v72
	v_pk_add_f32 v[14:15], v[14:15], v[14:15] op_sel_hi:[0,1]
	v_pk_fma_f32 v[18:19], v[72:73], v[72:73], v[6:7] op_sel_hi:[1,1,0]
	v_fmac_f32_e32 v67, 0xba000000, v20
	v_fmac_f32_e32 v101, 0xba000000, v20
	v_fmac_f32_e32 v69, 0xba000000, v20
	v_fmac_f32_e32 v117, 0xba000000, v20
	v_mul_f32_e32 v16, v117, v117
	v_mul_f32_e32 v18, v69, v69
	v_mul_f32_e32 v6, v101, v101
	v_mul_f32_e32 v14, v67, v67
	v_pk_add_f32 v[16:17], v[16:17], v[18:19]
	v_pk_add_f32 v[6:7], v[6:7], v[14:15]
	v_fmac_f32_e32 v8, 0xba000000, v20
	v_fmac_f32_e32 v9, 0xba000000, v20
	v_fmac_f32_e32 v99, 0xba000000, v20
	v_pk_add_f32 v[6:7], v[16:17], v[6:7]
	v_fmac_f32_e32 v98, 0xba000000, v20
	v_mov_b32_e32 v118, v99
	v_mov_b32_e32 v119, v9
	v_mov_b32_e32 v99, v8
	v_pk_add_f32 v[6:7], v[6:7], v[6:7] op_sel_hi:[0,1]
	v_pk_mul_f32 v[14:15], v[118:119], v[118:119]
	v_pk_mul_f32 v[8:9], v[98:99], v[98:99]
	v_fmac_f32_e32 v94, 0xba000000, v20
	v_pk_mov_b32 v[16:17], v[8:9], v[14:15] op_sel:[1,0]
	v_mov_b32_e32 v9, v15
	v_fmac_f32_e32 v95, 0xba000000, v20
	v_fmac_f32_e32 v96, 0xba000000, v20
	v_mul_f32_e32 v6, v94, v94
	v_pk_add_f32 v[8:9], v[16:17], v[8:9]
	v_fmac_f32_e32 v97, 0xba000000, v20
	v_pk_fma_f32 v[14:15], v[94:95], v[94:95], v[6:7] op_sel_hi:[1,1,0]
	v_mul_f32_e32 v6, v96, v96
	v_pk_add_f32 v[8:9], v[8:9], v[8:9] op_sel_hi:[0,1]
	v_pk_fma_f32 v[16:17], v[96:97], v[96:97], v[6:7] op_sel_hi:[1,1,0]
	v_fmac_f32_e32 v91, 0xba000000, v20
	v_fmac_f32_e32 v103, 0xba000000, v20
	v_fmac_f32_e32 v93, 0xba000000, v20
	v_fmac_f32_e32 v92, 0xba000000, v20
	v_mul_f32_e32 v14, v92, v92
	v_mul_f32_e32 v16, v93, v93
	v_mul_f32_e32 v8, v103, v103
	v_mul_f32_e32 v6, v91, v91
	v_pk_add_f32 v[14:15], v[14:15], v[16:17]
	v_pk_add_f32 v[6:7], v[8:9], v[6:7]
	global_load_dwordx4 v[62:65], v[12:13], off
	v_pk_add_f32 v[6:7], v[14:15], v[6:7]
	global_load_dwordx4 v[54:57], v[10:11], off offset:1024
	global_load_dwordx4 v[58:61], v[12:13], off offset:1024
	v_add_f32_e32 v6, v6, v7
	s_nop 1
	v_mov_b32_dpp v7, v6 quad_perm:[1,0,3,2] row_mask:0xf bank_mask:0xf
	global_load_dwordx4 v[46:49], v[10:11], off offset:2048
	global_load_dwordx4 v[38:41], v[10:11], off offset:3072
	global_load_dwordx4 v[50:53], v[12:13], off offset:2048
	global_load_dwordx4 v[42:45], v[12:13], off offset:3072
	v_mov_b32_e32 v124, v107
	v_mov_b32_e32 v107, v108
	v_mov_b32_e32 v122, v111
	s_waitcnt lgkmcnt(0)
	v_add_f32_e32 v6, v6, v7
	s_nop 1
	v_mov_b32_dpp v7, v6 quad_perm:[2,3,0,1] row_mask:0xf bank_mask:0xf
	v_mov_b32_e32 v123, v113
	v_mov_b32_e32 v111, v112
	v_mov_b32_e32 v125, v109
	s_waitcnt lgkmcnt(0)
	v_add_f32_e32 v8, v6, v7
	s_nop 1
	v_mov_b32_dpp v9, v8 row_shl:4 row_mask:0xf bank_mask:0x5
	s_nop 1
	v_mov_b32_dpp v9, v8 row_shr:4 row_mask:0xf bank_mask:0xa
	v_add_co_u32_e32 v6, vcc, s41, v10
	s_waitcnt lgkmcnt(0)
	v_add_f32_e32 v8, v8, v9
	s_nop 1
	v_mov_b32_dpp v9, v8 row_ror:8 row_mask:0xf bank_mask:0xf
	v_addc_co_u32_e32 v7, vcc, 0, v11, vcc
	v_add_co_u32_e32 v10, vcc, s41, v12
	global_load_dwordx4 v[30:33], v[6:7], off
	global_load_dwordx4 v[22:25], v[6:7], off offset:1024
	v_addc_co_u32_e32 v11, vcc, 0, v13, vcc
	s_waitcnt lgkmcnt(0)
	v_add_f32_e32 v12, v8, v9
	v_mov_b32_e32 v13, v12
	s_nop 1
	v_permlane16_swap_b32_e32 v13, v12
	global_load_dwordx4 v[34:37], v[10:11], off
	global_load_dwordx4 v[26:29], v[10:11], off offset:1024
	global_load_dwordx4 v[14:17], v[6:7], off offset:2048
	s_nop 0
	global_load_dwordx4 v[6:9], v[6:7], off offset:3072
	s_waitcnt lgkmcnt(0)
	v_add_f32_e32 v66, v12, v13
	global_load_dwordx4 v[18:21], v[10:11], off offset:2048
	s_nop 0
	global_load_dwordx4 v[10:13], v[10:11], off offset:3072
	v_mov_b32_e32 v68, v66
	s_nop 1
	v_permlane32_swap_b32_e32 v68, v66
	s_waitcnt lgkmcnt(0)
; __device__ __forceinline__ unsigned cvt_pk_bf16(float lo, float hi) { unsigned r; asm volatile("v_cvt_pk_bf16_f32 %0, %1, %2" : "=v"(r) : "v"(lo), "v"(hi)); return r; }
; __device__ __forceinline__ void p6_router(Frame& F) {
;     ...
;                 float rstd = 1.f / sqrtf(wave_sum(s2) * (1.f / DM) + LN_EPS);
;                 s = 0.f;
; #pragma unroll
;                 for (int j = 0; j < 8; ++j) { v[j] = v[j] * rstd * pw[j] + pb[j]; { u32x2 xb; xb.x = cvt_pk_bf16(v[j][0], v[j][1]); xb.y = cvt_pk_bf16(v[j][2], v[j][3]); ((u32x2*)(X1 + (size_t)t * DM))[lane + 64 * j] = xb; } s += (v[j][0] + v[j][1]) + (v[j][2] + v[j][3]); }
;                 mean = wave_sum(s) * (1.f / DM); s2 = 0.f;
	v_add_f32_e32 v66, v66, v68
	v_fmamk_f32 v66, v66, 0x3a000000, v148
	v_mul_f32_e32 v68, 0x4f800000, v66
	v_cmp_gt_f32_e32 vcc, s45, v66
	s_nop 1
	v_cndmask_b32_e32 v66, v66, v68, vcc
	v_sqrt_f32_e32 v68, v66
	s_nop 0
	v_add_u32_e32 v90, -1, v68
	v_fma_f32 v100, -v90, v68, v66
	v_cmp_ge_f32_e64 s[0:1], 0, v100
	v_add_u32_e32 v100, 1, v68
	s_nop 0
	v_cndmask_b32_e64 v90, v68, v90, s[0:1]
	v_fma_f32 v68, -v100, v68, v66
	v_cmp_lt_f32_e64 s[0:1], 0, v68
	s_nop 1
	v_cndmask_b32_e64 v68, v90, v100, s[0:1]
	v_mul_f32_e32 v90, 0x37800000, v68
	v_cndmask_b32_e32 v68, v68, v90, vcc
	v_cmp_class_f32_e32 vcc, v66, v149
	s_nop 1
	v_cndmask_b32_e32 v66, v68, v66, vcc
	v_div_scale_f32 v68, s[0:1], v66, v66, 1.0
	v_rcp_f32_e32 v90, v68
	s_add_u32 s0, s42, s16
	s_addc_u32 s1, s43, s17
	s_lshl_b64 s[38:39], s[4:5], 11
	v_fma_f32 v100, -v68, v90, 1.0
	v_fmac_f32_e32 v90, v100, v90
	v_div_scale_f32 v100, vcc, 1.0, v66, 1.0
	v_mul_f32_e32 v102, v100, v90
	v_fma_f32 v108, -v68, v102, v100
	v_fmac_f32_e32 v102, v108, v90
	v_fma_f32 v68, -v68, v102, v100
	v_div_fmas_f32 v68, v68, v90, v102
	v_div_fixup_f32 v102, v68, v66, 1.0
	v_pk_mul_f32 v[106:107], v[106:107], v[102:103] op_sel_hi:[1,0]
	v_pk_mul_f32 v[108:109], v[110:111], v[102:103] op_sel_hi:[1,0]
	s_waitcnt vmcnt(14)
	v_pk_fma_f32 v[112:113], v[4:5], v[106:107], v[64:65]
	v_pk_mul_f32 v[106:107], v[122:123], v[102:103] op_sel_hi:[1,0]
	v_pk_fma_f32 v[114:115], v[2:3], v[108:109], v[62:63]
	v_pk_mul_f32 v[108:109], v[124:125], v[102:103] op_sel_hi:[1,0]
	s_waitcnt vmcnt(12)
	v_pk_fma_f32 v[110:111], v[54:55], v[106:107], v[58:59]
	v_pk_fma_f32 v[108:109], v[56:57], v[108:109], v[60:61]
	v_mov_b32_e32 v106, v110
	v_mov_b32_e32 v107, v114
	v_mov_b32_e32 v122, v111
	v_mov_b32_e32 v123, v115
	v_pk_add_f32 v[106:107], v[106:107], v[122:123]
	v_mov_b32_e32 v122, v109
	v_mov_b32_e32 v123, v113
	v_mov_b32_e32 v124, v108
	v_mov_b32_e32 v125, v112
	v_pk_add_f32 v[122:123], v[122:123], v[124:125]
	v_mov_b32_e32 v68, v117
	v_pk_add_f32 v[106:107], v[106:107], v[122:123]
	v_pk_mul_f32 v[68:69], v[68:69], v[102:103] op_sel_hi:[1,0]
	v_add_f32_e32 v66, 0, v107
	v_add_f32_e32 v123, v106, v66
	v_pk_mul_f32 v[106:107], v[104:105], v[102:103] op_sel_hi:[1,0]
	v_pk_mul_f32 v[104:105], v[120:121], v[102:103] op_sel_hi:[1,0]
	s_waitcnt vmcnt(9)
	v_pk_fma_f32 v[106:107], v[46:47], v[106:107], v[50:51]
	v_pk_fma_f32 v[104:105], v[48:49], v[104:105], v[52:53]
	v_mov_b32_e32 v120, v106
	v_mov_b32_e32 v121, v105
	v_pk_mov_b32 v[124:125], v[106:107], v[104:105] op_sel:[1,0]
	v_mov_b32_e32 v66, v101
	v_pk_add_f32 v[120:121], v[120:121], v[124:125]
	v_pk_mul_f32 v[124:125], v[70:71], v[102:103] op_sel_hi:[1,0]
	v_pk_mul_f32 v[70:71], v[72:73], v[102:103] op_sel_hi:[1,0]
	v_pk_mul_f32 v[66:67], v[66:67], v[102:103] op_sel_hi:[1,0]
	v_pk_add_f32 v[120:121], v[120:121], v[120:121] op_sel_hi:[0,1]
	s_waitcnt vmcnt(8)
	v_pk_fma_f32 v[70:71], v[40:41], v[70:71], v[44:45]
	v_pk_fma_f32 v[72:73], v[38:39], v[124:125], v[42:43]
	s_waitcnt vmcnt(5)
	v_pk_fma_f32 v[66:67], v[32:33], v[66:67], v[36:37]
	v_pk_fma_f32 v[68:69], v[30:31], v[68:69], v[34:35]
	v_add_f32_e32 v125, v72, v73
	v_add_f32_e32 v129, v71, v70
	v_mov_b32_e32 v124, v68
	v_mov_b32_e32 v128, v69
	v_mov_b32_e32 v120, v67
	v_mov_b32_e32 v122, v66
	v_pk_add_f32 v[100:101], v[124:125], v[128:129]
	v_pk_add_f32 v[116:117], v[120:121], v[122:123]
	v_mov_b32_e32 v90, v103
	v_pk_add_f32 v[100:101], v[100:101], v[116:117]
	v_pk_mul_f32 v[92:93], v[92:93], v[102:103] op_sel_hi:[1,0]
	v_pk_add_f32 v[116:117], v[100:101], v[100:101] op_sel_hi:[0,1]
	v_pk_mul_f32 v[100:101], v[98:99], v[102:103] op_sel_hi:[1,0]
	v_pk_mul_f32 v[98:99], v[118:119], v[102:103] op_sel_hi:[1,0]
	s_waitcnt vmcnt(4)
	v_pk_fma_f32 v[100:101], v[22:23], v[100:101], v[26:27]
	v_pk_fma_f32 v[98:99], v[24:25], v[98:99], v[28:29]
	v_mov_b32_e32 v118, v100
	v_mov_b32_e32 v119, v99
	v_pk_mov_b32 v[120:121], v[100:101], v[98:99] op_sel:[1,0]
	v_pk_mul_f32 v[90:91], v[90:91], v[102:103] op_sel_hi:[1,0]
	v_pk_add_f32 v[118:119], v[118:119], v[120:121]
	v_pk_mul_f32 v[120:121], v[94:95], v[102:103] op_sel_hi:[1,0]
	v_pk_mul_f32 v[94:95], v[96:97], v[102:103] op_sel_hi:[1,0]
	v_pk_add_f32 v[118:119], v[118:119], v[118:119] op_sel_hi:[0,1]
	s_waitcnt vmcnt(1)
	v_pk_fma_f32 v[94:95], v[16:17], v[94:95], v[20:21]
	v_pk_fma_f32 v[96:97], v[14:15], v[120:121], v[18:19]
	s_waitcnt vmcnt(0)
	v_pk_fma_f32 v[90:91], v[8:9], v[90:91], v[12:13]
	v_pk_fma_f32 v[92:93], v[6:7], v[92:93], v[10:11]
	v_add_f32_e32 v121, v96, v97
	v_add_f32_e32 v123, v95, v94
	v_mov_b32_e32 v120, v92
	v_mov_b32_e32 v122, v93
	v_mov_b32_e32 v118, v91
	v_mov_b32_e32 v116, v90
	v_pk_add_f32 v[102:103], v[120:121], v[122:123]
	v_pk_add_f32 v[116:117], v[118:119], v[116:117]
	v_cvt_pk_bf16_f32 v126, v114, v115
	v_cvt_pk_bf16_f32 v127, v112, v113
	global_store_dwordx2 v146, v[126:127], s[0:1]
	v_pk_add_f32 v[102:103], v[102:103], v[116:117]
	s_nop 0
	v_add_f32_e32 v103, v102, v103
	s_nop 1
	v_mov_b32_dpp v116, v103 quad_perm:[1,0,3,2] row_mask:0xf bank_mask:0xf
	v_cvt_pk_bf16_f32 v102, v110, v111
	s_waitcnt lgkmcnt(0)
	v_add_f32_e32 v116, v103, v116
	s_nop 1
	v_mov_b32_dpp v117, v116 quad_perm:[2,3,0,1] row_mask:0xf bank_mask:0xf
	v_cvt_pk_bf16_f32 v103, v108, v109
	global_store_dwordx2 v146, v[102:103], s[0:1] offset:512
	v_cvt_pk_bf16_f32 v102, v106, v107
	v_cvt_pk_bf16_f32 v103, v104, v105
	s_waitcnt lgkmcnt(0)
	v_add_f32_e32 v116, v116, v117
	s_nop 1
	v_mov_b32_dpp v117, v116 row_shl:4 row_mask:0xf bank_mask:0x5
	s_nop 1
	v_mov_b32_dpp v117, v116 row_shr:4 row_mask:0xf bank_mask:0xa
	global_store_dwordx2 v146, v[102:103], s[0:1] offset:1024
	v_cvt_pk_bf16_f32 v102, v72, v73
	v_cvt_pk_bf16_f32 v103, v70, v71
	global_store_dwordx2 v146, v[102:103], s[0:1] offset:1536
	s_waitcnt lgkmcnt(0)
; __device__ __forceinline__ void p6_router(Frame& F) {
;     ...
;                 mean = wave_sum(s) * (1.f / DM); s2 = 0.f;
; #pragma unroll
;                 for (int j = 0; j < 8; ++j) { v[j] = v[j] - mean; s2 += (v[j][0] * v[j][0] + v[j][1] * v[j][1]) + (v[j][2] * v[j][2] + v[j][3] * v[j][3]); }
;                 rstd = 1.f / sqrtf(wave_sum(s2) * (1.f / DM) + LN_EPS);
;                 int loq = lane; asm volatile("" : "+v"(loq));
; #pragma unroll
;                 for (int j = 0; j < 8; ++j) { const f32x4 sh = ((const f32x4*)(mod + (size_t)b * 12288 + 6144))[loq + 64 * j], sc = ((const f32x4*)(mod + (size_t)b * 12288 + 8192))[loq + 64 * j];
	v_add_f32_e32 v116, v116, v117
	s_nop 1
	v_mov_b32_dpp v117, v116 row_ror:8 row_mask:0xf bank_mask:0xf
	v_cvt_pk_bf16_f32 v102, v68, v69
	v_cvt_pk_bf16_f32 v103, v66, v67
	global_store_dwordx2 v146, v[102:103], s[0:1] offset:2048
	v_cvt_pk_bf16_f32 v102, v100, v101
	s_waitcnt lgkmcnt(0)
	v_add_f32_e32 v116, v116, v117
	v_mov_b32_e32 v117, v116
	s_nop 1
	v_permlane16_swap_b32_e32 v117, v116
	v_cvt_pk_bf16_f32 v103, v98, v99
	global_store_dwordx2 v146, v[102:103], s[0:1] offset:2560
	v_cvt_pk_bf16_f32 v102, v96, v97
	v_cvt_pk_bf16_f32 v103, v94, v95
	s_waitcnt lgkmcnt(0)
	v_add_f32_e32 v116, v116, v117
	v_mov_b32_e32 v117, v116
	s_nop 1
	v_permlane32_swap_b32_e32 v117, v116
	global_store_dwordx2 v146, v[102:103], s[0:1] offset:3072
	v_cvt_pk_bf16_f32 v102, v92, v93
	v_cvt_pk_bf16_f32 v103, v90, v91
	global_store_dwordx2 v146, v[102:103], s[0:1] offset:3584
	s_waitcnt lgkmcnt(0)
	v_add_f32_e32 v122, v116, v117
	v_fmamk_f32 v115, v122, 0xba000000, v115
	v_fmamk_f32 v111, v122, 0xba000000, v111
	v_fmamk_f32 v113, v122, 0xba000000, v113
	v_fmac_f32_e32 v114, 0xba000000, v122
	v_fmamk_f32 v109, v122, 0xba000000, v109
	v_fmac_f32_e32 v110, 0xba000000, v122
	v_mov_b32_e32 v116, v115
	v_mov_b32_e32 v117, v111
	v_fmac_f32_e32 v112, 0xba000000, v122
	v_fmac_f32_e32 v108, 0xba000000, v122
	v_mov_b32_e32 v102, v114
	v_mov_b32_e32 v103, v110
	v_pk_mul_f32 v[116:117], v[116:117], v[116:117]
	v_mov_b32_e32 v118, v113
	v_mov_b32_e32 v119, v109
	v_pk_fma_f32 v[102:103], v[102:103], v[102:103], v[116:117]
	v_mov_b32_e32 v116, v112
	v_mov_b32_e32 v117, v108
	v_pk_mul_f32 v[118:119], v[118:119], v[118:119]
	v_fmamk_f32 v107, v122, 0xba000000, v107
	v_pk_fma_f32 v[116:117], v[116:117], v[116:117], v[118:119]
	v_fmac_f32_e32 v106, 0xba000000, v122
	v_pk_add_f32 v[102:103], v[102:103], v[116:117]
	v_fmamk_f32 v105, v122, 0xba000000, v105
	v_fmac_f32_e32 v104, 0xba000000, v122
	v_pk_add_f32 v[102:103], v[102:103], v[102:103] op_sel_hi:[0,1]
	v_pk_mul_f32 v[116:117], v[104:105], v[104:105]
	v_pk_mul_f32 v[118:119], v[106:107], v[106:107]
	v_fmac_f32_e32 v72, 0xba000000, v122
	v_pk_mov_b32 v[120:121], v[118:119], v[116:117] op_sel:[1,0]
	v_mov_b32_e32 v119, v117
	v_fmamk_f32 v73, v122, 0xba000000, v73
	v_fmac_f32_e32 v70, 0xba000000, v122
	v_mul_f32_e32 v102, v72, v72
	v_pk_add_f32 v[116:117], v[120:121], v[118:119]
	v_fmamk_f32 v71, v122, 0xba000000, v71
	v_pk_fma_f32 v[118:119], v[72:73], v[72:73], v[102:103] op_sel_hi:[1,1,0]
	v_mul_f32_e32 v102, v70, v70
	v_pk_add_f32 v[116:117], v[116:117], v[116:117] op_sel_hi:[0,1]
	v_pk_fma_f32 v[120:121], v[70:71], v[70:71], v[102:103] op_sel_hi:[1,1,0]
	v_fmamk_f32 v67, v122, 0xba000000, v67
	v_fmac_f32_e32 v66, 0xba000000, v122
	v_fmamk_f32 v69, v122, 0xba000000, v69
	v_fmac_f32_e32 v68, 0xba000000, v122
	v_mul_f32_e32 v118, v68, v68
	v_mul_f32_e32 v120, v69, v69
	v_mul_f32_e32 v116, v66, v66
	v_mul_f32_e32 v102, v67, v67
	v_pk_add_f32 v[118:119], v[118:119], v[120:121]
	v_pk_add_f32 v[102:103], v[116:117], v[102:103]
	v_fmamk_f32 v101, v122, 0xba000000, v101
	v_fmac_f32_e32 v100, 0xba000000, v122
	v_fmamk_f32 v99, v122, 0xba000000, v99
	v_fmac_f32_e32 v98, 0xba000000, v122
	v_pk_add_f32 v[102:103], v[118:119], v[102:103]
	v_pk_mul_f32 v[116:117], v[98:99], v[98:99]
	v_pk_mul_f32 v[118:119], v[100:101], v[100:101]
	s_mul_hi_i32 s0, s20, 0xc000
	s_mul_i32 s20, s20, 0xc000
	v_pk_mov_b32 v[120:121], v[118:119], v[116:117] op_sel:[1,0]
	v_mov_b32_e32 v119, v117
	s_add_u32 s1, s82, s20
	v_pk_add_f32 v[116:117], v[120:121], v[118:119]
	s_addc_u32 s0, s83, s0
	v_pk_add_f32 v[128:129], v[116:117], v[116:117] op_sel_hi:[0,1]
	v_mov_b32_e32 v116, v170
	s_add_u32 s16, s1, 0x106000
	s_addc_u32 s17, s0, 0
	v_ashrrev_i32_e32 v117, 31, v116
	v_lshlrev_b64 v[118:119], 4, v[116:117]
	s_add_u32 s20, s1, 0x108000
	v_lshl_add_u64 v[116:117], s[16:17], 0, v[118:119]
	s_addc_u32 s21, s0, 0
	v_fmamk_f32 v97, v122, 0xba000000, v97
	v_fmac_f32_e32 v96, 0xba000000, v122
	v_fmamk_f32 v95, v122, 0xba000000, v95
	v_fmac_f32_e32 v94, 0xba000000, v122
	v_fmamk_f32 v91, v122, 0xba000000, v91
	v_fmac_f32_e32 v90, 0xba000000, v122
	v_fmamk_f32 v93, v122, 0xba000000, v93
	v_fmac_f32_e32 v92, 0xba000000, v122
	v_lshl_add_u64 v[118:119], s[20:21], 0, v[118:119]
	global_load_dwordx4 v[120:123], v[116:117], off
	global_load_dwordx4 v[124:127], v[118:119], off
	v_pk_add_f32 v[102:103], v[102:103], v[102:103] op_sel_hi:[0,1]
	v_mul_f32_e32 v102, v96, v96
	v_pk_fma_f32 v[130:131], v[96:97], v[96:97], v[102:103] op_sel_hi:[1,1,0]
	v_mul_f32_e32 v102, v94, v94
	v_pk_fma_f32 v[132:133], v[94:95], v[94:95], v[102:103] op_sel_hi:[1,1,0]
	v_mul_f32_e32 v130, v92, v92
	v_mul_f32_e32 v132, v93, v93
	v_mul_f32_e32 v128, v90, v90
	v_mul_f32_e32 v102, v91, v91
	v_pk_add_f32 v[130:131], v[130:131], v[132:133]
	v_pk_add_f32 v[102:103], v[128:129], v[102:103]
	s_lshl_b32 s5, s46, 5
	v_pk_add_f32 v[102:103], v[130:131], v[102:103]
	v_and_b32_e32 v133, 0xffff0000, v85
	v_add_f32_e32 v102, v102, v103
	s_nop 1
	v_mov_b32_dpp v103, v102 quad_perm:[1,0,3,2] row_mask:0xf bank_mask:0xf
	v_and_b32_e32 v132, 0xffff0000, v84
	s_waitcnt lgkmcnt(0)
	v_add_f32_e32 v102, v102, v103
	s_nop 1
	v_mov_b32_dpp v103, v102 quad_perm:[2,3,0,1] row_mask:0xf bank_mask:0xf
	s_waitcnt lgkmcnt(0)
	v_add_f32_e32 v102, v102, v103
	s_nop 1
	v_mov_b32_dpp v103, v102 row_shl:4 row_mask:0xf bank_mask:0x5
	s_nop 1
	v_mov_b32_dpp v103, v102 row_shr:4 row_mask:0xf bank_mask:0xa
	s_waitcnt lgkmcnt(0)
	v_add_f32_e32 v102, v102, v103
	s_nop 1
	v_mov_b32_dpp v103, v102 row_ror:8 row_mask:0xf bank_mask:0xf
	s_waitcnt lgkmcnt(0)
	v_add_f32_e32 v102, v102, v103
	v_mov_b32_e32 v103, v102
	s_nop 1
	v_permlane16_swap_b32_e32 v103, v102
	s_waitcnt lgkmcnt(0)
; #define LAS __attribute__((address_space(3)))
; __device__ __forceinline__ unsigned cvt_pk_bf16(float lo, float hi) { unsigned r; asm volatile("v_cvt_pk_bf16_f32 %0, %1, %2" : "=v"(r) : "v"(lo), "v"(hi)); return r; }
; __device__ __forceinline__ unsigned pk4_fp8(float a, float b, float c, float d) { int w = 0; w = __builtin_amdgcn_cvt_pk_fp8_f32(a, b, w, false); w = __builtin_amdgcn_cvt_pk_fp8_f32(c, d, w, true); return (unsigned)w; }
; __device__ __forceinline__ float bf_lo(unsigned w) { return __uint_as_float(w << 16); }
; __device__ __forceinline__ float bf_hi(unsigned w) { return __uint_as_float(w & 0xffff0000u); }
; __device__ __forceinline__ void p6_router(Frame& F) {
;     ...
;                 rstd = 1.f / sqrtf(wave_sum(s2) * (1.f / DM) + LN_EPS);
;                 int loq = lane; asm volatile("" : "+v"(loq));
; #pragma unroll
;                 for (int j = 0; j < 8; ++j) { const f32x4 sh = ((const f32x4*)(mod + (size_t)b * 12288 + 6144))[loq + 64 * j], sc = ((const f32x4*)(mod + (size_t)b * 12288 + 8192))[loq + 64 * j];
;                     const f32x4 y = v[j] * rstd * (sc + 1.0f) + sh;
;                     u32x2 wh; wh.x = cvt_pk_bf16(y[0], y[1]); wh.y = cvt_pk_bf16(y[2], y[3]);
;                     const f32x4 yl = {y[0] - bf_lo(wh.x), y[1] - bf_hi(wh.x), y[2] - bf_lo(wh.y), y[3] - bf_hi(wh.y)};
;                     u32x2 wl; wl.x = cvt_pk_bf16(yl[0], yl[1]); wl.y = cvt_pk_bf16(yl[2], yl[3]);
;                     { const int r = 2 * wave + q; LAS unsigned char* rowp = F.lds + r * 4096 + ((((lane >> 1) + 32 * j) ^ r) << 4) + (lane & 1) * 8;
;                       *(LAS u32x2*)rowp = wh; *(LAS u32x2*)(rowp + 65536) = wl; }
;                     U2F[(size_t)t * (DM / 4) + lane + 64 * j] = pk4_fp8(y[0], y[1], y[2], y[3]); }
	v_add_f32_e32 v102, v102, v103
	v_mov_b32_e32 v103, v102
	s_nop 1
	v_permlane32_swap_b32_e32 v103, v102
	s_waitcnt lgkmcnt(0)
	v_add_f32_e32 v102, v102, v103
	v_fmamk_f32 v102, v102, 0x3a000000, v148
	v_mul_f32_e32 v103, 0x4f800000, v102
	v_cmp_gt_f32_e32 vcc, s45, v102
	s_waitcnt vmcnt(0)
	v_pk_add_f32 v[124:125], v[124:125], 1.0 op_sel_hi:[1,0]
	v_cndmask_b32_e32 v102, v102, v103, vcc
	v_sqrt_f32_e32 v103, v102
	v_pk_add_f32 v[126:127], v[126:127], 1.0 op_sel_hi:[1,0]
	v_add_u32_e32 v128, -1, v103
	v_fma_f32 v129, -v128, v103, v102
	v_cmp_ge_f32_e64 s[0:1], 0, v129
	v_add_u32_e32 v129, 1, v103
	s_nop 0
	v_cndmask_b32_e64 v128, v103, v128, s[0:1]
	v_fma_f32 v103, -v129, v103, v102
	v_cmp_lt_f32_e64 s[0:1], 0, v103
	s_nop 1
	v_cndmask_b32_e64 v103, v128, v129, s[0:1]
	v_mul_f32_e32 v128, 0x37800000, v103
	v_cndmask_b32_e32 v103, v103, v128, vcc
	v_cmp_class_f32_e32 vcc, v102, v149
	s_nop 1
	v_cndmask_b32_e32 v102, v103, v102, vcc
	v_div_scale_f32 v103, s[0:1], v102, v102, 1.0
	v_rcp_f32_e32 v128, v103
	s_lshl_b32 s0, s46, 13
	s_add_i32 s0, s0, 0
	s_add_u32 s38, s40, s38
	v_fma_f32 v129, -v103, v128, 1.0
	v_fmac_f32_e32 v128, v129, v128
	v_div_scale_f32 v129, vcc, 1.0, v102, 1.0
	v_mul_f32_e32 v130, v129, v128
	v_fma_f32 v131, -v103, v130, v129
	v_fmac_f32_e32 v130, v131, v128
	v_fma_f32 v103, -v103, v130, v129
	v_div_fmas_f32 v103, v103, v128, v130
	v_div_fixup_f32 v102, v103, v102, 1.0
	v_pk_mul_f32 v[114:115], v[114:115], v[102:103] op_sel_hi:[1,0]
	v_pk_mul_f32 v[112:113], v[112:113], v[102:103] op_sel_hi:[1,0]
	v_pk_fma_f32 v[114:115], v[124:125], v[114:115], v[120:121]
	v_pk_fma_f32 v[112:113], v[126:127], v[112:113], v[122:123]
	v_cvt_pk_bf16_f32 v124, v114, v115
	s_addc_u32 s39, s44, s39
	v_lshlrev_b32_e32 v103, 16, v124
	v_sub_f32_e32 v103, v114, v103
	v_and_b32_e32 v120, 0xffff0000, v124
	v_cvt_pk_bf16_f32 v125, v112, v113
	v_sub_f32_e32 v120, v115, v120
	v_cvt_pk_bf16_f32 v126, v103, v120
	v_mov_b32_e32 v103, 0
	v_cvt_pk_fp8_f32 v103, v114, v115
	v_lshlrev_b32_e32 v121, 16, v125
	v_and_b32_e32 v122, 0xffff0000, v125
	v_sub_f32_e32 v121, v112, v121
	v_cvt_pk_fp8_f32 v103, v112, v113 op_sel:[0,0,1]
	v_sub_f32_e32 v122, v113, v122
	v_cvt_pk_bf16_f32 v127, v121, v122
	v_and_b32_e32 v130, 0x1f0, v146
	global_store_dword v150, v103, s[38:39]
	global_load_dwordx4 v[112:115], v[118:119], off offset:1024
	global_load_dwordx4 v[120:123], v[116:117], off offset:1024
	v_mov_b32_e32 v103, 0x1f0
	v_bitop3_b32 v128, s5, v146, v103 bitop3:0x78
	v_and_b32_e32 v103, 8, v146
	v_pk_mul_f32 v[110:111], v[110:111], v[102:103] op_sel_hi:[1,0]
	v_pk_mul_f32 v[108:109], v[108:109], v[102:103] op_sel_hi:[1,0]
	v_add3_u32 v159, s0, v128, v103
	v_add_u32_e32 v160, 0x10000, v159
	ds_write_b64 v159, v[124:125]
	ds_write_b64 v160, v[126:127]
	v_pk_mul_f32 v[106:107], v[106:107], v[102:103] op_sel_hi:[1,0]
	v_pk_mul_f32 v[104:105], v[104:105], v[102:103] op_sel_hi:[1,0]
	v_mov_b32_e32 v124, 0x200
	v_bitop3_b32 v124, v130, s5, v124 bitop3:0x36
	v_add3_u32 v161, s0, v124, v103
	v_add_u32_e32 v162, 0x10000, v161
	v_pk_mul_f32 v[72:73], v[72:73], v[102:103] op_sel_hi:[1,0]
	v_pk_mul_f32 v[70:71], v[70:71], v[102:103] op_sel_hi:[1,0]
	v_pk_mul_f32 v[68:69], v[68:69], v[102:103] op_sel_hi:[1,0]
	v_pk_mul_f32 v[66:67], v[66:67], v[102:103] op_sel_hi:[1,0]
	v_and_b32_e32 v125, 0xffff0000, v88
	v_and_b32_e32 v124, 0xffff0000, v86
	v_pk_mul_f32 v[100:101], v[100:101], v[102:103] op_sel_hi:[1,0]
	v_pk_mul_f32 v[98:99], v[98:99], v[102:103] op_sel_hi:[1,0]
	v_pk_mul_f32 v[96:97], v[96:97], v[102:103] op_sel_hi:[1,0]
	v_pk_mul_f32 v[94:95], v[94:95], v[102:103] op_sel_hi:[1,0]
	v_pk_mul_f32 v[92:93], v[92:93], v[102:103] op_sel_hi:[1,0]
	v_pk_mul_f32 v[90:91], v[90:91], v[102:103] op_sel_hi:[1,0]
	s_waitcnt vmcnt(1)
	v_pk_add_f32 v[114:115], v[114:115], 1.0 op_sel_hi:[1,0]
	v_pk_add_f32 v[112:113], v[112:113], 1.0 op_sel_hi:[1,0]
	s_waitcnt vmcnt(0)
	v_pk_fma_f32 v[108:109], v[114:115], v[108:109], v[122:123]
	v_pk_fma_f32 v[110:111], v[112:113], v[110:111], v[120:121]
	v_mov_b32_e32 v114, 0
	v_cvt_pk_fp8_f32 v114, v110, v111
	v_cvt_pk_bf16_f32 v120, v110, v111
	v_cvt_pk_bf16_f32 v121, v108, v109
	v_cvt_pk_fp8_f32 v114, v108, v109 op_sel:[0,0,1]
	v_lshlrev_b32_e32 v112, 16, v120
	v_and_b32_e32 v113, 0xffff0000, v120
	v_sub_f32_e32 v112, v110, v112
	v_sub_f32_e32 v113, v111, v113
	v_lshlrev_b32_e32 v110, 16, v121
	v_and_b32_e32 v111, 0xffff0000, v121
	v_sub_f32_e32 v110, v108, v110
	v_sub_f32_e32 v108, v109, v111
	v_cvt_pk_bf16_f32 v122, v112, v113
	v_cvt_pk_bf16_f32 v123, v110, v108
	global_store_dword v150, v114, s[38:39] offset:256
	global_load_dwordx4 v[108:111], v[118:119], off offset:2048
	s_nop 0
	global_load_dwordx4 v[112:115], v[116:117], off offset:2048
	ds_write_b64 v161, v[120:121]
	ds_write_b64 v162, v[122:123]
	v_mov_b32_e32 v120, 0x400
	v_bitop3_b32 v120, v130, s5, v120 bitop3:0x36
	v_add3_u32 v165, s0, v120, v103
	v_add_u32_e32 v166, 0x10000, v165
	v_lshlrev_b32_e32 v123, 16, v88
	v_lshlrev_b32_e32 v122, 16, v86
	v_and_b32_e32 v121, 0xffff0000, v89
	v_and_b32_e32 v120, 0xffff0000, v87
	v_pk_add_f32 v[136:137], v[122:123], v[124:125]
	v_mov_b32_e32 v88, 0
	s_waitcnt vmcnt(1)
	v_pk_add_f32 v[110:111], v[110:111], 1.0 op_sel_hi:[1,0]
	v_pk_add_f32 v[108:109], v[108:109], 1.0 op_sel_hi:[1,0]
	s_waitcnt vmcnt(0)
; #define LAS __attribute__((address_space(3)))
; __device__ __forceinline__ unsigned cvt_pk_bf16(float lo, float hi) { unsigned r; asm volatile("v_cvt_pk_bf16_f32 %0, %1, %2" : "=v"(r) : "v"(lo), "v"(hi)); return r; }
; __device__ __forceinline__ unsigned pk4_fp8(float a, float b, float c, float d) { int w = 0; w = __builtin_amdgcn_cvt_pk_fp8_f32(a, b, w, false); w = __builtin_amdgcn_cvt_pk_fp8_f32(c, d, w, true); return (unsigned)w; }
; __device__ __forceinline__ float bf_lo(unsigned w) { return __uint_as_float(w << 16); }
; __device__ __forceinline__ float bf_hi(unsigned w) { return __uint_as_float(w & 0xffff0000u); }
; __device__ __forceinline__ void p6_router(Frame& F) {
;     ...
;                 const int t = ta + q; f32x4 v[8]; float s = 0.f;
; #pragma unroll
;                 for (int j = 0; j < 8; ++j) { const u32x2 zb = zr[q][j]; v[j] = (f32x4){bf_lo(zb.x), bf_hi(zb.x), bf_lo(zb.y), bf_hi(zb.y)}; s += (v[j][0] + v[j][1]) + (v[j][2] + v[j][3]); }
;                 float mean = wave_sum(s) * (1.f / DM), s2 = 0.f;
;     ...
; #pragma unroll
;                 for (int j = 0; j < 8; ++j) { const f32x4 sh = ((const f32x4*)(mod + (size_t)b * 12288 + 6144))[loq + 64 * j], sc = ((const f32x4*)(mod + (size_t)b * 12288 + 8192))[loq + 64 * j];
;                     const f32x4 y = v[j] * rstd * (sc + 1.0f) + sh;
;                     u32x2 wh; wh.x = cvt_pk_bf16(y[0], y[1]); wh.y = cvt_pk_bf16(y[2], y[3]);
;                     const f32x4 yl = {y[0] - bf_lo(wh.x), y[1] - bf_hi(wh.x), y[2] - bf_lo(wh.y), y[3] - bf_hi(wh.y)};
;                     u32x2 wl; wl.x = cvt_pk_bf16(yl[0], yl[1]); wl.y = cvt_pk_bf16(yl[2], yl[3]);
;                     { const int r = 2 * wave + q; LAS unsigned char* rowp = F.lds + r * 4096 + ((((lane >> 1) + 32 * j) ^ r) << 4) + (lane & 1) * 8;
;                       *(LAS u32x2*)rowp = wh; *(LAS u32x2*)(rowp + 65536) = wl; }
;                     U2F[(size_t)t * (DM / 4) + lane + 64 * j] = pk4_fp8(y[0], y[1], y[2], y[3]); }
	v_pk_fma_f32 v[104:105], v[110:111], v[104:105], v[114:115]
	v_pk_fma_f32 v[106:107], v[108:109], v[106:107], v[112:113]
	v_mov_b32_e32 v110, 0
	v_cvt_pk_fp8_f32 v110, v106, v107
	v_cvt_pk_bf16_f32 v112, v106, v107
	v_cvt_pk_bf16_f32 v113, v104, v105
	v_cvt_pk_fp8_f32 v110, v104, v105 op_sel:[0,0,1]
	v_lshlrev_b32_e32 v108, 16, v112
	v_and_b32_e32 v109, 0xffff0000, v112
	v_sub_f32_e32 v108, v106, v108
	v_sub_f32_e32 v109, v107, v109
	v_lshlrev_b32_e32 v106, 16, v113
	v_and_b32_e32 v107, 0xffff0000, v113
	v_sub_f32_e32 v106, v104, v106
	v_sub_f32_e32 v104, v105, v107
	v_cvt_pk_bf16_f32 v114, v108, v109
	v_cvt_pk_bf16_f32 v115, v106, v104
	global_store_dword v150, v110, s[38:39] offset:512
	global_load_dwordx4 v[104:107], v[118:119], off offset:3072
	s_nop 0
	global_load_dwordx4 v[108:111], v[116:117], off offset:3072
	ds_write_b64 v165, v[112:113]
	ds_write_b64 v166, v[114:115]
	s_waitcnt vmcnt(1)
	v_pk_add_f32 v[106:107], v[106:107], 1.0 op_sel_hi:[1,0]
	v_pk_add_f32 v[104:105], v[104:105], 1.0 op_sel_hi:[1,0]
	s_waitcnt vmcnt(0)
	v_pk_fma_f32 v[70:71], v[70:71], v[106:107], v[110:111]
	v_pk_fma_f32 v[72:73], v[72:73], v[104:105], v[108:109]
	v_mov_b32_e32 v106, 0
	v_cvt_pk_fp8_f32 v106, v72, v73
	v_cvt_pk_bf16_f32 v112, v72, v73
	v_cvt_pk_bf16_f32 v113, v70, v71
	v_cvt_pk_fp8_f32 v106, v70, v71 op_sel:[0,0,1]
	v_lshlrev_b32_e32 v104, 16, v112
	v_sub_f32_e32 v104, v72, v104
	v_and_b32_e32 v105, 0xffff0000, v112
	v_sub_f32_e32 v105, v73, v105
	v_cvt_pk_bf16_f32 v114, v104, v105
	v_add_co_u32_e32 v104, vcc, s41, v118
	v_lshlrev_b32_e32 v72, 16, v113
	v_and_b32_e32 v73, 0xffff0000, v113
	v_addc_co_u32_e32 v105, vcc, 0, v119, vcc
	v_sub_f32_e32 v72, v70, v72
	v_sub_f32_e32 v70, v71, v73
	v_cvt_pk_bf16_f32 v115, v72, v70
	global_store_dword v150, v106, s[38:39] offset:768
	v_add_co_u32_e32 v106, vcc, s41, v116
	global_load_dwordx4 v[70:73], v[104:105], off
	s_nop 0
	v_addc_co_u32_e32 v107, vcc, 0, v117, vcc
	global_load_dwordx4 v[108:111], v[106:107], off
	v_mov_b32_e32 v117, 0
	v_mov_b32_e32 v116, 0x600
	v_bitop3_b32 v116, v130, s5, v116 bitop3:0x36
	v_add3_u32 v155, s0, v116, v103
	v_add_u32_e32 v156, 0x10000, v155
	ds_write_b64 v155, v[112:113]
	ds_write_b64 v156, v[114:115]
	v_lshlrev_b32_e32 v119, 16, v89
	v_lshlrev_b32_e32 v118, 16, v87
	v_lshlrev_b32_e32 v116, 16, v84
	v_lshlrev_b32_e32 v112, 16, v82
	v_and_b32_e32 v113, 0xffff0000, v82
	v_lshlrev_b32_e32 v114, 16, v83
	v_and_b32_e32 v115, 0xffff0000, v83
	v_and_b32_e32 v89, 0xffff0000, v80
	v_and_b32_e32 v87, 0xffff0000, v81
	v_lshlrev_b32_e32 v82, 16, v77
	v_and_b32_e32 v83, 0xffff0000, v77
	v_pk_add_f32 v[138:139], v[118:119], v[120:121]
	v_lshlrev_b32_e32 v84, 16, v78
	v_and_b32_e32 v77, 0xffff0000, v74
	v_pk_add_f32 v[136:137], v[136:137], v[138:139]
	v_add_f32_e32 v86, v114, v115
	s_waitcnt vmcnt(1)
	v_pk_add_f32 v[70:71], v[70:71], 1.0 op_sel_hi:[1,0]
	v_pk_add_f32 v[72:73], v[72:73], 1.0 op_sel_hi:[1,0]
	s_waitcnt vmcnt(0)
	v_pk_fma_f32 v[68:69], v[68:69], v[70:71], v[108:109]
	s_nop 0
	v_cvt_pk_fp8_f32 v117, v68, v69
	v_pk_fma_f32 v[66:67], v[66:67], v[72:73], v[110:111]
	v_cvt_pk_bf16_f32 v126, v68, v69
	v_lshlrev_b32_e32 v111, 16, v80
	v_cvt_pk_fp8_f32 v117, v66, v67 op_sel:[0,0,1]
	v_cvt_pk_bf16_f32 v127, v66, v67
	v_lshlrev_b32_e32 v70, 16, v126
	v_and_b32_e32 v71, 0xffff0000, v126
	v_lshlrev_b32_e32 v72, 16, v127
	v_and_b32_e32 v73, 0xffff0000, v127
	v_sub_f32_e32 v68, v68, v70
	v_sub_f32_e32 v69, v69, v71
	v_sub_f32_e32 v70, v66, v72
	v_sub_f32_e32 v66, v67, v73
	v_cvt_pk_bf16_f32 v128, v68, v69
	v_cvt_pk_bf16_f32 v129, v70, v66
	global_store_dword v150, v117, s[38:39] offset:1024
	global_load_dwordx4 v[70:73], v[104:105], off offset:1024
	global_load_dwordx4 v[66:69], v[106:107], off offset:1024
	v_lshlrev_b32_e32 v117, 16, v85
	v_lshlrev_b32_e32 v109, 16, v81
	v_lshlrev_b32_e32 v80, 16, v76
	v_and_b32_e32 v81, 0xffff0000, v76
	v_lshlrev_b32_e32 v85, 16, v79
	v_lshlrev_b32_e32 v76, 16, v74
	v_lshlrev_b32_e32 v79, 16, v75
	v_and_b32_e32 v75, 0xffff0000, v75
	v_pk_add_f32 v[140:141], v[116:117], v[132:133]
	v_add_f32_e32 v78, v80, v81
	v_add_f32_e32 v74, v82, v83
	v_pk_add_f32 v[138:139], v[140:141], v[140:141] op_sel:[0,1] op_sel_hi:[1,0]
	v_pk_add_f32 v[168:169], v[78:79], v[74:75]
	v_add_f32_e32 v74, 0, v136
	v_add_f32_e32 v108, v112, v113
	v_mov_b32_e32 v139, v89
	v_add_f32_e32 v110, v74, v137
	v_pk_add_f32 v[140:141], v[108:109], v[86:87]
	v_pk_add_f32 v[136:137], v[110:111], v[138:139]
	v_pk_add_f32 v[152:153], v[84:85], v[134:135]
	v_pk_add_f32 v[136:137], v[136:137], v[140:141]
	v_pk_add_f32 v[152:153], v[152:153], v[152:153] op_sel:[0,1] op_sel_hi:[1,0]
	v_pk_add_f32 v[136:137], v[136:137], v[136:137] op_sel:[0,1] op_sel_hi:[1,0]
	v_mov_b32_e32 v153, v77
	v_mov_b32_e32 v137, v76
	v_pk_add_f32 v[136:137], v[136:137], v[152:153]
	v_mov_b32_e32 v86, 0x800
	v_pk_add_f32 v[136:137], v[136:137], v[168:169]
	v_bitop3_b32 v86, v130, s5, v86 bitop3:0x36
	v_add_f32_e32 v74, v136, v137
	s_nop 1
	v_mov_b32_dpp v78, v74 quad_perm:[1,0,3,2] row_mask:0xf bank_mask:0xf
	v_add3_u32 v169, s0, v86, v103
	v_add_u32_e32 v171, 0x10000, v169
	ds_write_b64 v169, v[126:127]
	ds_write_b64 v171, v[128:129]
	s_waitcnt lgkmcnt(2)
	v_add_f32_e32 v74, v74, v78
	s_nop 1
	v_mov_b32_dpp v78, v74 quad_perm:[2,3,0,1] row_mask:0xf bank_mask:0xf
	s_waitcnt lgkmcnt(0)
	v_add_f32_e32 v74, v74, v78
	s_nop 1
	v_mov_b32_dpp v78, v74 row_shl:4 row_mask:0xf bank_mask:0x5
	s_nop 1
	v_mov_b32_dpp v78, v74 row_shr:4 row_mask:0xf bank_mask:0xa
	s_waitcnt lgkmcnt(0)
	v_add_f32_e32 v74, v74, v78
	s_waitcnt vmcnt(1)
	v_pk_add_f32 v[70:71], v[70:71], 1.0 op_sel_hi:[1,0]
	s_waitcnt vmcnt(0)
; #define LAS __attribute__((address_space(3)))
; __device__ __forceinline__ unsigned cvt_pk_bf16(float lo, float hi) { unsigned r; asm volatile("v_cvt_pk_bf16_f32 %0, %1, %2" : "=v"(r) : "v"(lo), "v"(hi)); return r; }
; __device__ __forceinline__ unsigned pk4_fp8(float a, float b, float c, float d) { int w = 0; w = __builtin_amdgcn_cvt_pk_fp8_f32(a, b, w, false); w = __builtin_amdgcn_cvt_pk_fp8_f32(c, d, w, true); return (unsigned)w; }
; __device__ __forceinline__ float bf_lo(unsigned w) { return __uint_as_float(w << 16); }
; __device__ __forceinline__ float bf_hi(unsigned w) { return __uint_as_float(w & 0xffff0000u); }
; __device__ __forceinline__ void p6_router(Frame& F) {
;     ...
;                 float mean = wave_sum(s) * (1.f / DM), s2 = 0.f;
; #pragma unroll
;                 for (int j = 0; j < 8; ++j) { v[j] = v[j] - mean; s2 += (v[j][0] * v[j][0] + v[j][1] * v[j][1]) + (v[j][2] * v[j][2] + v[j][3] * v[j][3]); }
;                 float rstd = 1.f / sqrtf(wave_sum(s2) * (1.f / DM) + LN_EPS);
;     ...
; #pragma unroll
;                 for (int j = 0; j < 8; ++j) { const f32x4 sh = ((const f32x4*)(mod + (size_t)b * 12288 + 6144))[loq + 64 * j], sc = ((const f32x4*)(mod + (size_t)b * 12288 + 8192))[loq + 64 * j];
;                     const f32x4 y = v[j] * rstd * (sc + 1.0f) + sh;
;                     u32x2 wh; wh.x = cvt_pk_bf16(y[0], y[1]); wh.y = cvt_pk_bf16(y[2], y[3]);
;                     const f32x4 yl = {y[0] - bf_lo(wh.x), y[1] - bf_hi(wh.x), y[2] - bf_lo(wh.y), y[3] - bf_hi(wh.y)};
;                     u32x2 wl; wl.x = cvt_pk_bf16(yl[0], yl[1]); wl.y = cvt_pk_bf16(yl[2], yl[3]);
;                     { const int r = 2 * wave + q; LAS unsigned char* rowp = F.lds + r * 4096 + ((((lane >> 1) + 32 * j) ^ r) << 4) + (lane & 1) * 8;
;                       *(LAS u32x2*)rowp = wh; *(LAS u32x2*)(rowp + 65536) = wl; }
;                     U2F[(size_t)t * (DM / 4) + lane + 64 * j] = pk4_fp8(y[0], y[1], y[2], y[3]); }
	v_pk_fma_f32 v[66:67], v[100:101], v[70:71], v[66:67]
	v_pk_add_f32 v[72:73], v[72:73], 1.0 op_sel_hi:[1,0]
	v_cvt_pk_fp8_f32 v88, v66, v67
	v_pk_fma_f32 v[68:69], v[98:99], v[72:73], v[68:69]
	v_cvt_pk_bf16_f32 v72, v66, v67
	s_nop 0
	v_cvt_pk_fp8_f32 v88, v68, v69 op_sel:[0,0,1]
	v_cvt_pk_bf16_f32 v73, v68, v69
	v_lshlrev_b32_e32 v70, 16, v72
	v_and_b32_e32 v71, 0xffff0000, v72
	v_lshlrev_b32_e32 v78, 16, v73
	v_and_b32_e32 v86, 0xffff0000, v73
	v_sub_f32_e32 v66, v66, v70
	v_sub_f32_e32 v67, v67, v71
	v_sub_f32_e32 v70, v68, v78
	v_sub_f32_e32 v68, v69, v86
	v_cvt_pk_bf16_f32 v126, v66, v67
	v_cvt_pk_bf16_f32 v127, v70, v68
	global_store_dword v150, v88, s[38:39] offset:1280
	global_load_dwordx4 v[68:71], v[104:105], off offset:2048
	global_load_dwordx4 v[98:101], v[106:107], off offset:2048
	s_nop 1
	v_mov_b32_dpp v66, v74 row_ror:8 row_mask:0xf bank_mask:0xf
	v_mov_b32_e32 v86, 0
	s_waitcnt lgkmcnt(0)
	v_add_f32_e32 v66, v74, v66
	v_mov_b32_e32 v67, v66
	s_nop 1
	v_permlane16_swap_b32_e32 v67, v66
	v_mov_b32_e32 v74, 0xa00
	v_bitop3_b32 v74, v130, s5, v74 bitop3:0x36
	v_add3_u32 v152, s0, v74, v103
	v_add_u32_e32 v153, 0x10000, v152
	s_waitcnt lgkmcnt(0)
	v_add_f32_e32 v66, v66, v67
	v_mov_b32_e32 v67, v66
	s_nop 1
	v_permlane32_swap_b32_e32 v67, v66
	ds_write_b64 v152, v[72:73]
	ds_write_b64 v153, v[126:127]
	s_waitcnt lgkmcnt(2)
	v_add_f32_e32 v88, v66, v67
	v_fmac_f32_e32 v112, 0xba000000, v88
	v_fmac_f32_e32 v114, 0xba000000, v88
	v_fmac_f32_e32 v113, 0xba000000, v88
	v_fmac_f32_e32 v115, 0xba000000, v88
	v_mul_f32_e32 v74, v112, v112
	v_mul_f32_e32 v78, v114, v114
	v_pk_fma_f32 v[140:141], v[112:113], v[112:113], v[74:75] op_sel_hi:[1,1,0]
	v_pk_fma_f32 v[172:173], v[114:115], v[114:115], v[78:79] op_sel_hi:[1,1,0]
	v_fmac_f32_e32 v120, 0xba000000, v88
	v_fmac_f32_e32 v124, 0xba000000, v88
	v_fmac_f32_e32 v121, 0xba000000, v88
	v_fmac_f32_e32 v125, 0xba000000, v88
	v_fmac_f32_e32 v132, 0xba000000, v88
	v_fmac_f32_e32 v133, 0xba000000, v88
	v_fmac_f32_e32 v117, 0xba000000, v88
	v_fmac_f32_e32 v118, 0xba000000, v88
	v_fmac_f32_e32 v122, 0xba000000, v88
	v_fmac_f32_e32 v119, 0xba000000, v88
	v_fmac_f32_e32 v123, 0xba000000, v88
	v_fmac_f32_e32 v116, 0xba000000, v88
	v_fmac_f32_e32 v134, 0xba000000, v88
	v_fmac_f32_e32 v135, 0xba000000, v88
	v_fmac_f32_e32 v85, 0xba000000, v88
	v_pk_mul_f32 v[128:129], v[124:125], v[124:125]
	v_pk_mul_f32 v[136:137], v[120:121], v[120:121]
	v_mov_b32_e32 v138, v117
	v_mov_b32_e32 v139, v133
	v_mov_b32_e32 v117, v132
	v_mov_b32_e32 v66, v85
	v_mov_b32_e32 v67, v135
	v_mov_b32_e32 v85, v134
	v_pk_fma_f32 v[128:129], v[122:123], v[122:123], v[128:129]
	v_pk_fma_f32 v[132:133], v[118:119], v[118:119], v[136:137]
	v_pk_mul_f32 v[134:135], v[138:139], v[138:139]
	v_pk_mul_f32 v[136:137], v[116:117], v[116:117]
	v_pk_add_f32 v[128:129], v[128:129], v[132:133]
	v_pk_mov_b32 v[132:133], v[136:137], v[134:135] op_sel:[1,0]
	v_mov_b32_e32 v137, v135
	v_pk_add_f32 v[132:133], v[132:133], v[136:137]
	v_fmac_f32_e32 v87, 0xba000000, v88
	v_fmac_f32_e32 v109, 0xba000000, v88
	v_fmac_f32_e32 v89, 0xba000000, v88
	v_fmac_f32_e32 v111, 0xba000000, v88
	v_fmac_f32_e32 v84, 0xba000000, v88
	v_pk_add_f32 v[128:129], v[128:129], v[128:129] op_sel_hi:[0,1]
	v_pk_add_f32 v[132:133], v[132:133], v[132:133] op_sel_hi:[0,1]
	v_pk_mul_f32 v[174:175], v[66:67], v[66:67]
	v_pk_mul_f32 v[176:177], v[84:85], v[84:85]
	v_mul_f32_e32 v140, v111, v111
	v_mul_f32_e32 v172, v89, v89
	v_mul_f32_e32 v128, v87, v87
	v_mul_f32_e32 v132, v109, v109
	v_fmac_f32_e32 v80, 0xba000000, v88
	v_pk_mov_b32 v[134:135], v[176:177], v[174:175] op_sel:[1,0]
	v_pk_add_f32 v[136:137], v[140:141], v[172:173]
	v_pk_add_f32 v[128:129], v[132:133], v[128:129]
	v_mov_b32_e32 v177, v175
	v_fmac_f32_e32 v81, 0xba000000, v88
	v_fmac_f32_e32 v82, 0xba000000, v88
	v_pk_add_f32 v[128:129], v[136:137], v[128:129]
	s_waitcnt vmcnt(1)
	v_pk_add_f32 v[68:69], v[68:69], 1.0 op_sel_hi:[1,0]
	v_pk_add_f32 v[70:71], v[70:71], 1.0 op_sel_hi:[1,0]
	s_waitcnt vmcnt(0)
	v_pk_fma_f32 v[68:69], v[96:97], v[68:69], v[98:99]
	v_pk_fma_f32 v[70:71], v[94:95], v[70:71], v[100:101]
	v_cvt_pk_fp8_f32 v86, v68, v69
	v_cvt_pk_bf16_f32 v72, v68, v69
	v_cvt_pk_bf16_f32 v73, v70, v71
	v_pk_add_f32 v[100:101], v[134:135], v[176:177]
	v_cvt_pk_fp8_f32 v86, v70, v71 op_sel:[0,0,1]
	v_lshlrev_b32_e32 v74, 16, v72
	v_and_b32_e32 v78, 0xffff0000, v72
	v_lshlrev_b32_e32 v94, 16, v73
	v_and_b32_e32 v95, 0xffff0000, v73
	v_sub_f32_e32 v68, v68, v74
	v_sub_f32_e32 v69, v69, v78
	v_sub_f32_e32 v74, v70, v94
	v_sub_f32_e32 v70, v71, v95
	v_cvt_pk_bf16_f32 v98, v68, v69
	v_cvt_pk_bf16_f32 v99, v74, v70
	global_store_dword v150, v86, s[38:39] offset:1536
	global_load_dwordx4 v[68:71], v[106:107], off offset:3072
	global_load_dwordx4 v[94:97], v[104:105], off offset:3072
	v_mul_f32_e32 v74, v80, v80
	v_fmac_f32_e32 v83, 0xba000000, v88
	v_pk_fma_f32 v[104:105], v[80:81], v[80:81], v[74:75] op_sel_hi:[1,1,0]
	v_mul_f32_e32 v74, v82, v82
	v_pk_add_f32 v[128:129], v[128:129], v[128:129] op_sel_hi:[0,1]
	v_pk_add_f32 v[100:101], v[100:101], v[100:101] op_sel_hi:[0,1]
	v_pk_fma_f32 v[106:107], v[82:83], v[82:83], v[74:75] op_sel_hi:[1,1,0]
	v_fmac_f32_e32 v75, 0xba000000, v88
	v_fmac_f32_e32 v79, 0xba000000, v88
	v_fmac_f32_e32 v77, 0xba000000, v88
	v_fmac_f32_e32 v76, 0xba000000, v88
	v_mul_f32_e32 v104, v76, v76
	v_mul_f32_e32 v106, v77, v77
	v_mul_f32_e32 v100, v79, v79
	v_mul_f32_e32 v128, v75, v75
	v_pk_add_f32 v[104:105], v[104:105], v[106:107]
	v_pk_add_f32 v[100:101], v[100:101], v[128:129]
	v_mov_b32_e32 v86, 0xc00
	v_pk_add_f32 v[100:101], v[104:105], v[100:101]
	v_mov_b32_e32 v88, 0xe00
	v_add_f32_e32 v74, v100, v101
	s_nop 1
	v_mov_b32_dpp v78, v74 quad_perm:[1,0,3,2] row_mask:0xf bank_mask:0xf
	v_bitop3_b32 v86, v130, s5, v86 bitop3:0x36
	v_bitop3_b32 v88, v130, s5, v88 bitop3:0x36
	v_add3_u32 v163, s0, v86, v103
	v_add3_u32 v157, s0, v88, v103
	s_waitcnt lgkmcnt(0)
; __device__ __forceinline__ unsigned cvt_pk_bf16(float lo, float hi) { unsigned r; asm volatile("v_cvt_pk_bf16_f32 %0, %1, %2" : "=v"(r) : "v"(lo), "v"(hi)); return r; }
; __device__ __forceinline__ void p6_router(Frame& F) {
;     ...
;                 for (int j = 0; j < 8; ++j) { v[j] = v[j] - mean; s2 += (v[j][0] * v[j][0] + v[j][1] * v[j][1]) + (v[j][2] * v[j][2] + v[j][3] * v[j][3]); }
;                 float rstd = 1.f / sqrtf(wave_sum(s2) * (1.f / DM) + LN_EPS);
;                 s = 0.f;
; #pragma unroll
;                 for (int j = 0; j < 8; ++j) { v[j] = v[j] * rstd * pw[j] + pb[j]; { u32x2 xb; xb.x = cvt_pk_bf16(v[j][0], v[j][1]); xb.y = cvt_pk_bf16(v[j][2], v[j][3]); ((u32x2*)(X1 + (size_t)t * DM))[lane + 64 * j] = xb; } s += (v[j][0] + v[j][1]) + (v[j][2] + v[j][3]); }
;                 mean = wave_sum(s) * (1.f / DM); s2 = 0.f;
	v_add_f32_e32 v74, v74, v78
	s_nop 1
	v_mov_b32_dpp v78, v74 quad_perm:[2,3,0,1] row_mask:0xf bank_mask:0xf
	v_add_u32_e32 v164, 0x10000, v163
	ds_write_b64 v163, v[72:73]
	ds_write_b64 v164, v[98:99]
	v_mov_b32_e32 v105, 0
	v_add_u32_e32 v158, 0x10000, v157
	s_waitcnt lgkmcnt(2)
	v_add_f32_e32 v74, v74, v78
	s_nop 1
	v_mov_b32_dpp v78, v74 row_shl:4 row_mask:0xf bank_mask:0x5
	s_nop 1
	v_mov_b32_dpp v78, v74 row_shr:4 row_mask:0xf bank_mask:0xa
	v_mov_b32_e32 v100, v123
	v_mov_b32_e32 v123, v124
	v_mov_b32_e32 v101, v125
	v_mov_b32_e32 v104, v119
	s_waitcnt lgkmcnt(0)
	v_add_f32_e32 v74, v74, v78
	s_nop 1
	v_mov_b32_dpp v78, v74 row_ror:8 row_mask:0xf bank_mask:0xf
	v_mov_b32_e32 v119, v120
	s_waitcnt lgkmcnt(0)
	v_add_f32_e32 v74, v74, v78
	v_mov_b32_e32 v78, v74
	s_nop 1
	v_permlane16_swap_b32_e32 v78, v74
	s_waitcnt lgkmcnt(0)
	v_add_f32_e32 v74, v74, v78
	v_mov_b32_e32 v78, v74
	s_nop 1
	v_permlane32_swap_b32_e32 v78, v74
	s_waitcnt lgkmcnt(0)
	v_add_f32_e32 v74, v74, v78
	v_fmamk_f32 v74, v74, 0x3a000000, v148
	v_mul_f32_e32 v78, 0x4f800000, v74
	v_cmp_gt_f32_e32 vcc, s45, v74
	s_waitcnt vmcnt(0)
	v_pk_add_f32 v[72:73], v[96:97], 1.0 op_sel_hi:[1,0]
	v_cndmask_b32_e32 v74, v74, v78, vcc
	v_sqrt_f32_e32 v78, v74
	v_pk_add_f32 v[94:95], v[94:95], 1.0 op_sel_hi:[1,0]
	v_pk_fma_f32 v[70:71], v[90:91], v[72:73], v[70:71]
	v_pk_fma_f32 v[68:69], v[92:93], v[94:95], v[68:69]
	v_add_u32_e32 v86, -1, v78
	v_add_u32_e32 v88, 1, v78
	v_fma_f32 v106, -v86, v78, v74
	v_fma_f32 v107, -v88, v78, v74
	v_cmp_ge_f32_e64 s[0:1], 0, v106
	v_cvt_pk_bf16_f32 v72, v68, v69
	v_cvt_pk_fp8_f32 v105, v68, v69
	v_cvt_pk_bf16_f32 v73, v70, v71
	v_cvt_pk_fp8_f32 v105, v70, v71 op_sel:[0,0,1]
	v_cndmask_b32_e64 v78, v78, v86, s[0:1]
	v_cmp_lt_f32_e64 s[0:1], 0, v107
	v_lshlrev_b32_e32 v90, 16, v73
	v_and_b32_e32 v91, 0xffff0000, v73
	v_cndmask_b32_e64 v78, v78, v88, s[0:1]
	v_mul_f32_e32 v86, 0x37800000, v78
	v_cndmask_b32_e32 v78, v78, v86, vcc
	v_lshlrev_b32_e32 v86, 16, v72
	v_and_b32_e32 v88, 0xffff0000, v72
	v_sub_f32_e32 v68, v68, v86
	v_sub_f32_e32 v69, v69, v88
	v_cvt_pk_bf16_f32 v68, v68, v69
	v_cmp_class_f32_e32 vcc, v74, v149
	v_sub_f32_e32 v86, v70, v90
	v_sub_f32_e32 v88, v71, v91
	v_cvt_pk_bf16_f32 v69, v86, v88
	ds_write_b64 v157, v[72:73]
	ds_write_b64 v158, v[68:69]
	v_cndmask_b32_e32 v68, v78, v74, vcc
	v_div_scale_f32 v69, s[0:1], v68, v68, 1.0
	v_rcp_f32_e32 v70, v69
	global_store_dword v150, v105, s[38:39] offset:1792
	v_mov_b32_e32 v105, v121
	v_mov_b32_e32 v88, v111
	v_fma_f32 v71, -v69, v70, 1.0
	v_fmac_f32_e32 v70, v71, v70
	v_div_scale_f32 v71, vcc, 1.0, v68, 1.0
	v_mul_f32_e32 v72, v71, v70
	v_fma_f32 v73, -v69, v72, v71
	v_fmac_f32_e32 v72, v73, v70
	v_fma_f32 v69, -v69, v72, v71
	v_div_fmas_f32 v69, v69, v70, v72
	v_div_fixup_f32 v68, v69, v68, 1.0
	v_pk_mul_f32 v[70:71], v[122:123], v[68:69] op_sel_hi:[1,0]
	v_pk_mul_f32 v[72:73], v[118:119], v[68:69] op_sel_hi:[1,0]
	v_pk_fma_f32 v[62:63], v[2:3], v[70:71], v[62:63]
	v_pk_mul_f32 v[2:3], v[100:101], v[68:69] op_sel_hi:[1,0]
	v_pk_fma_f32 v[64:65], v[4:5], v[72:73], v[64:65]
	v_pk_mul_f32 v[4:5], v[104:105], v[68:69] op_sel_hi:[1,0]
	v_pk_fma_f32 v[54:55], v[54:55], v[2:3], v[58:59]
	v_pk_fma_f32 v[56:57], v[56:57], v[4:5], v[60:61]
	v_mov_b32_e32 v2, v54
	v_mov_b32_e32 v3, v62
	v_mov_b32_e32 v4, v55
	v_mov_b32_e32 v5, v63
	v_pk_add_f32 v[2:3], v[2:3], v[4:5]
	v_mov_b32_e32 v4, v57
	v_mov_b32_e32 v5, v65
	v_mov_b32_e32 v58, v56
	v_mov_b32_e32 v59, v64
	v_pk_add_f32 v[4:5], v[4:5], v[58:59]
	v_pk_mul_f32 v[58:59], v[138:139], v[68:69] op_sel_hi:[1,0]
	v_pk_add_f32 v[2:3], v[2:3], v[4:5]
	v_pk_mul_f32 v[4:5], v[116:117], v[68:69] op_sel_hi:[1,0]
	v_pk_fma_f32 v[48:49], v[48:49], v[58:59], v[52:53]
	v_pk_fma_f32 v[46:47], v[46:47], v[4:5], v[50:51]
	v_mov_b32_e32 v5, v49
	v_mov_b32_e32 v4, v46
	v_pk_mov_b32 v[50:51], v[46:47], v[48:49] op_sel:[1,0]
	v_pk_mul_f32 v[52:53], v[114:115], v[68:69] op_sel_hi:[1,0]
	v_pk_add_f32 v[4:5], v[4:5], v[50:51]
	v_pk_mul_f32 v[50:51], v[112:113], v[68:69] op_sel_hi:[1,0]
	v_mov_b32_e32 v86, v109
	v_pk_fma_f32 v[40:41], v[40:41], v[52:53], v[44:45]
	v_pk_fma_f32 v[38:39], v[38:39], v[50:51], v[42:43]
	v_pk_mul_f32 v[50:51], v[88:89], v[68:69] op_sel_hi:[1,0]
	v_pk_mul_f32 v[52:53], v[86:87], v[68:69] op_sel_hi:[1,0]
	v_add_f32_e32 v3, 0, v3
	v_pk_add_f32 v[4:5], v[4:5], v[4:5] op_sel_hi:[0,1]
	v_pk_fma_f32 v[32:33], v[32:33], v[52:53], v[36:37]
	v_pk_fma_f32 v[30:31], v[30:31], v[50:51], v[34:35]
	v_add_f32_e32 v3, v2, v3
	v_add_f32_e32 v43, v38, v39
	v_add_f32_e32 v45, v41, v40
	v_mov_b32_e32 v42, v30
	v_mov_b32_e32 v44, v31
	v_mov_b32_e32 v4, v33
	v_mov_b32_e32 v2, v32
	v_pk_add_f32 v[34:35], v[42:43], v[44:45]
	v_pk_add_f32 v[2:3], v[4:5], v[2:3]
	v_pk_mul_f32 v[4:5], v[66:67], v[68:69] op_sel_hi:[1,0]
	v_pk_add_f32 v[2:3], v[34:35], v[2:3]
	v_pk_fma_f32 v[24:25], v[24:25], v[4:5], v[28:29]
	v_pk_add_f32 v[34:35], v[2:3], v[2:3] op_sel_hi:[0,1]
	v_pk_mul_f32 v[2:3], v[84:85], v[68:69] op_sel_hi:[1,0]
	v_mov_b32_e32 v74, v79
	v_pk_fma_f32 v[22:23], v[22:23], v[2:3], v[26:27]
	v_mov_b32_e32 v3, v25
	v_mov_b32_e32 v2, v22
	v_pk_mov_b32 v[4:5], v[22:23], v[24:25] op_sel:[1,0]
	s_add_u32 s0, s42, s36
	v_pk_add_f32 v[2:3], v[2:3], v[4:5]
	v_pk_mul_f32 v[4:5], v[82:83], v[68:69] op_sel_hi:[1,0]
	v_pk_add_f32 v[26:27], v[2:3], v[2:3] op_sel_hi:[0,1]
	v_pk_mul_f32 v[2:3], v[80:81], v[68:69] op_sel_hi:[1,0]
	v_pk_fma_f32 v[16:17], v[16:17], v[4:5], v[20:21]
	v_pk_fma_f32 v[14:15], v[14:15], v[2:3], v[18:19]
	v_pk_mul_f32 v[4:5], v[76:77], v[68:69] op_sel_hi:[1,0]
	v_pk_mul_f32 v[2:3], v[74:75], v[68:69] op_sel_hi:[1,0]
	v_pk_fma_f32 v[4:5], v[6:7], v[4:5], v[10:11]
	v_pk_fma_f32 v[2:3], v[8:9], v[2:3], v[12:13]
	v_add_f32_e32 v19, v14, v15
	v_add_f32_e32 v21, v17, v16
	v_mov_b32_e32 v18, v4
	v_mov_b32_e32 v20, v5
	v_mov_b32_e32 v26, v3
	v_mov_b32_e32 v34, v2
	v_pk_add_f32 v[6:7], v[18:19], v[20:21]
	v_pk_add_f32 v[8:9], v[26:27], v[34:35]
	s_addc_u32 s1, s43, s37
	v_pk_add_f32 v[6:7], v[6:7], v[8:9]
	v_cvt_pk_bf16_f32 v70, v62, v63
	v_cvt_pk_bf16_f32 v71, v64, v65
	global_store_dwordx2 v146, v[70:71], s[0:1]
	v_add_f32_e32 v7, v6, v7
	s_nop 1
	v_mov_b32_dpp v8, v7 quad_perm:[1,0,3,2] row_mask:0xf bank_mask:0xf
	v_cvt_pk_bf16_f32 v6, v54, v55
	s_mov_b32 s37, 0
	v_mov_b32_e32 v79, 0
	s_waitcnt lgkmcnt(0)
; __device__ __forceinline__ void p6_router(Frame& F) {
;     ...
;                 mean = wave_sum(s) * (1.f / DM); s2 = 0.f;
; #pragma unroll
;                 for (int j = 0; j < 8; ++j) { v[j] = v[j] - mean; s2 += (v[j][0] * v[j][0] + v[j][1] * v[j][1]) + (v[j][2] * v[j][2] + v[j][3] * v[j][3]); }
;                 rstd = 1.f / sqrtf(wave_sum(s2) * (1.f / DM) + LN_EPS);
;                 int loq = lane; asm volatile("" : "+v"(loq));
; #pragma unroll
;                 for (int j = 0; j < 8; ++j) { const f32x4 sh = ((const f32x4*)(mod + (size_t)b * 12288 + 6144))[loq + 64 * j], sc = ((const f32x4*)(mod + (size_t)b * 12288 + 8192))[loq + 64 * j];
	v_add_f32_e32 v8, v7, v8
	s_nop 1
	v_mov_b32_dpp v9, v8 quad_perm:[2,3,0,1] row_mask:0xf bank_mask:0xf
	v_cvt_pk_bf16_f32 v7, v56, v57
	global_store_dwordx2 v146, v[6:7], s[0:1] offset:512
	v_cvt_pk_bf16_f32 v6, v46, v47
	v_cvt_pk_bf16_f32 v7, v48, v49
	s_waitcnt lgkmcnt(0)
	v_add_f32_e32 v8, v8, v9
	s_nop 1
	v_mov_b32_dpp v9, v8 row_shl:4 row_mask:0xf bank_mask:0x5
	s_nop 1
	v_mov_b32_dpp v9, v8 row_shr:4 row_mask:0xf bank_mask:0xa
	global_store_dwordx2 v146, v[6:7], s[0:1] offset:1024
	v_cvt_pk_bf16_f32 v6, v38, v39
	v_cvt_pk_bf16_f32 v7, v40, v41
	global_store_dwordx2 v146, v[6:7], s[0:1] offset:1536
	s_waitcnt lgkmcnt(0)
	v_add_f32_e32 v8, v8, v9
	s_nop 1
	v_mov_b32_dpp v9, v8 row_ror:8 row_mask:0xf bank_mask:0xf
	v_cvt_pk_bf16_f32 v6, v30, v31
	v_cvt_pk_bf16_f32 v7, v32, v33
	global_store_dwordx2 v146, v[6:7], s[0:1] offset:2048
	v_cvt_pk_bf16_f32 v6, v22, v23
	s_waitcnt lgkmcnt(0)
	v_add_f32_e32 v8, v8, v9
	v_mov_b32_e32 v9, v8
	s_nop 1
	v_permlane16_swap_b32_e32 v9, v8
	v_cvt_pk_bf16_f32 v7, v24, v25
	global_store_dwordx2 v146, v[6:7], s[0:1] offset:2560
	v_cvt_pk_bf16_f32 v6, v14, v15
	v_cvt_pk_bf16_f32 v7, v16, v17
	s_waitcnt lgkmcnt(0)
	v_add_f32_e32 v8, v8, v9
	v_mov_b32_e32 v9, v8
	s_nop 1
	v_permlane32_swap_b32_e32 v9, v8
	global_store_dwordx2 v146, v[6:7], s[0:1] offset:3072
	v_cvt_pk_bf16_f32 v6, v4, v5
	v_cvt_pk_bf16_f32 v7, v2, v3
	global_store_dwordx2 v146, v[6:7], s[0:1] offset:3584
	s_waitcnt lgkmcnt(0)
	v_add_f32_e32 v18, v8, v9
	v_fmamk_f32 v63, v18, 0xba000000, v63
	v_fmamk_f32 v55, v18, 0xba000000, v55
	v_fmamk_f32 v65, v18, 0xba000000, v65
	v_fmac_f32_e32 v62, 0xba000000, v18
	v_fmamk_f32 v57, v18, 0xba000000, v57
	v_fmac_f32_e32 v54, 0xba000000, v18
	v_mov_b32_e32 v8, v63
	v_mov_b32_e32 v9, v55
	v_fmac_f32_e32 v64, 0xba000000, v18
	v_fmac_f32_e32 v56, 0xba000000, v18
	v_mov_b32_e32 v6, v62
	v_mov_b32_e32 v7, v54
	v_pk_mul_f32 v[8:9], v[8:9], v[8:9]
	v_mov_b32_e32 v10, v65
	v_mov_b32_e32 v11, v57
	v_pk_fma_f32 v[6:7], v[6:7], v[6:7], v[8:9]
	v_mov_b32_e32 v8, v64
	v_mov_b32_e32 v9, v56
	v_pk_mul_f32 v[10:11], v[10:11], v[10:11]
	v_fmamk_f32 v47, v18, 0xba000000, v47
	v_pk_fma_f32 v[8:9], v[8:9], v[8:9], v[10:11]
	v_fmac_f32_e32 v46, 0xba000000, v18
	v_pk_add_f32 v[6:7], v[6:7], v[8:9]
	v_fmamk_f32 v49, v18, 0xba000000, v49
	v_fmac_f32_e32 v48, 0xba000000, v18
	v_pk_add_f32 v[6:7], v[6:7], v[6:7] op_sel_hi:[0,1]
	v_pk_mul_f32 v[8:9], v[48:49], v[48:49]
	v_pk_mul_f32 v[10:11], v[46:47], v[46:47]
	v_fmac_f32_e32 v38, 0xba000000, v18
	v_pk_mov_b32 v[12:13], v[10:11], v[8:9] op_sel:[1,0]
	v_mov_b32_e32 v11, v9
	v_fmamk_f32 v39, v18, 0xba000000, v39
	v_fmac_f32_e32 v40, 0xba000000, v18
	v_mul_f32_e32 v6, v38, v38
	v_pk_add_f32 v[8:9], v[12:13], v[10:11]
	v_fmamk_f32 v41, v18, 0xba000000, v41
	v_pk_fma_f32 v[10:11], v[38:39], v[38:39], v[6:7] op_sel_hi:[1,1,0]
	v_mul_f32_e32 v6, v40, v40
	v_pk_add_f32 v[8:9], v[8:9], v[8:9] op_sel_hi:[0,1]
	v_pk_fma_f32 v[12:13], v[40:41], v[40:41], v[6:7] op_sel_hi:[1,1,0]
	v_fmamk_f32 v33, v18, 0xba000000, v33
	v_fmac_f32_e32 v32, 0xba000000, v18
	v_fmamk_f32 v31, v18, 0xba000000, v31
	v_fmac_f32_e32 v30, 0xba000000, v18
	v_mul_f32_e32 v10, v30, v30
	v_mul_f32_e32 v12, v31, v31
	v_mul_f32_e32 v8, v32, v32
	v_mul_f32_e32 v6, v33, v33
	v_pk_add_f32 v[10:11], v[10:11], v[12:13]
	v_pk_add_f32 v[6:7], v[8:9], v[6:7]
	v_fmamk_f32 v23, v18, 0xba000000, v23
	v_fmac_f32_e32 v22, 0xba000000, v18
	v_fmamk_f32 v25, v18, 0xba000000, v25
	v_fmac_f32_e32 v24, 0xba000000, v18
	v_pk_add_f32 v[6:7], v[10:11], v[6:7]
	v_pk_mul_f32 v[8:9], v[24:25], v[24:25]
	v_pk_mul_f32 v[10:11], v[22:23], v[22:23]
	v_pk_add_f32 v[6:7], v[6:7], v[6:7] op_sel_hi:[0,1]
	v_pk_mov_b32 v[12:13], v[10:11], v[8:9] op_sel:[1,0]
	v_mov_b32_e32 v11, v9
	v_fmac_f32_e32 v14, 0xba000000, v18
	v_pk_add_f32 v[8:9], v[12:13], v[10:11]
	v_fmamk_f32 v15, v18, 0xba000000, v15
	v_fmac_f32_e32 v16, 0xba000000, v18
	v_mul_f32_e32 v6, v14, v14
	v_pk_add_f32 v[12:13], v[8:9], v[8:9] op_sel_hi:[0,1]
	v_fmamk_f32 v17, v18, 0xba000000, v17
	v_pk_fma_f32 v[8:9], v[14:15], v[14:15], v[6:7] op_sel_hi:[1,1,0]
	v_mul_f32_e32 v6, v16, v16
	v_pk_fma_f32 v[10:11], v[16:17], v[16:17], v[6:7] op_sel_hi:[1,1,0]
	v_fmamk_f32 v5, v18, 0xba000000, v5
	v_fmac_f32_e32 v4, 0xba000000, v18
	v_mul_f32_e32 v8, v4, v4
	v_mul_f32_e32 v10, v5, v5
	v_pk_add_f32 v[34:35], v[8:9], v[10:11]
	v_mov_b32_e32 v8, v170
	v_fmamk_f32 v3, v18, 0xba000000, v3
	v_ashrrev_i32_e32 v9, 31, v8
	v_lshlrev_b64 v[10:11], 4, v[8:9]
	v_lshl_add_u64 v[8:9], s[16:17], 0, v[10:11]
	v_fmac_f32_e32 v2, 0xba000000, v18
	v_lshl_add_u64 v[10:11], s[20:21], 0, v[10:11]
	global_load_dwordx4 v[18:21], v[8:9], off
	global_load_dwordx4 v[26:29], v[10:11], off
	v_mul_f32_e32 v12, v2, v2
	v_mul_f32_e32 v6, v3, v3
	v_pk_add_f32 v[6:7], v[12:13], v[6:7]
	s_waitcnt vmcnt(0)
	v_pk_add_f32 v[28:29], v[28:29], 1.0 op_sel_hi:[1,0]
	v_pk_add_f32 v[6:7], v[34:35], v[6:7]
	v_pk_add_f32 v[26:27], v[26:27], 1.0 op_sel_hi:[1,0]
	v_add_f32_e32 v6, v6, v7
	s_nop 1
	v_mov_b32_dpp v7, v6 quad_perm:[1,0,3,2] row_mask:0xf bank_mask:0xf
	s_waitcnt lgkmcnt(0)
	v_add_f32_e32 v6, v6, v7
	s_nop 1
	v_mov_b32_dpp v7, v6 quad_perm:[2,3,0,1] row_mask:0xf bank_mask:0xf
	s_waitcnt lgkmcnt(0)
	v_add_f32_e32 v6, v6, v7
	s_nop 1
	v_mov_b32_dpp v7, v6 row_shl:4 row_mask:0xf bank_mask:0x5
	s_nop 1
	v_mov_b32_dpp v7, v6 row_shr:4 row_mask:0xf bank_mask:0xa
	s_waitcnt lgkmcnt(0)
	v_add_f32_e32 v6, v6, v7
	s_nop 1
	v_mov_b32_dpp v7, v6 row_ror:8 row_mask:0xf bank_mask:0xf
	s_waitcnt lgkmcnt(0)
	v_add_f32_e32 v6, v6, v7
	v_mov_b32_e32 v7, v6
	s_nop 1
	v_permlane16_swap_b32_e32 v7, v6
	s_waitcnt lgkmcnt(0)
; #define LAS __attribute__((address_space(3)))
; __device__ __forceinline__ unsigned cvt_pk_bf16(float lo, float hi) { unsigned r; asm volatile("v_cvt_pk_bf16_f32 %0, %1, %2" : "=v"(r) : "v"(lo), "v"(hi)); return r; }
; __device__ __forceinline__ unsigned pk4_fp8(float a, float b, float c, float d) { int w = 0; w = __builtin_amdgcn_cvt_pk_fp8_f32(a, b, w, false); w = __builtin_amdgcn_cvt_pk_fp8_f32(c, d, w, true); return (unsigned)w; }
; __device__ __forceinline__ float bf_lo(unsigned w) { return __uint_as_float(w << 16); }
; __device__ __forceinline__ float bf_hi(unsigned w) { return __uint_as_float(w & 0xffff0000u); }
; __device__ __forceinline__ void p6_router(Frame& F) {
;     ...
;                 rstd = 1.f / sqrtf(wave_sum(s2) * (1.f / DM) + LN_EPS);
;                 int loq = lane; asm volatile("" : "+v"(loq));
; #pragma unroll
;                 for (int j = 0; j < 8; ++j) { const f32x4 sh = ((const f32x4*)(mod + (size_t)b * 12288 + 6144))[loq + 64 * j], sc = ((const f32x4*)(mod + (size_t)b * 12288 + 8192))[loq + 64 * j];
;                     const f32x4 y = v[j] * rstd * (sc + 1.0f) + sh;
;                     u32x2 wh; wh.x = cvt_pk_bf16(y[0], y[1]); wh.y = cvt_pk_bf16(y[2], y[3]);
;                     const f32x4 yl = {y[0] - bf_lo(wh.x), y[1] - bf_hi(wh.x), y[2] - bf_lo(wh.y), y[3] - bf_hi(wh.y)};
;                     u32x2 wl; wl.x = cvt_pk_bf16(yl[0], yl[1]); wl.y = cvt_pk_bf16(yl[2], yl[3]);
;                     { const int r = 2 * wave + q; LAS unsigned char* rowp = F.lds + r * 4096 + ((((lane >> 1) + 32 * j) ^ r) << 4) + (lane & 1) * 8;
;                       *(LAS u32x2*)rowp = wh; *(LAS u32x2*)(rowp + 65536) = wl; }
;                     U2F[(size_t)t * (DM / 4) + lane + 64 * j] = pk4_fp8(y[0], y[1], y[2], y[3]); }
	v_add_f32_e32 v6, v6, v7
	v_mov_b32_e32 v7, v6
	s_nop 1
	v_permlane32_swap_b32_e32 v7, v6
	s_waitcnt lgkmcnt(0)
	v_add_f32_e32 v6, v6, v7
	v_fmamk_f32 v6, v6, 0x3a000000, v148
	v_mul_f32_e32 v7, 0x4f800000, v6
	v_cmp_gt_f32_e32 vcc, s45, v6
	s_nop 1
	v_cndmask_b32_e32 v6, v6, v7, vcc
	v_sqrt_f32_e32 v7, v6
	s_nop 0
	v_add_u32_e32 v12, -1, v7
	v_fma_f32 v13, -v12, v7, v6
	v_cmp_ge_f32_e64 s[0:1], 0, v13
	v_add_u32_e32 v13, 1, v7
	s_nop 0
	v_cndmask_b32_e64 v12, v7, v12, s[0:1]
	v_fma_f32 v7, -v13, v7, v6
	v_cmp_lt_f32_e64 s[0:1], 0, v7
	s_nop 1
	v_cndmask_b32_e64 v7, v12, v13, s[0:1]
	v_mul_f32_e32 v12, 0x37800000, v7
	v_cndmask_b32_e32 v7, v7, v12, vcc
	v_cmp_class_f32_e32 vcc, v6, v149
	s_nop 1
	v_cndmask_b32_e32 v6, v7, v6, vcc
	v_div_scale_f32 v7, s[0:1], v6, v6, 1.0
	v_rcp_f32_e32 v12, v7
	s_lshl_b64 s[0:1], s[24:25], 11
	s_lshl_b32 s25, s46, 1
	s_or_b32 s24, s25, 1
	v_fma_f32 v13, -v7, v12, 1.0
	v_fmac_f32_e32 v12, v13, v12
	v_div_scale_f32 v13, vcc, 1.0, v6, 1.0
	v_mul_f32_e32 v34, v13, v12
	v_fma_f32 v35, -v7, v34, v13
	v_fmac_f32_e32 v34, v35, v12
	v_fma_f32 v7, -v7, v34, v13
	v_div_fmas_f32 v7, v7, v12, v34
	v_div_fixup_f32 v6, v7, v6, 1.0
	v_pk_mul_f32 v[12:13], v[62:63], v[6:7] op_sel_hi:[1,0]
	v_pk_mul_f32 v[34:35], v[64:65], v[6:7] op_sel_hi:[1,0]
	v_pk_fma_f32 v[12:13], v[26:27], v[12:13], v[18:19]
	v_pk_fma_f32 v[20:21], v[28:29], v[34:35], v[20:21]
	v_cvt_pk_bf16_f32 v34, v12, v13
	s_lshl_b32 s24, s24, 12
	v_lshlrev_b32_e32 v7, 16, v34
	v_sub_f32_e32 v7, v12, v7
	v_and_b32_e32 v18, 0xffff0000, v34
	v_cvt_pk_bf16_f32 v35, v20, v21
	v_sub_f32_e32 v18, v13, v18
	v_cvt_pk_bf16_f32 v36, v7, v18
	v_mov_b32_e32 v7, 0
	v_cvt_pk_fp8_f32 v7, v12, v13
	s_add_i32 s24, s24, 0
	s_add_u32 s0, s40, s0
	v_lshlrev_b32_e32 v19, 16, v35
	v_cvt_pk_fp8_f32 v7, v20, v21 op_sel:[0,0,1]
	v_and_b32_e32 v26, 0xffff0000, v35
	s_addc_u32 s1, s44, s1
	v_sub_f32_e32 v19, v20, v19
	v_sub_f32_e32 v26, v21, v26
	v_cvt_pk_bf16_f32 v37, v19, v26
	global_store_dword v150, v7, s[0:1]
	global_load_dwordx4 v[18:21], v[10:11], off offset:1024
	global_load_dwordx4 v[26:29], v[8:9], off offset:1024
	v_lshrrev_b32_e32 v7, 1, v170
	v_bitop3_b32 v12, s25, v7, 1 bitop3:0x36
	v_lshlrev_b32_e32 v12, 4, v12
	v_add3_u32 v172, s24, v12, v103
	v_pk_mul_f32 v[12:13], v[54:55], v[6:7] op_sel_hi:[1,0]
	ds_write_b64 v172, v[34:35]
	v_pk_mul_f32 v[34:35], v[56:57], v[6:7] op_sel_hi:[1,0]
	v_add_u32_e32 v173, 0x10000, v172
	ds_write_b64 v173, v[36:37]
	v_or_b32_e32 v36, 32, v7
	v_bitop3_b32 v36, s25, v36, 1 bitop3:0x36
	v_lshlrev_b32_e32 v36, 4, v36
	v_add3_u32 v174, s24, v36, v103
	v_add_u32_e32 v175, 0x10000, v174
	v_or_b32_e32 v36, 64, v7
	v_bitop3_b32 v36, s25, v36, 1 bitop3:0x36
	v_lshlrev_b32_e32 v36, 4, v36
	v_add3_u32 v167, s24, v36, v103
	v_add_u32_e32 v168, 0x10000, v167
	v_pk_mul_f32 v[22:23], v[22:23], v[6:7] op_sel_hi:[1,0]
	v_pk_mul_f32 v[24:25], v[24:25], v[6:7] op_sel_hi:[1,0]
	v_pk_mul_f32 v[14:15], v[14:15], v[6:7] op_sel_hi:[1,0]
	v_pk_mul_f32 v[16:17], v[16:17], v[6:7] op_sel_hi:[1,0]
	s_waitcnt vmcnt(1)
	v_pk_add_f32 v[18:19], v[18:19], 1.0 op_sel_hi:[1,0]
	s_waitcnt vmcnt(0)
	v_pk_fma_f32 v[12:13], v[18:19], v[12:13], v[26:27]
	v_mov_b32_e32 v26, 0
	v_cvt_pk_fp8_f32 v26, v12, v13
	v_pk_add_f32 v[20:21], v[20:21], 1.0 op_sel_hi:[1,0]
	s_nop 0
	v_pk_fma_f32 v[20:21], v[20:21], v[34:35], v[28:29]
	v_cvt_pk_bf16_f32 v34, v12, v13
	s_nop 0
	v_cvt_pk_fp8_f32 v26, v20, v21 op_sel:[0,0,1]
	v_lshlrev_b32_e32 v18, 16, v34
	v_cvt_pk_bf16_f32 v35, v20, v21
	v_sub_f32_e32 v18, v12, v18
	v_and_b32_e32 v19, 0xffff0000, v34
	v_lshlrev_b32_e32 v12, 16, v35
	v_sub_f32_e32 v19, v13, v19
	v_sub_f32_e32 v13, v20, v12
	v_and_b32_e32 v12, 0xffff0000, v35
	v_sub_f32_e32 v20, v21, v12
	v_cvt_pk_bf16_f32 v12, v18, v19
	v_cvt_pk_bf16_f32 v13, v13, v20
	global_store_dword v150, v26, s[0:1] offset:256
	global_load_dwordx4 v[18:21], v[10:11], off offset:2048
	s_nop 0
	global_load_dwordx4 v[26:29], v[8:9], off offset:2048
	ds_write_b64 v175, v[12:13]
	v_pk_mul_f32 v[12:13], v[46:47], v[6:7] op_sel_hi:[1,0]
	ds_write_b64 v174, v[34:35]
	v_pk_mul_f32 v[34:35], v[48:49], v[6:7] op_sel_hi:[1,0]
	s_waitcnt vmcnt(1)
	v_pk_add_f32 v[18:19], v[18:19], 1.0 op_sel_hi:[1,0]
	s_waitcnt vmcnt(0)
	v_pk_fma_f32 v[12:13], v[18:19], v[12:13], v[26:27]
	v_mov_b32_e32 v26, 0
	v_cvt_pk_fp8_f32 v26, v12, v13
	v_pk_add_f32 v[20:21], v[20:21], 1.0 op_sel_hi:[1,0]
	s_nop 0
	v_pk_fma_f32 v[20:21], v[20:21], v[34:35], v[28:29]
	v_cvt_pk_bf16_f32 v34, v12, v13
	s_nop 0
	v_cvt_pk_fp8_f32 v26, v20, v21 op_sel:[0,0,1]
	v_lshlrev_b32_e32 v18, 16, v34
	v_cvt_pk_bf16_f32 v35, v20, v21
	v_sub_f32_e32 v18, v12, v18
	v_and_b32_e32 v19, 0xffff0000, v34
	v_lshlrev_b32_e32 v12, 16, v35
	v_sub_f32_e32 v19, v13, v19
	v_sub_f32_e32 v13, v20, v12
	v_and_b32_e32 v12, 0xffff0000, v35
	v_sub_f32_e32 v20, v21, v12
	v_cvt_pk_bf16_f32 v12, v18, v19
	v_cvt_pk_bf16_f32 v13, v13, v20
	global_store_dword v150, v26, s[0:1] offset:512
	global_load_dwordx4 v[18:21], v[10:11], off offset:3072
	s_nop 0
	global_load_dwordx4 v[26:29], v[8:9], off offset:3072
	ds_write_b64 v167, v[34:35]
	ds_write_b64 v168, v[12:13]
	v_pk_mul_f32 v[12:13], v[38:39], v[6:7] op_sel_hi:[1,0]
	v_pk_mul_f32 v[34:35], v[40:41], v[6:7] op_sel_hi:[1,0]
	v_mov_b32_e32 v38, 0
	s_waitcnt vmcnt(1)
	v_pk_add_f32 v[20:21], v[20:21], 1.0 op_sel_hi:[1,0]
	v_pk_add_f32 v[18:19], v[18:19], 1.0 op_sel_hi:[1,0]
	s_waitcnt vmcnt(0)
; #define LAS __attribute__((address_space(3)))
; __device__ __forceinline__ unsigned cvt_pk_bf16(float lo, float hi) { unsigned r; asm volatile("v_cvt_pk_bf16_f32 %0, %1, %2" : "=v"(r) : "v"(lo), "v"(hi)); return r; }
; __device__ __forceinline__ unsigned pk4_fp8(float a, float b, float c, float d) { int w = 0; w = __builtin_amdgcn_cvt_pk_fp8_f32(a, b, w, false); w = __builtin_amdgcn_cvt_pk_fp8_f32(c, d, w, true); return (unsigned)w; }
; __device__ __forceinline__ float bf_lo(unsigned w) { return __uint_as_float(w << 16); }
; __device__ __forceinline__ float bf_hi(unsigned w) { return __uint_as_float(w & 0xffff0000u); }
; __device__ __forceinline__ void p6_router(Frame& F) {
;     ...
; #pragma unroll
;                 for (int j = 0; j < 8; ++j) { const f32x4 sh = ((const f32x4*)(mod + (size_t)b * 12288 + 6144))[loq + 64 * j], sc = ((const f32x4*)(mod + (size_t)b * 12288 + 8192))[loq + 64 * j];
;                     const f32x4 y = v[j] * rstd * (sc + 1.0f) + sh;
;                     u32x2 wh; wh.x = cvt_pk_bf16(y[0], y[1]); wh.y = cvt_pk_bf16(y[2], y[3]);
;                     const f32x4 yl = {y[0] - bf_lo(wh.x), y[1] - bf_hi(wh.x), y[2] - bf_lo(wh.y), y[3] - bf_hi(wh.y)};
;                     u32x2 wl; wl.x = cvt_pk_bf16(yl[0], yl[1]); wl.y = cvt_pk_bf16(yl[2], yl[3]);
;                     { const int r = 2 * wave + q; LAS unsigned char* rowp = F.lds + r * 4096 + ((((lane >> 1) + 32 * j) ^ r) << 4) + (lane & 1) * 8;
;                       *(LAS u32x2*)rowp = wh; *(LAS u32x2*)(rowp + 65536) = wl; }
;                     U2F[(size_t)t * (DM / 4) + lane + 64 * j] = pk4_fp8(y[0], y[1], y[2], y[3]); }
	v_pk_fma_f32 v[20:21], v[34:35], v[20:21], v[28:29]
	v_pk_fma_f32 v[12:13], v[12:13], v[18:19], v[26:27]
	v_mov_b32_e32 v34, 0
	v_cvt_pk_fp8_f32 v34, v12, v13
	v_cvt_pk_bf16_f32 v26, v12, v13
	v_cvt_pk_bf16_f32 v27, v20, v21
	v_cvt_pk_fp8_f32 v34, v20, v21 op_sel:[0,0,1]
	v_lshlrev_b32_e32 v18, 16, v26
	v_and_b32_e32 v19, 0xffff0000, v26
	v_sub_f32_e32 v18, v12, v18
	v_sub_f32_e32 v19, v13, v19
	v_lshlrev_b32_e32 v12, 16, v27
	v_and_b32_e32 v13, 0xffff0000, v27
	v_sub_f32_e32 v12, v20, v12
	v_sub_f32_e32 v13, v21, v13
	v_cvt_pk_bf16_f32 v28, v18, v19
	v_cvt_pk_bf16_f32 v29, v12, v13
	global_store_dword v150, v34, s[0:1] offset:768
	v_add_co_u32_e32 v34, vcc, s41, v10
	s_nop 1
	v_addc_co_u32_e32 v35, vcc, 0, v11, vcc
	v_add_co_u32_e32 v36, vcc, s41, v8
	global_load_dwordx4 v[10:13], v[34:35], off
	s_nop 0
	v_addc_co_u32_e32 v37, vcc, 0, v9, vcc
	global_load_dwordx4 v[18:21], v[36:37], off
	v_or_b32_e32 v8, 0x60, v7
	v_bitop3_b32 v8, s25, v8, 1 bitop3:0x36
	v_lshlrev_b32_e32 v8, 4, v8
	v_add3_u32 v176, s24, v8, v103
	v_pk_mul_f32 v[8:9], v[30:31], v[6:7] op_sel_hi:[1,0]
	v_pk_mul_f32 v[30:31], v[32:33], v[6:7] op_sel_hi:[1,0]
	v_add_u32_e32 v177, 0x10000, v176
	ds_write_b64 v176, v[26:27]
	ds_write_b64 v177, v[28:29]
	v_mov_b32_e32 v28, 0
	v_or_b32_e32 v29, 0x80, v7
	v_bitop3_b32 v29, s25, v29, 1 bitop3:0x36
	v_lshlrev_b32_e32 v29, 4, v29
	v_add3_u32 v178, s24, v29, v103
	v_add_u32_e32 v179, 0x10000, v178
	s_waitcnt vmcnt(1)
	v_pk_add_f32 v[10:11], v[10:11], 1.0 op_sel_hi:[1,0]
	v_pk_add_f32 v[12:13], v[12:13], 1.0 op_sel_hi:[1,0]
	s_waitcnt vmcnt(0)
	v_pk_fma_f32 v[8:9], v[8:9], v[10:11], v[18:19]
	s_nop 0
	v_cvt_pk_fp8_f32 v38, v8, v9
	v_pk_fma_f32 v[12:13], v[30:31], v[12:13], v[20:21]
	v_cvt_pk_bf16_f32 v26, v8, v9
	s_nop 0
	v_cvt_pk_fp8_f32 v38, v12, v13 op_sel:[0,0,1]
	v_cvt_pk_bf16_f32 v27, v12, v13
	v_lshlrev_b32_e32 v10, 16, v26
	v_and_b32_e32 v11, 0xffff0000, v26
	v_lshlrev_b32_e32 v18, 16, v27
	v_and_b32_e32 v19, 0xffff0000, v27
	v_sub_f32_e32 v8, v8, v10
	v_sub_f32_e32 v9, v9, v11
	v_sub_f32_e32 v10, v12, v18
	v_sub_f32_e32 v11, v13, v19
	v_cvt_pk_bf16_f32 v12, v8, v9
	v_cvt_pk_bf16_f32 v13, v10, v11
	global_store_dword v150, v38, s[0:1] offset:1024
	global_load_dwordx4 v[8:11], v[34:35], off offset:1024
	global_load_dwordx4 v[18:21], v[36:37], off offset:1024
	ds_write_b64 v178, v[26:27]
	ds_write_b64 v179, v[12:13]
	s_waitcnt vmcnt(1)
	v_pk_add_f32 v[8:9], v[8:9], 1.0 op_sel_hi:[1,0]
	s_waitcnt vmcnt(0)
	v_pk_fma_f32 v[8:9], v[22:23], v[8:9], v[18:19]
	v_pk_add_f32 v[10:11], v[10:11], 1.0 op_sel_hi:[1,0]
	v_cvt_pk_fp8_f32 v28, v8, v9
	v_pk_fma_f32 v[10:11], v[24:25], v[10:11], v[20:21]
	v_cvt_pk_bf16_f32 v12, v8, v9
	v_mov_b32_e32 v24, 0
	v_cvt_pk_fp8_f32 v28, v10, v11 op_sel:[0,0,1]
	v_cvt_pk_bf16_f32 v13, v10, v11
	v_lshlrev_b32_e32 v18, 16, v12
	v_and_b32_e32 v19, 0xffff0000, v12
	v_lshlrev_b32_e32 v20, 16, v13
	v_and_b32_e32 v21, 0xffff0000, v13
	v_sub_f32_e32 v8, v8, v18
	v_sub_f32_e32 v9, v9, v19
	v_sub_f32_e32 v18, v10, v20
	v_sub_f32_e32 v10, v11, v21
	v_cvt_pk_bf16_f32 v22, v8, v9
	v_cvt_pk_bf16_f32 v23, v18, v10
	global_store_dword v150, v28, s[0:1] offset:1280
	global_load_dwordx4 v[8:11], v[34:35], off offset:2048
	global_load_dwordx4 v[18:21], v[36:37], off offset:2048
	v_or_b32_e32 v25, 0xa0, v7
	v_bitop3_b32 v25, s25, v25, 1 bitop3:0x36
	v_lshlrev_b32_e32 v25, 4, v25
	v_add3_u32 v180, s24, v25, v103
	v_add_u32_e32 v181, 0x10000, v180
	ds_write_b64 v180, v[12:13]
	ds_write_b64 v181, v[22:23]
	s_waitcnt vmcnt(1)
	v_pk_add_f32 v[8:9], v[8:9], 1.0 op_sel_hi:[1,0]
	s_waitcnt vmcnt(0)
	v_pk_fma_f32 v[8:9], v[14:15], v[8:9], v[18:19]
	v_pk_add_f32 v[10:11], v[10:11], 1.0 op_sel_hi:[1,0]
	v_cvt_pk_fp8_f32 v24, v8, v9
	v_pk_fma_f32 v[10:11], v[16:17], v[10:11], v[20:21]
	v_cvt_pk_bf16_f32 v16, v8, v9
	v_or_b32_e32 v21, 0xc0, v7
	v_cvt_pk_fp8_f32 v24, v10, v11 op_sel:[0,0,1]
	v_cvt_pk_bf16_f32 v17, v10, v11
	v_lshlrev_b32_e32 v12, 16, v16
	v_and_b32_e32 v13, 0xffff0000, v16
	v_lshlrev_b32_e32 v14, 16, v17
	v_and_b32_e32 v15, 0xffff0000, v17
	v_sub_f32_e32 v8, v8, v12
	v_sub_f32_e32 v9, v9, v13
	v_sub_f32_e32 v12, v10, v14
	v_sub_f32_e32 v10, v11, v15
	v_cvt_pk_bf16_f32 v18, v8, v9
	v_cvt_pk_bf16_f32 v19, v12, v10
	global_store_dword v150, v24, s[0:1] offset:1536
	global_load_dwordx4 v[8:11], v[34:35], off offset:3072
	global_load_dwordx4 v[12:15], v[36:37], off offset:3072
	v_or_b32_e32 v7, 0xe0, v7
	v_bitop3_b32 v7, s25, v7, 1 bitop3:0x36
	v_pk_mul_f32 v[4:5], v[4:5], v[6:7] op_sel_hi:[1,0]
	v_mov_b32_e32 v20, 0
	v_lshlrev_b32_e32 v22, 4, v7
	v_pk_mul_f32 v[2:3], v[2:3], v[6:7] op_sel_hi:[1,0]
	v_bitop3_b32 v21, s25, v21, 1 bitop3:0x36
	v_lshlrev_b32_e32 v21, 4, v21
	v_add3_u32 v184, s24, v21, v103
	v_add_u32_e32 v185, 0x10000, v184
	ds_write_b64 v184, v[16:17]
	ds_write_b64 v185, v[18:19]
	v_add3_u32 v182, s24, v22, v103
	v_add_u32_e32 v183, 0x10000, v182
	s_waitcnt vmcnt(1)
	v_pk_add_f32 v[8:9], v[8:9], 1.0 op_sel_hi:[1,0]
	s_waitcnt vmcnt(0)
; #define LAS __attribute__((address_space(3)))
; __device__ __forceinline__ void p6_router(Frame& F) {
;     ...
;             __builtin_amdgcn_sched_barrier(0);
;             bf16x8 bh[2][2], bl[2][2]; f32x4 cur[2] = {(f32x4){0.f, 0.f, 0.f, 0.f}, (f32x4){0.f, 0.f, 0.f, 0.f}};
;             const bf16_t* wbh = WRH + (size_t)fr * DM + wave * 256 + fq * 8; const bf16_t* wbl = WRL + (size_t)fr * DM + wave * 256 + fq * 8;
; #pragma unroll
;             for (int n = 0; n < 2; ++n) { bh[0][n] = *(const bf16x8*)(wbh + (size_t)(16 * n) * DM); bl[0][n] = *(const bf16x8*)(wbl + (size_t)(16 * n) * DM); }
;             if (rp == 0) {
; #pragma unroll
;                 for (int q = 0; q < 2; ++q)
; #pragma unroll
;                     for (int j = 0; j < 8; ++j) zr[q][j] = ((const u32x2*)(ZB + (size_t)(ta + 2 + q) * DM))[lane + 64 * j];
;             }
;             __syncthreads();
; #pragma unroll
;             for (int ks = 0; ks < 8; ++ks) {
;                 if (ks < 7) {
; #pragma unroll
;                     for (int n = 0; n < 2; ++n) { bh[(ks + 1) & 1][n] = *(const bf16x8*)(wbh + (size_t)(16 * n) * DM + (ks + 1) * 32); bl[(ks + 1) & 1][n] = *(const bf16x8*)(wbl + (size_t)(16 * n) * DM + (ks + 1) * 32); }
;                 }
;                 const LAS unsigned char* ap = F.lds + fr * 4096 + (((wave * 32 + ks * 4 + fq) ^ fr) << 4);
;                 const bf16x8 ah = *(const LAS bf16x8*)ap, al = *(const LAS bf16x8*)(ap + 65536);
; #pragma unroll
;                 for (int n = 0; n < 2; ++n) {
;                     cur[n] = __builtin_amdgcn_mfma_f32_16x16x32_bf16(ah, bh[ks & 1][n], cur[n], 0, 0, 0);
;                     cur[n] = __builtin_amdgcn_mfma_f32_16x16x32_bf16(ah, bl[ks & 1][n], cur[n], 0, 0, 0);
;                     cur[n] = __builtin_amdgcn_mfma_f32_16x16x32_bf16(al, bh[ks & 1][n], cur[n], 0, 0, 0);
;                 }
;                 __builtin_amdgcn_sched_barrier(0);
;             }
	v_pk_fma_f32 v[4:5], v[4:5], v[8:9], v[12:13]
	v_pk_add_f32 v[6:7], v[10:11], 1.0 op_sel_hi:[1,0]
	v_cvt_pk_fp8_f32 v20, v4, v5
	v_pk_fma_f32 v[2:3], v[2:3], v[6:7], v[14:15]
	v_cvt_pk_bf16_f32 v6, v4, v5
	s_nop 0
	v_cvt_pk_fp8_f32 v20, v2, v3 op_sel:[0,0,1]
	v_lshlrev_b32_e32 v8, 16, v6
	v_and_b32_e32 v9, 0xffff0000, v6
	v_cvt_pk_bf16_f32 v7, v2, v3
	v_sub_f32_e32 v4, v4, v8
	v_lshlrev_b32_e32 v10, 16, v7
	v_and_b32_e32 v11, 0xffff0000, v7
	v_sub_f32_e32 v5, v5, v9
	v_sub_f32_e32 v8, v2, v10
	v_sub_f32_e32 v9, v3, v11
	v_cvt_pk_bf16_f32 v4, v4, v5
	v_cvt_pk_bf16_f32 v5, v8, v9
	ds_write_b64 v182, v[6:7]
	ds_write_b64 v183, v[4:5]
	global_store_dword v150, v20, s[0:1] offset:1792
	v_lshlrev_b32_e32 v78, 12, v151
	s_lshl_b32 s36, s46, 9
	v_lshl_add_u64 v[4:5], s[82:83], 0, v[78:79]
	v_and_b32_e32 v2, 48, v170
	v_mov_b32_e32 v3, v79
	v_lshl_add_u64 v[4:5], v[4:5], 0, s[36:37]
	v_lshl_add_u64 v[44:45], v[4:5], 0, v[2:3]
	s_mov_b32 s0, 0x3c00000
	v_add_co_u32_e32 v84, vcc, s0, v44
	s_mov_b32 s1, 0x3c10000
	s_nop 0
	v_addc_co_u32_e32 v85, vcc, 0, v45, vcc
	global_load_dwordx4 v[2:5], v[84:85], off
	v_add_co_u32_e32 v74, vcc, s1, v44
	s_mov_b32 s0, 0x3c20000
	s_nop 0
	v_addc_co_u32_e32 v75, vcc, 0, v45, vcc
	v_add_co_u32_e32 v86, vcc, s0, v44
	global_load_dwordx4 v[6:9], v[74:75], off
	s_nop 0
	v_addc_co_u32_e32 v87, vcc, 0, v45, vcc
	global_load_dwordx4 v[20:23], v[86:87], off
	s_mov_b32 s0, 0x3c30000
	v_add_co_u32_e32 v76, vcc, s0, v44
	s_or_b32 s0, s4, 2
	s_nop 0
	v_addc_co_u32_e32 v77, vcc, 0, v45, vcc
	global_load_dwordx4 v[24:27], v[76:77], off
	s_ashr_i32 s1, s0, 31
	s_lshl_b64 s[0:1], s[0:1], 12
	s_add_u32 s0, s6, s0
	s_addc_u32 s1, s7, s1
	s_or_b32 s24, s4, 3
	v_bitop3_b32 v10, s5, v151, v154 bitop3:0x36
	v_add_u32_e32 v52, 0, v78
	s_ashr_i32 s25, s24, 31
	v_lshl_add_u32 v186, v10, 4, v52
	global_load_dwordx2 v[46:47], v146, s[0:1]
	global_load_dwordx2 v[48:49], v146, s[0:1] offset:512
	global_load_dwordx2 v[50:51], v146, s[0:1] offset:1024
	global_load_dwordx2 v[18:19], v146, s[0:1] offset:1536
	global_load_dwordx2 v[16:17], v146, s[0:1] offset:2048
	global_load_dwordx2 v[14:15], v146, s[0:1] offset:2560
	global_load_dwordx2 v[12:13], v146, s[0:1] offset:3072
	global_load_dwordx2 v[10:11], v146, s[0:1] offset:3584
	s_lshl_b64 s[0:1], s[24:25], 12
	s_add_u32 s0, s6, s0
	s_addc_u32 s1, s7, s1
	global_load_dwordx2 v[100:101], v146, s[0:1]
	global_load_dwordx2 v[102:103], v146, s[0:1] offset:512
	global_load_dwordx2 v[98:99], v146, s[0:1] offset:1024
	global_load_dwordx2 v[96:97], v146, s[0:1] offset:1536
	global_load_dwordx2 v[94:95], v146, s[0:1] offset:2048
	global_load_dwordx2 v[92:93], v146, s[0:1] offset:2560
	global_load_dwordx2 v[90:91], v146, s[0:1] offset:3072
	global_load_dwordx2 v[88:89], v146, s[0:1] offset:3584
	s_waitcnt lgkmcnt(0)
	s_barrier
	ds_read_b128 v[28:31], v186
	v_add_u32_e32 v187, 0x10000, v186
	ds_read_b128 v[32:35], v187
	s_mov_b64 s[0:1], 0x3c00000
	s_mov_b64 s[6:7], 0x3c20000
	v_lshl_add_u64 v[80:81], v[44:45], 0, s[0:1]
	v_lshl_add_u64 v[82:83], v[44:45], 0, s[6:7]
	v_or_b32_e32 v44, s5, v154
	s_waitcnt vmcnt(19) lgkmcnt(1)
	v_mfma_f32_16x16x32_bf16 v[36:39], v[28:31], v[2:5], 0
	s_waitcnt vmcnt(18)
	v_mfma_f32_16x16x32_bf16 v[40:43], v[28:31], v[6:9], 0
	s_waitcnt vmcnt(17)
	v_mfma_f32_16x16x32_bf16 v[20:23], v[28:31], v[20:23], v[36:39]
	s_waitcnt vmcnt(16)
	v_mfma_f32_16x16x32_bf16 v[24:27], v[28:31], v[24:27], v[40:43]
	global_load_dwordx4 v[28:31], v[80:81], off offset:64
	s_nop 0
	global_load_dwordx4 v[36:39], v[82:83], off offset:64
	s_waitcnt lgkmcnt(0)
	v_mfma_f32_16x16x32_bf16 v[2:5], v[32:35], v[2:5], v[20:23]
	s_nop 2
	global_load_dwordx4 v[20:23], v[74:75], off offset:64
	global_load_dwordx4 v[40:43], v[76:77], off offset:64
	v_mfma_f32_16x16x32_bf16 v[6:9], v[32:35], v[6:9], v[24:27]
	s_nop 2
	v_bitop3_b32 v24, v44, v151, 4 bitop3:0x36
	v_lshl_add_u32 v188, v24, 4, v52
	ds_read_b128 v[24:27], v188
	v_add_u32_e32 v189, 0x10000, v188
	ds_read_b128 v[32:35], v189
	s_waitcnt vmcnt(3) lgkmcnt(1)
	v_mfma_f32_16x16x32_bf16 v[2:5], v[24:27], v[28:31], v[2:5]
	s_waitcnt vmcnt(1)
	v_mfma_f32_16x16x32_bf16 v[6:9], v[24:27], v[20:23], v[6:9]
	v_mfma_f32_16x16x32_bf16 v[2:5], v[24:27], v[36:39], v[2:5]
	s_waitcnt vmcnt(0)
	v_mfma_f32_16x16x32_bf16 v[6:9], v[24:27], v[40:43], v[6:9]
	global_load_dwordx4 v[24:27], v[80:81], off offset:128
	global_load_dwordx4 v[36:39], v[82:83], off offset:128
	s_waitcnt lgkmcnt(0)
	v_mfma_f32_16x16x32_bf16 v[2:5], v[32:35], v[28:31], v[2:5]
	global_load_dwordx4 v[28:31], v[74:75], off offset:128
	global_load_dwordx4 v[40:43], v[76:77], off offset:128
	v_mfma_f32_16x16x32_bf16 v[6:9], v[32:35], v[20:23], v[6:9]
	v_bitop3_b32 v20, v44, v151, 8 bitop3:0x36
	v_lshl_add_u32 v190, v20, 4, v52
	ds_read_b128 v[20:23], v190
	v_add_u32_e32 v191, 0x10000, v190
	ds_read_b128 v[32:35], v191
	s_waitcnt vmcnt(3) lgkmcnt(1)
	v_mfma_f32_16x16x32_bf16 v[2:5], v[20:23], v[24:27], v[2:5]
	s_waitcnt vmcnt(1)
	v_mfma_f32_16x16x32_bf16 v[6:9], v[20:23], v[28:31], v[6:9]
	v_mfma_f32_16x16x32_bf16 v[2:5], v[20:23], v[36:39], v[2:5]
	s_waitcnt vmcnt(0)
	v_mfma_f32_16x16x32_bf16 v[6:9], v[20:23], v[40:43], v[6:9]
	global_load_dwordx4 v[20:23], v[80:81], off offset:192
	global_load_dwordx4 v[36:39], v[82:83], off offset:192
	s_waitcnt lgkmcnt(0)
	v_mfma_f32_16x16x32_bf16 v[2:5], v[32:35], v[24:27], v[2:5]
	global_load_dwordx4 v[24:27], v[74:75], off offset:192
	global_load_dwordx4 v[40:43], v[76:77], off offset:192
	v_mfma_f32_16x16x32_bf16 v[6:9], v[32:35], v[28:31], v[6:9]
	v_bitop3_b32 v28, v44, v151, 12 bitop3:0x36
	v_lshl_add_u32 v192, v28, 4, v52
	ds_read_b128 v[28:31], v192
	v_add_u32_e32 v193, 0x10000, v192
	ds_read_b128 v[32:35], v193
	s_waitcnt vmcnt(3) lgkmcnt(1)
; #define LAS __attribute__((address_space(3)))
; __device__ __forceinline__ float bf_lo(unsigned w) { return __uint_as_float(w << 16); }
; __device__ __forceinline__ float bf_hi(unsigned w) { return __uint_as_float(w & 0xffff0000u); }
; __device__ __forceinline__ void p6_router(Frame& F) {
;     ...
;                 const int t = ta + q; f32x4 v[8]; float s = 0.f;
; #pragma unroll
;                 for (int j = 0; j < 8; ++j) { const u32x2 zb = zr[q][j]; v[j] = (f32x4){bf_lo(zb.x), bf_hi(zb.x), bf_lo(zb.y), bf_hi(zb.y)}; s += (v[j][0] + v[j][1]) + (v[j][2] + v[j][3]); }
;     ...
; #pragma unroll
;             for (int ks = 0; ks < 8; ++ks) {
;                 if (ks < 7) {
; #pragma unroll
;                     for (int n = 0; n < 2; ++n) { bh[(ks + 1) & 1][n] = *(const bf16x8*)(wbh + (size_t)(16 * n) * DM + (ks + 1) * 32); bl[(ks + 1) & 1][n] = *(const bf16x8*)(wbl + (size_t)(16 * n) * DM + (ks + 1) * 32); }
;                 }
;                 const LAS unsigned char* ap = F.lds + fr * 4096 + (((wave * 32 + ks * 4 + fq) ^ fr) << 4);
;                 const bf16x8 ah = *(const LAS bf16x8*)ap, al = *(const LAS bf16x8*)(ap + 65536);
; #pragma unroll
;                 for (int n = 0; n < 2; ++n) {
;                     cur[n] = __builtin_amdgcn_mfma_f32_16x16x32_bf16(ah, bh[ks & 1][n], cur[n], 0, 0, 0);
;                     cur[n] = __builtin_amdgcn_mfma_f32_16x16x32_bf16(ah, bl[ks & 1][n], cur[n], 0, 0, 0);
;                     cur[n] = __builtin_amdgcn_mfma_f32_16x16x32_bf16(al, bh[ks & 1][n], cur[n], 0, 0, 0);
;                 }
;                 __builtin_amdgcn_sched_barrier(0);
;             }
;             accp[0] = cur[0]; accp[1] = cur[1];
;             __syncthreads();
;         };
;         pass(0, acc[0]); pass(1, acc[1]);
	v_mfma_f32_16x16x32_bf16 v[2:5], v[28:31], v[20:23], v[2:5]
	s_waitcnt vmcnt(1)
	v_mfma_f32_16x16x32_bf16 v[6:9], v[28:31], v[24:27], v[6:9]
	v_mfma_f32_16x16x32_bf16 v[2:5], v[28:31], v[36:39], v[2:5]
	s_waitcnt vmcnt(0)
	v_mfma_f32_16x16x32_bf16 v[6:9], v[28:31], v[40:43], v[6:9]
	global_load_dwordx4 v[28:31], v[80:81], off offset:256
	global_load_dwordx4 v[36:39], v[82:83], off offset:256
	s_waitcnt lgkmcnt(0)
	v_mfma_f32_16x16x32_bf16 v[2:5], v[32:35], v[20:23], v[2:5]
	global_load_dwordx4 v[20:23], v[74:75], off offset:256
	global_load_dwordx4 v[40:43], v[76:77], off offset:256
	v_mfma_f32_16x16x32_bf16 v[6:9], v[32:35], v[24:27], v[6:9]
	v_bitop3_b32 v24, v44, v151, 16 bitop3:0x36
	v_lshl_add_u32 v194, v24, 4, v52
	ds_read_b128 v[24:27], v194
	v_add_u32_e32 v195, 0x10000, v194
	ds_read_b128 v[32:35], v195
	s_waitcnt vmcnt(3) lgkmcnt(1)
	v_mfma_f32_16x16x32_bf16 v[2:5], v[24:27], v[28:31], v[2:5]
	s_waitcnt vmcnt(1)
	v_mfma_f32_16x16x32_bf16 v[6:9], v[24:27], v[20:23], v[6:9]
	v_mfma_f32_16x16x32_bf16 v[2:5], v[24:27], v[36:39], v[2:5]
	s_waitcnt vmcnt(0)
	v_mfma_f32_16x16x32_bf16 v[6:9], v[24:27], v[40:43], v[6:9]
	global_load_dwordx4 v[24:27], v[80:81], off offset:320
	global_load_dwordx4 v[36:39], v[82:83], off offset:320
	s_waitcnt lgkmcnt(0)
	v_mfma_f32_16x16x32_bf16 v[2:5], v[32:35], v[28:31], v[2:5]
	global_load_dwordx4 v[28:31], v[74:75], off offset:320
	global_load_dwordx4 v[40:43], v[76:77], off offset:320
	v_mfma_f32_16x16x32_bf16 v[6:9], v[32:35], v[20:23], v[6:9]
	v_bitop3_b32 v20, v44, v151, 20 bitop3:0x36
	v_lshl_add_u32 v196, v20, 4, v52
	ds_read_b128 v[20:23], v196
	v_add_u32_e32 v197, 0x10000, v196
	ds_read_b128 v[32:35], v197
	s_waitcnt vmcnt(3) lgkmcnt(1)
	v_mfma_f32_16x16x32_bf16 v[2:5], v[20:23], v[24:27], v[2:5]
	s_waitcnt vmcnt(1)
	v_mfma_f32_16x16x32_bf16 v[6:9], v[20:23], v[28:31], v[6:9]
	v_mfma_f32_16x16x32_bf16 v[2:5], v[20:23], v[36:39], v[2:5]
	s_waitcnt vmcnt(0)
	v_mfma_f32_16x16x32_bf16 v[6:9], v[20:23], v[40:43], v[6:9]
	global_load_dwordx4 v[20:23], v[80:81], off offset:384
	global_load_dwordx4 v[36:39], v[82:83], off offset:384
	s_waitcnt lgkmcnt(0)
	v_mfma_f32_16x16x32_bf16 v[2:5], v[32:35], v[24:27], v[2:5]
	global_load_dwordx4 v[24:27], v[74:75], off offset:384
	global_load_dwordx4 v[40:43], v[76:77], off offset:384
	v_mfma_f32_16x16x32_bf16 v[6:9], v[32:35], v[28:31], v[6:9]
	v_bitop3_b32 v28, v44, v151, 24 bitop3:0x36
	v_lshl_add_u32 v199, v28, 4, v52
	ds_read_b128 v[28:31], v199
	v_add_u32_e32 v201, 0x10000, v199
	ds_read_b128 v[32:35], v201
	s_waitcnt vmcnt(3) lgkmcnt(1)
	v_mfma_f32_16x16x32_bf16 v[2:5], v[28:31], v[20:23], v[2:5]
	s_waitcnt vmcnt(1)
	v_mfma_f32_16x16x32_bf16 v[6:9], v[28:31], v[24:27], v[6:9]
	v_mfma_f32_16x16x32_bf16 v[2:5], v[28:31], v[36:39], v[2:5]
	s_waitcnt vmcnt(0)
	v_mfma_f32_16x16x32_bf16 v[6:9], v[28:31], v[40:43], v[6:9]
	global_load_dwordx4 v[28:31], v[80:81], off offset:448
	global_load_dwordx4 v[36:39], v[82:83], off offset:448
	s_waitcnt lgkmcnt(0)
	v_mfma_f32_16x16x32_bf16 v[2:5], v[32:35], v[20:23], v[2:5]
	global_load_dwordx4 v[20:23], v[74:75], off offset:448
	global_load_dwordx4 v[40:43], v[76:77], off offset:448
	v_mfma_f32_16x16x32_bf16 v[6:9], v[32:35], v[24:27], v[6:9]
	v_bitop3_b32 v24, v44, v151, 28 bitop3:0x36
	v_lshl_add_u32 v198, v24, 4, v52
	ds_read_b128 v[24:27], v198
	v_add_u32_e32 v200, 0x10000, v198
	ds_read_b128 v[32:35], v200
	s_waitcnt vmcnt(3) lgkmcnt(1)
	v_mfma_f32_16x16x32_bf16 v[2:5], v[24:27], v[28:31], v[2:5]
	s_waitcnt vmcnt(1)
	v_mfma_f32_16x16x32_bf16 v[6:9], v[24:27], v[20:23], v[6:9]
	v_mfma_f32_16x16x32_bf16 v[2:5], v[24:27], v[36:39], v[2:5]
	s_waitcnt vmcnt(0)
	v_mfma_f32_16x16x32_bf16 v[6:9], v[24:27], v[40:43], v[6:9]
	s_waitcnt lgkmcnt(0)
	v_mfma_f32_16x16x32_bf16 v[2:5], v[32:35], v[28:31], v[2:5]
	v_mfma_f32_16x16x32_bf16 v[6:9], v[32:35], v[20:23], v[6:9]
	v_lshlrev_b32_e32 v131, 16, v48
	v_lshlrev_b32_e32 v130, 16, v46
	v_and_b32_e32 v133, 0xffff0000, v48
	v_and_b32_e32 v132, 0xffff0000, v46
	v_lshlrev_b32_e32 v127, 16, v49
	v_lshlrev_b32_e32 v126, 16, v47
	v_and_b32_e32 v129, 0xffff0000, v49
	v_and_b32_e32 v128, 0xffff0000, v47
	v_pk_add_f32 v[20:21], v[130:131], v[132:133]
	v_pk_add_f32 v[22:23], v[126:127], v[128:129]
	v_lshlrev_b32_e32 v125, 16, v51
	v_pk_add_f32 v[20:21], v[20:21], v[22:23]
	v_lshlrev_b32_e32 v124, 16, v50
	v_add_f32_e32 v20, 0, v20
	v_add_f32_e32 v114, v20, v21
	v_and_b32_e32 v21, 0xffff0000, v51
	v_and_b32_e32 v20, 0xffff0000, v50
	v_pk_add_f32 v[22:23], v[124:125], v[20:21]
	v_lshlrev_b32_e32 v120, 16, v18
	v_and_b32_e32 v121, 0xffff0000, v18
	v_lshlrev_b32_e32 v122, 16, v19
	v_and_b32_e32 v123, 0xffff0000, v19
	v_lshlrev_b32_e32 v115, 16, v16
	v_and_b32_e32 v139, 0xffff0000, v16
	v_lshlrev_b32_e32 v119, 16, v17
	v_and_b32_e32 v117, 0xffff0000, v17
	v_pk_add_f32 v[16:17], v[22:23], v[22:23] op_sel:[0,1] op_sel_hi:[1,0]
	v_add_f32_e32 v118, v120, v121
	v_add_f32_e32 v116, v122, v123
	v_mov_b32_e32 v17, v139
	v_pk_add_f32 v[16:17], v[114:115], v[16:17]
	v_pk_add_f32 v[18:19], v[118:119], v[116:117]
	v_lshlrev_b32_e32 v113, 16, v15
	v_lshlrev_b32_e32 v112, 16, v14
	v_and_b32_e32 v15, 0xffff0000, v15
	v_and_b32_e32 v14, 0xffff0000, v14
	v_pk_add_f32 v[16:17], v[16:17], v[18:19]
	v_pk_add_f32 v[18:19], v[112:113], v[14:15]
	v_lshlrev_b32_e32 v108, 16, v12
	v_and_b32_e32 v109, 0xffff0000, v12
	v_lshlrev_b32_e32 v110, 16, v13
	v_and_b32_e32 v111, 0xffff0000, v13
	v_lshlrev_b32_e32 v136, 16, v10
	v_and_b32_e32 v137, 0xffff0000, v10
	v_lshlrev_b32_e32 v107, 16, v11
	v_and_b32_e32 v105, 0xffff0000, v11
	v_pk_add_f32 v[10:11], v[16:17], v[16:17] op_sel:[0,1] op_sel_hi:[1,0]
	v_pk_add_f32 v[12:13], v[18:19], v[18:19] op_sel:[0,1] op_sel_hi:[1,0]
	v_add_f32_e32 v106, v108, v109
	v_add_f32_e32 v104, v110, v111
	v_mov_b32_e32 v11, v136
	v_mov_b32_e32 v13, v137
	v_pk_add_f32 v[10:11], v[10:11], v[12:13]
	v_pk_add_f32 v[12:13], v[106:107], v[104:105]
	s_nop 0
	v_pk_add_f32 v[10:11], v[10:11], v[12:13]
	s_barrier
; __device__ __forceinline__ float bf_lo(unsigned w) { return __uint_as_float(w << 16); }
; __device__ __forceinline__ float bf_hi(unsigned w) { return __uint_as_float(w & 0xffff0000u); }
; __device__ __forceinline__ void p6_router(Frame& F) {
;     ...
;             for (int j = 0; j < 8; ++j) { pw[j] = ((const f32x4*)F.in[I_LN1W])[lop + 64 * j]; pb[j] = ((const f32x4*)F.in[I_LN1B])[lop + 64 * j]; }
; #pragma unroll
;             for (int q = 0; q < 2; ++q) {
;                 const int t = ta + q; f32x4 v[8]; float s = 0.f;
; #pragma unroll
;                 for (int j = 0; j < 8; ++j) { const u32x2 zb = zr[q][j]; v[j] = (f32x4){bf_lo(zb.x), bf_hi(zb.x), bf_lo(zb.y), bf_hi(zb.y)}; s += (v[j][0] + v[j][1]) + (v[j][2] + v[j][3]); }
;                 float mean = wave_sum(s) * (1.f / DM), s2 = 0.f;
; #pragma unroll
;                 for (int j = 0; j < 8; ++j) { v[j] = v[j] - mean; s2 += (v[j][0] * v[j][0] + v[j][1] * v[j][1]) + (v[j][2] * v[j][2] + v[j][3] * v[j][3]); }
;                 float rstd = 1.f / sqrtf(wave_sum(s2) * (1.f / DM) + LN_EPS);
	v_add_f32_e32 v10, v10, v11
	s_nop 1
	v_mov_b32_dpp v11, v10 quad_perm:[1,0,3,2] row_mask:0xf bank_mask:0xf
	s_waitcnt lgkmcnt(0)
	v_and_b32_e32 v215, 0xffff0000, v93
	v_and_b32_e32 v214, 0xffff0000, v92
	v_add_f32_e32 v10, v10, v11
	s_nop 1
	v_mov_b32_dpp v11, v10 quad_perm:[2,3,0,1] row_mask:0xf bank_mask:0xf
	s_waitcnt lgkmcnt(0)
	v_add_f32_e32 v10, v10, v11
	s_nop 1
	v_mov_b32_dpp v11, v10 row_shl:4 row_mask:0xf bank_mask:0x5
	s_nop 1
	v_mov_b32_dpp v11, v10 row_shr:4 row_mask:0xf bank_mask:0xa
	s_waitcnt lgkmcnt(0)
	v_add_f32_e32 v10, v10, v11
	s_nop 1
	v_mov_b32_dpp v11, v10 row_ror:8 row_mask:0xf bank_mask:0xf
	s_waitcnt lgkmcnt(0)
	v_add_f32_e32 v12, v10, v11
	v_mov_b32_e32 v13, v12
	s_nop 1
	v_permlane16_swap_b32_e32 v13, v12
	v_mov_b32_e32 v10, v170
	s_waitcnt lgkmcnt(0)
	v_add_f32_e32 v22, v12, v13
	v_mov_b32_e32 v23, v22
	s_nop 1
	v_permlane32_swap_b32_e32 v23, v22
	v_ashrrev_i32_e32 v11, 31, v10
	v_lshlrev_b64 v[10:11], 4, v[10:11]
	v_lshl_add_u64 v[18:19], s[10:11], 0, v[10:11]
	v_lshl_add_u64 v[16:17], s[8:9], 0, v[10:11]
	s_waitcnt lgkmcnt(0)
	v_add_f32_e32 v28, v22, v23
	v_fmac_f32_e32 v128, 0xba000000, v28
	v_fmac_f32_e32 v132, 0xba000000, v28
	v_fmac_f32_e32 v129, 0xba000000, v28
	v_fmac_f32_e32 v133, 0xba000000, v28
	v_fmac_f32_e32 v126, 0xba000000, v28
	v_fmac_f32_e32 v130, 0xba000000, v28
	v_fmac_f32_e32 v127, 0xba000000, v28
	v_fmac_f32_e32 v131, 0xba000000, v28
	v_pk_mul_f32 v[22:23], v[132:133], v[132:133]
	v_pk_mul_f32 v[24:25], v[128:129], v[128:129]
	v_fmac_f32_e32 v20, 0xba000000, v28
	v_fmac_f32_e32 v21, 0xba000000, v28
	v_fmac_f32_e32 v125, 0xba000000, v28
	v_pk_fma_f32 v[22:23], v[130:131], v[130:131], v[22:23]
	v_pk_fma_f32 v[24:25], v[126:127], v[126:127], v[24:25]
	v_fmac_f32_e32 v124, 0xba000000, v28
	v_mov_b32_e32 v202, v125
	v_mov_b32_e32 v203, v21
	v_mov_b32_e32 v125, v20
	v_pk_add_f32 v[22:23], v[22:23], v[24:25]
	v_pk_mul_f32 v[24:25], v[202:203], v[202:203]
	v_pk_mul_f32 v[20:21], v[124:125], v[124:125]
	v_fmac_f32_e32 v120, 0xba000000, v28
	v_pk_mov_b32 v[26:27], v[20:21], v[24:25] op_sel:[1,0]
	v_mov_b32_e32 v21, v25
	v_pk_add_f32 v[20:21], v[26:27], v[20:21]
	v_fmac_f32_e32 v121, 0xba000000, v28
	v_pk_add_f32 v[20:21], v[20:21], v[20:21] op_sel_hi:[0,1]
	v_fmac_f32_e32 v122, 0xba000000, v28
	v_mul_f32_e32 v20, v120, v120
	v_fmac_f32_e32 v123, 0xba000000, v28
	v_pk_fma_f32 v[24:25], v[120:121], v[120:121], v[20:21] op_sel_hi:[1,1,0]
	v_mul_f32_e32 v20, v122, v122
	v_pk_add_f32 v[22:23], v[22:23], v[22:23] op_sel_hi:[0,1]
	v_pk_fma_f32 v[26:27], v[122:123], v[122:123], v[20:21] op_sel_hi:[1,1,0]
	v_fmac_f32_e32 v117, 0xba000000, v28
	v_fmac_f32_e32 v119, 0xba000000, v28
	v_fmac_f32_e32 v139, 0xba000000, v28
	v_fmac_f32_e32 v115, 0xba000000, v28
	v_fmac_f32_e32 v14, 0xba000000, v28
	v_fmac_f32_e32 v15, 0xba000000, v28
	v_fmac_f32_e32 v113, 0xba000000, v28
	v_mul_f32_e32 v24, v115, v115
	v_mul_f32_e32 v26, v139, v139
	v_mul_f32_e32 v20, v119, v119
	v_mul_f32_e32 v22, v117, v117
	v_fmac_f32_e32 v112, 0xba000000, v28
	v_mov_b32_e32 v140, v113
	v_mov_b32_e32 v141, v15
	v_mov_b32_e32 v113, v14
	v_pk_add_f32 v[24:25], v[24:25], v[26:27]
	v_pk_add_f32 v[20:21], v[20:21], v[22:23]
	v_pk_mul_f32 v[22:23], v[140:141], v[140:141]
	v_pk_mul_f32 v[14:15], v[112:113], v[112:113]
	v_pk_add_f32 v[20:21], v[24:25], v[20:21]
	v_pk_mov_b32 v[24:25], v[14:15], v[22:23] op_sel:[1,0]
	v_mov_b32_e32 v15, v23
	v_pk_add_f32 v[14:15], v[24:25], v[14:15]
	v_fmac_f32_e32 v108, 0xba000000, v28
	v_pk_add_f32 v[14:15], v[14:15], v[14:15] op_sel_hi:[0,1]
	v_fmac_f32_e32 v109, 0xba000000, v28
	v_fmac_f32_e32 v110, 0xba000000, v28
	v_mul_f32_e32 v14, v108, v108
	v_fmac_f32_e32 v111, 0xba000000, v28
	v_pk_fma_f32 v[22:23], v[108:109], v[108:109], v[14:15] op_sel_hi:[1,1,0]
	v_mul_f32_e32 v14, v110, v110
	v_pk_add_f32 v[20:21], v[20:21], v[20:21] op_sel_hi:[0,1]
	v_pk_fma_f32 v[24:25], v[110:111], v[110:111], v[14:15] op_sel_hi:[1,1,0]
	v_fmac_f32_e32 v105, 0xba000000, v28
	v_fmac_f32_e32 v107, 0xba000000, v28
	v_fmac_f32_e32 v137, 0xba000000, v28
	v_fmac_f32_e32 v136, 0xba000000, v28
	v_mul_f32_e32 v22, v136, v136
	v_mul_f32_e32 v24, v137, v137
	v_mul_f32_e32 v14, v107, v107
	v_mul_f32_e32 v20, v105, v105
	v_pk_add_f32 v[22:23], v[22:23], v[24:25]
	v_pk_add_f32 v[14:15], v[14:15], v[20:21]
	global_load_dwordx4 v[10:13], v[18:19], off
	v_pk_add_f32 v[14:15], v[22:23], v[14:15]
	global_load_dwordx4 v[70:73], v[16:17], off
	global_load_dwordx4 v[62:65], v[16:17], off offset:1024
	global_load_dwordx4 v[66:69], v[18:19], off offset:1024
	v_add_f32_e32 v14, v14, v15
	s_nop 1
	v_mov_b32_dpp v15, v14 quad_perm:[1,0,3,2] row_mask:0xf bank_mask:0xf
	global_load_dwordx4 v[54:57], v[16:17], off offset:2048
	global_load_dwordx4 v[46:49], v[16:17], off offset:3072
	global_load_dwordx4 v[58:61], v[18:19], off offset:2048
	global_load_dwordx4 v[50:53], v[18:19], off offset:3072
	v_mov_b32_e32 v206, v127
	v_mov_b32_e32 v127, v128
	v_mov_b32_e32 v204, v131
	s_waitcnt lgkmcnt(0)
	v_add_f32_e32 v14, v14, v15
	s_nop 1
	v_mov_b32_dpp v15, v14 quad_perm:[2,3,0,1] row_mask:0xf bank_mask:0xf
	v_mov_b32_e32 v205, v133
	v_mov_b32_e32 v131, v132
	v_mov_b32_e32 v207, v129
	v_mov_b32_e32 v138, v115
	s_waitcnt lgkmcnt(0)
	v_add_f32_e32 v20, v14, v15
	s_nop 1
	v_mov_b32_dpp v21, v20 row_shl:4 row_mask:0xf bank_mask:0x5
	s_nop 1
	v_mov_b32_dpp v21, v20 row_shr:4 row_mask:0xf bank_mask:0xa
	v_add_co_u32_e32 v14, vcc, s41, v16
	s_add_i32 s8, s4, 2
	s_nop 0
	v_addc_co_u32_e32 v15, vcc, 0, v17, vcc
	s_waitcnt lgkmcnt(0)
; __device__ __forceinline__ unsigned cvt_pk_bf16(float lo, float hi) { unsigned r; asm volatile("v_cvt_pk_bf16_f32 %0, %1, %2" : "=v"(r) : "v"(lo), "v"(hi)); return r; }
; __device__ __forceinline__ void p6_router(Frame& F) {
;     ...
;                 float rstd = 1.f / sqrtf(wave_sum(s2) * (1.f / DM) + LN_EPS);
;                 s = 0.f;
; #pragma unroll
;                 for (int j = 0; j < 8; ++j) { v[j] = v[j] * rstd * pw[j] + pb[j]; { u32x2 xb; xb.x = cvt_pk_bf16(v[j][0], v[j][1]); xb.y = cvt_pk_bf16(v[j][2], v[j][3]); ((u32x2*)(X1 + (size_t)t * DM))[lane + 64 * j] = xb; } s += (v[j][0] + v[j][1]) + (v[j][2] + v[j][3]); }
;                 mean = wave_sum(s) * (1.f / DM); s2 = 0.f;
	v_add_f32_e32 v16, v20, v21
	s_nop 1
	v_mov_b32_dpp v17, v16 row_ror:8 row_mask:0xf bank_mask:0xf
	v_add_co_u32_e32 v18, vcc, s41, v18
	global_load_dwordx4 v[38:41], v[14:15], off
	global_load_dwordx4 v[30:33], v[14:15], off offset:1024
	v_addc_co_u32_e32 v19, vcc, 0, v19, vcc
	s_waitcnt lgkmcnt(0)
	v_add_f32_e32 v20, v16, v17
	v_mov_b32_e32 v21, v20
	s_nop 1
	v_permlane16_swap_b32_e32 v21, v20
	global_load_dwordx4 v[42:45], v[18:19], off
	global_load_dwordx4 v[34:37], v[18:19], off offset:1024
	global_load_dwordx4 v[22:25], v[14:15], off offset:2048
	s_nop 0
	global_load_dwordx4 v[14:17], v[14:15], off offset:3072
	s_ashr_i32 s9, s8, 31
	s_waitcnt lgkmcnt(0)
	v_add_f32_e32 v78, v20, v21
	global_load_dwordx4 v[26:29], v[18:19], off offset:2048
	s_nop 0
	global_load_dwordx4 v[18:21], v[18:19], off offset:3072
	v_mov_b32_e32 v104, v78
	s_nop 1
	v_permlane32_swap_b32_e32 v104, v78
	s_waitcnt lgkmcnt(0)
	v_add_f32_e32 v78, v78, v104
	v_fmamk_f32 v78, v78, 0x3a000000, v148
	v_mul_f32_e32 v104, 0x4f800000, v78
	v_cmp_gt_f32_e32 vcc, s45, v78
	s_nop 1
	v_cndmask_b32_e32 v78, v78, v104, vcc
	v_sqrt_f32_e32 v104, v78
	s_nop 0
	v_add_u32_e32 v106, -1, v104
	v_fma_f32 v114, -v106, v104, v78
	v_cmp_ge_f32_e64 s[0:1], 0, v114
	v_add_u32_e32 v114, 1, v104
	s_nop 0
	v_cndmask_b32_e64 v106, v104, v106, s[0:1]
	v_fma_f32 v104, -v114, v104, v78
	v_cmp_lt_f32_e64 s[0:1], 0, v104
	s_nop 1
	v_cndmask_b32_e64 v104, v106, v114, s[0:1]
	v_mul_f32_e32 v106, 0x37800000, v104
	v_cndmask_b32_e32 v104, v104, v106, vcc
	v_cmp_class_f32_e32 vcc, v78, v149
	s_nop 1
	v_cndmask_b32_e32 v78, v104, v78, vcc
	v_div_scale_f32 v104, s[0:1], v78, v78, 1.0
	v_rcp_f32_e32 v106, v104
	s_lshl_b64 s[0:1], s[8:9], 12
	s_add_u32 s0, s42, s0
	s_addc_u32 s1, s43, s1
	v_fma_f32 v114, -v104, v106, 1.0
	v_fmac_f32_e32 v106, v114, v106
	v_div_scale_f32 v114, vcc, 1.0, v78, 1.0
	v_mul_f32_e32 v116, v114, v106
	v_fma_f32 v118, -v104, v116, v114
	v_fmac_f32_e32 v116, v118, v106
	v_fma_f32 v104, -v104, v116, v114
	v_div_fmas_f32 v104, v104, v106, v116
	v_div_fixup_f32 v78, v104, v78, 1.0
	v_pk_mul_f32 v[126:127], v[126:127], v[78:79] op_sel_hi:[1,0]
	v_pk_mul_f32 v[128:129], v[130:131], v[78:79] op_sel_hi:[1,0]
	s_waitcnt vmcnt(14)
	v_pk_fma_f32 v[132:133], v[72:73], v[126:127], v[12:13]
	v_pk_mul_f32 v[126:127], v[204:205], v[78:79] op_sel_hi:[1,0]
	v_pk_fma_f32 v[134:135], v[70:71], v[128:129], v[10:11]
	v_pk_mul_f32 v[128:129], v[206:207], v[78:79] op_sel_hi:[1,0]
	s_waitcnt vmcnt(12)
	v_pk_fma_f32 v[130:131], v[62:63], v[126:127], v[66:67]
	v_pk_fma_f32 v[128:129], v[64:65], v[128:129], v[68:69]
	v_mov_b32_e32 v126, v130
	v_mov_b32_e32 v127, v134
	v_mov_b32_e32 v204, v131
	v_mov_b32_e32 v205, v135
	v_pk_add_f32 v[126:127], v[126:127], v[204:205]
	v_mov_b32_e32 v204, v129
	v_mov_b32_e32 v205, v133
	v_mov_b32_e32 v206, v128
	v_mov_b32_e32 v207, v132
	v_pk_add_f32 v[204:205], v[204:205], v[206:207]
	v_mov_b32_e32 v116, v119
	v_pk_add_f32 v[126:127], v[126:127], v[204:205]
	v_pk_mul_f32 v[114:115], v[138:139], v[78:79] op_sel_hi:[1,0]
	v_add_f32_e32 v104, 0, v127
	v_add_f32_e32 v205, v126, v104
	v_pk_mul_f32 v[126:127], v[124:125], v[78:79] op_sel_hi:[1,0]
	v_pk_mul_f32 v[124:125], v[202:203], v[78:79] op_sel_hi:[1,0]
	s_waitcnt vmcnt(9)
	v_pk_fma_f32 v[126:127], v[54:55], v[126:127], v[58:59]
	v_pk_fma_f32 v[124:125], v[56:57], v[124:125], v[60:61]
	v_mov_b32_e32 v202, v126
	v_mov_b32_e32 v203, v125
	v_pk_mov_b32 v[206:207], v[126:127], v[124:125] op_sel:[1,0]
	v_pk_mul_f32 v[116:117], v[116:117], v[78:79] op_sel_hi:[1,0]
	v_pk_add_f32 v[202:203], v[202:203], v[206:207]
	v_pk_mul_f32 v[206:207], v[120:121], v[78:79] op_sel_hi:[1,0]
	v_pk_mul_f32 v[120:121], v[122:123], v[78:79] op_sel_hi:[1,0]
	v_pk_add_f32 v[202:203], v[202:203], v[202:203] op_sel_hi:[0,1]
	s_waitcnt vmcnt(8)
	v_pk_fma_f32 v[120:121], v[48:49], v[120:121], v[52:53]
	v_pk_fma_f32 v[122:123], v[46:47], v[206:207], v[50:51]
	s_waitcnt vmcnt(5)
	v_pk_fma_f32 v[116:117], v[40:41], v[116:117], v[44:45]
	v_pk_fma_f32 v[118:119], v[38:39], v[114:115], v[42:43]
	v_add_f32_e32 v207, v122, v123
	v_add_f32_e32 v211, v121, v120
	v_mov_b32_e32 v206, v118
	v_mov_b32_e32 v210, v119
	v_mov_b32_e32 v202, v117
	v_mov_b32_e32 v204, v116
	v_pk_add_f32 v[114:115], v[206:207], v[210:211]
	v_pk_add_f32 v[138:139], v[202:203], v[204:205]
	v_mov_b32_e32 v104, v107
	v_pk_add_f32 v[114:115], v[114:115], v[138:139]
	v_pk_mul_f32 v[136:137], v[136:137], v[78:79] op_sel_hi:[1,0]
	v_pk_add_f32 v[138:139], v[114:115], v[114:115] op_sel_hi:[0,1]
	v_pk_mul_f32 v[114:115], v[112:113], v[78:79] op_sel_hi:[1,0]
	v_pk_mul_f32 v[112:113], v[140:141], v[78:79] op_sel_hi:[1,0]
	s_waitcnt vmcnt(4)
	v_pk_fma_f32 v[114:115], v[30:31], v[114:115], v[34:35]
	v_pk_fma_f32 v[112:113], v[32:33], v[112:113], v[36:37]
	v_mov_b32_e32 v140, v114
	v_mov_b32_e32 v141, v113
	v_pk_mov_b32 v[202:203], v[114:115], v[112:113] op_sel:[1,0]
	v_pk_mul_f32 v[104:105], v[104:105], v[78:79] op_sel_hi:[1,0]
	v_pk_add_f32 v[140:141], v[140:141], v[202:203]
	v_pk_mul_f32 v[202:203], v[108:109], v[78:79] op_sel_hi:[1,0]
	v_pk_mul_f32 v[108:109], v[110:111], v[78:79] op_sel_hi:[1,0]
	v_pk_add_f32 v[140:141], v[140:141], v[140:141] op_sel_hi:[0,1]
	s_waitcnt vmcnt(1)
	v_pk_fma_f32 v[108:109], v[24:25], v[108:109], v[28:29]
	v_pk_fma_f32 v[110:111], v[22:23], v[202:203], v[26:27]
	s_waitcnt vmcnt(0)
; __device__ __forceinline__ unsigned cvt_pk_bf16(float lo, float hi) { unsigned r; asm volatile("v_cvt_pk_bf16_f32 %0, %1, %2" : "=v"(r) : "v"(lo), "v"(hi)); return r; }
; __device__ __forceinline__ void p6_router(Frame& F) {
;     ...
;                 for (int j = 0; j < 8; ++j) { v[j] = v[j] * rstd * pw[j] + pb[j]; { u32x2 xb; xb.x = cvt_pk_bf16(v[j][0], v[j][1]); xb.y = cvt_pk_bf16(v[j][2], v[j][3]); ((u32x2*)(X1 + (size_t)t * DM))[lane + 64 * j] = xb; } s += (v[j][0] + v[j][1]) + (v[j][2] + v[j][3]); }
;                 mean = wave_sum(s) * (1.f / DM); s2 = 0.f;
; #pragma unroll
;                 for (int j = 0; j < 8; ++j) { v[j] = v[j] - mean; s2 += (v[j][0] * v[j][0] + v[j][1] * v[j][1]) + (v[j][2] * v[j][2] + v[j][3] * v[j][3]); }
;                 rstd = 1.f / sqrtf(wave_sum(s2) * (1.f / DM) + LN_EPS);
;                 int loq = lane; asm volatile("" : "+v"(loq));
; #pragma unroll
;                 for (int j = 0; j < 8; ++j) { const f32x4 sh = ((const f32x4*)(mod + (size_t)b * 12288 + 6144))[loq + 64 * j], sc = ((const f32x4*)(mod + (size_t)b * 12288 + 8192))[loq + 64 * j];
	v_pk_fma_f32 v[104:105], v[16:17], v[104:105], v[20:21]
	v_pk_fma_f32 v[106:107], v[14:15], v[136:137], v[18:19]
	v_add_f32_e32 v203, v110, v111
	v_add_f32_e32 v205, v109, v108
	v_mov_b32_e32 v202, v106
	v_mov_b32_e32 v204, v107
	v_mov_b32_e32 v140, v105
	v_mov_b32_e32 v138, v104
	v_pk_add_f32 v[136:137], v[202:203], v[204:205]
	v_pk_add_f32 v[138:139], v[140:141], v[138:139]
	v_cvt_pk_bf16_f32 v208, v134, v135
	v_cvt_pk_bf16_f32 v209, v132, v133
	global_store_dwordx2 v146, v[208:209], s[0:1]
	v_pk_add_f32 v[136:137], v[136:137], v[138:139]
	s_nop 0
	v_add_f32_e32 v78, v136, v137
	s_nop 1
	v_mov_b32_dpp v137, v78 quad_perm:[1,0,3,2] row_mask:0xf bank_mask:0xf
	v_cvt_pk_bf16_f32 v136, v130, v131
	s_waitcnt lgkmcnt(0)
	v_add_f32_e32 v78, v78, v137
	s_nop 1
	v_mov_b32_dpp v138, v78 quad_perm:[2,3,0,1] row_mask:0xf bank_mask:0xf
	v_cvt_pk_bf16_f32 v137, v128, v129
	global_store_dwordx2 v146, v[136:137], s[0:1] offset:512
	v_cvt_pk_bf16_f32 v136, v126, v127
	v_cvt_pk_bf16_f32 v137, v124, v125
	s_waitcnt lgkmcnt(0)
	v_add_f32_e32 v78, v78, v138
	s_nop 1
	v_mov_b32_dpp v138, v78 row_shl:4 row_mask:0xf bank_mask:0x5
	s_nop 1
	v_mov_b32_dpp v138, v78 row_shr:4 row_mask:0xf bank_mask:0xa
	global_store_dwordx2 v146, v[136:137], s[0:1] offset:1024
	v_cvt_pk_bf16_f32 v136, v122, v123
	v_cvt_pk_bf16_f32 v137, v120, v121
	global_store_dwordx2 v146, v[136:137], s[0:1] offset:1536
	s_waitcnt lgkmcnt(0)
	v_add_f32_e32 v78, v78, v138
	s_nop 1
	v_mov_b32_dpp v138, v78 row_ror:8 row_mask:0xf bank_mask:0xf
	v_cvt_pk_bf16_f32 v136, v118, v119
	v_cvt_pk_bf16_f32 v137, v116, v117
	global_store_dwordx2 v146, v[136:137], s[0:1] offset:2048
	v_cvt_pk_bf16_f32 v136, v114, v115
	s_waitcnt lgkmcnt(0)
	v_add_f32_e32 v78, v78, v138
	v_mov_b32_e32 v138, v78
	s_nop 1
	v_permlane16_swap_b32_e32 v138, v78
	v_cvt_pk_bf16_f32 v137, v112, v113
	global_store_dwordx2 v146, v[136:137], s[0:1] offset:2560
	v_cvt_pk_bf16_f32 v136, v110, v111
	v_cvt_pk_bf16_f32 v137, v108, v109
	s_waitcnt lgkmcnt(0)
	v_add_f32_e32 v78, v78, v138
	v_mov_b32_e32 v138, v78
	s_nop 1
	v_permlane32_swap_b32_e32 v138, v78
	global_store_dwordx2 v146, v[136:137], s[0:1] offset:3072
	v_cvt_pk_bf16_f32 v136, v106, v107
	v_cvt_pk_bf16_f32 v137, v104, v105
	global_store_dwordx2 v146, v[136:137], s[0:1] offset:3584
	s_waitcnt lgkmcnt(0)
	v_add_f32_e32 v204, v78, v138
	v_fmamk_f32 v135, v204, 0xba000000, v135
	v_fmamk_f32 v131, v204, 0xba000000, v131
	v_fmamk_f32 v133, v204, 0xba000000, v133
	v_fmac_f32_e32 v134, 0xba000000, v204
	v_fmamk_f32 v129, v204, 0xba000000, v129
	v_fmac_f32_e32 v130, 0xba000000, v204
	v_mov_b32_e32 v138, v135
	v_mov_b32_e32 v139, v131
	v_fmac_f32_e32 v132, 0xba000000, v204
	v_fmac_f32_e32 v128, 0xba000000, v204
	v_mov_b32_e32 v136, v134
	v_mov_b32_e32 v137, v130
	v_pk_mul_f32 v[138:139], v[138:139], v[138:139]
	v_mov_b32_e32 v140, v133
	v_mov_b32_e32 v141, v129
	v_pk_fma_f32 v[136:137], v[136:137], v[136:137], v[138:139]
	v_mov_b32_e32 v138, v132
	v_mov_b32_e32 v139, v128
	v_pk_mul_f32 v[140:141], v[140:141], v[140:141]
	v_fmamk_f32 v127, v204, 0xba000000, v127
	v_pk_fma_f32 v[138:139], v[138:139], v[138:139], v[140:141]
	v_fmac_f32_e32 v126, 0xba000000, v204
	v_fmamk_f32 v125, v204, 0xba000000, v125
	v_fmac_f32_e32 v124, 0xba000000, v204
	v_pk_add_f32 v[136:137], v[136:137], v[138:139]
	v_pk_mul_f32 v[138:139], v[124:125], v[124:125]
	v_pk_mul_f32 v[140:141], v[126:127], v[126:127]
	v_fmac_f32_e32 v122, 0xba000000, v204
	v_pk_mov_b32 v[202:203], v[140:141], v[138:139] op_sel:[1,0]
	v_mov_b32_e32 v141, v139
	v_fmamk_f32 v123, v204, 0xba000000, v123
	v_fmac_f32_e32 v120, 0xba000000, v204
	v_mul_f32_e32 v78, v122, v122
	v_pk_add_f32 v[138:139], v[202:203], v[140:141]
	v_fmamk_f32 v121, v204, 0xba000000, v121
	v_pk_fma_f32 v[140:141], v[122:123], v[122:123], v[78:79] op_sel_hi:[1,1,0]
	v_mul_f32_e32 v78, v120, v120
	v_pk_add_f32 v[136:137], v[136:137], v[136:137] op_sel_hi:[0,1]
	v_pk_add_f32 v[138:139], v[138:139], v[138:139] op_sel_hi:[0,1]
	v_pk_fma_f32 v[202:203], v[120:121], v[120:121], v[78:79] op_sel_hi:[1,1,0]
	v_fmamk_f32 v117, v204, 0xba000000, v117
	v_fmac_f32_e32 v116, 0xba000000, v204
	v_fmamk_f32 v119, v204, 0xba000000, v119
	v_fmac_f32_e32 v118, 0xba000000, v204
	v_mul_f32_e32 v140, v118, v118
	v_mul_f32_e32 v202, v119, v119
	v_mul_f32_e32 v138, v116, v116
	v_mul_f32_e32 v136, v117, v117
	v_pk_add_f32 v[140:141], v[140:141], v[202:203]
	v_pk_add_f32 v[136:137], v[138:139], v[136:137]
	v_fmamk_f32 v115, v204, 0xba000000, v115
	v_pk_add_f32 v[136:137], v[140:141], v[136:137]
	v_fmac_f32_e32 v114, 0xba000000, v204
	v_fmamk_f32 v113, v204, 0xba000000, v113
	v_fmac_f32_e32 v112, 0xba000000, v204
	v_pk_add_f32 v[140:141], v[136:137], v[136:137] op_sel_hi:[0,1]
	v_pk_mul_f32 v[136:137], v[112:113], v[112:113]
	v_pk_mul_f32 v[138:139], v[114:115], v[114:115]
	v_fmac_f32_e32 v110, 0xba000000, v204
	v_pk_mov_b32 v[202:203], v[138:139], v[136:137] op_sel:[1,0]
	v_mov_b32_e32 v139, v137
	v_pk_add_f32 v[136:137], v[202:203], v[138:139]
	v_fmamk_f32 v111, v204, 0xba000000, v111
	v_fmac_f32_e32 v108, 0xba000000, v204
	v_mul_f32_e32 v78, v110, v110
	v_pk_add_f32 v[206:207], v[136:137], v[136:137] op_sel_hi:[0,1]
	v_fmamk_f32 v109, v204, 0xba000000, v109
	v_pk_fma_f32 v[136:137], v[110:111], v[110:111], v[78:79] op_sel_hi:[1,1,0]
	v_mul_f32_e32 v78, v108, v108
	v_pk_fma_f32 v[138:139], v[108:109], v[108:109], v[78:79] op_sel_hi:[1,1,0]
	v_fmamk_f32 v107, v204, 0xba000000, v107
	v_fmac_f32_e32 v106, 0xba000000, v204
	v_mul_f32_e32 v136, v106, v106
	v_mul_f32_e32 v138, v107, v107
	v_pk_add_f32 v[208:209], v[136:137], v[138:139]
	v_mov_b32_e32 v136, v170
	v_fmamk_f32 v105, v204, 0xba000000, v105
	v_ashrrev_i32_e32 v137, 31, v136
	v_lshlrev_b64 v[136:137], 4, v[136:137]
	v_lshl_add_u64 v[210:211], s[16:17], 0, v[136:137]
	v_fmac_f32_e32 v104, 0xba000000, v204
	v_lshl_add_u64 v[212:213], s[20:21], 0, v[136:137]
	global_load_dwordx4 v[136:139], v[210:211], off
	global_load_dwordx4 v[202:205], v[212:213], off
	v_mul_f32_e32 v206, v104, v104
	v_mul_f32_e32 v140, v105, v105
	v_pk_add_f32 v[140:141], v[206:207], v[140:141]
	s_waitcnt vmcnt(0)
; #define LAS __attribute__((address_space(3)))
; __device__ __forceinline__ unsigned cvt_pk_bf16(float lo, float hi) { unsigned r; asm volatile("v_cvt_pk_bf16_f32 %0, %1, %2" : "=v"(r) : "v"(lo), "v"(hi)); return r; }
; __device__ __forceinline__ unsigned pk4_fp8(float a, float b, float c, float d) { int w = 0; w = __builtin_amdgcn_cvt_pk_fp8_f32(a, b, w, false); w = __builtin_amdgcn_cvt_pk_fp8_f32(c, d, w, true); return (unsigned)w; }
; __device__ __forceinline__ float bf_lo(unsigned w) { return __uint_as_float(w << 16); }
; __device__ __forceinline__ float bf_hi(unsigned w) { return __uint_as_float(w & 0xffff0000u); }
; __device__ __forceinline__ void p6_router(Frame& F) {
;     ...
;                 rstd = 1.f / sqrtf(wave_sum(s2) * (1.f / DM) + LN_EPS);
;                 int loq = lane; asm volatile("" : "+v"(loq));
; #pragma unroll
;                 for (int j = 0; j < 8; ++j) { const f32x4 sh = ((const f32x4*)(mod + (size_t)b * 12288 + 6144))[loq + 64 * j], sc = ((const f32x4*)(mod + (size_t)b * 12288 + 8192))[loq + 64 * j];
;                     const f32x4 y = v[j] * rstd * (sc + 1.0f) + sh;
;                     u32x2 wh; wh.x = cvt_pk_bf16(y[0], y[1]); wh.y = cvt_pk_bf16(y[2], y[3]);
;                     const f32x4 yl = {y[0] - bf_lo(wh.x), y[1] - bf_hi(wh.x), y[2] - bf_lo(wh.y), y[3] - bf_hi(wh.y)};
;                     u32x2 wl; wl.x = cvt_pk_bf16(yl[0], yl[1]); wl.y = cvt_pk_bf16(yl[2], yl[3]);
;                     { const int r = 2 * wave + q; LAS unsigned char* rowp = F.lds + r * 4096 + ((((lane >> 1) + 32 * j) ^ r) << 4) + (lane & 1) * 8;
;                       *(LAS u32x2*)rowp = wh; *(LAS u32x2*)(rowp + 65536) = wl; }
;                     U2F[(size_t)t * (DM / 4) + lane + 64 * j] = pk4_fp8(y[0], y[1], y[2], y[3]); }
	v_pk_add_f32 v[202:203], v[202:203], 1.0 op_sel_hi:[1,0]
	v_pk_add_f32 v[140:141], v[208:209], v[140:141]
	s_nop 0
	v_add_f32_e32 v78, v140, v141
	s_nop 1
	v_mov_b32_dpp v140, v78 quad_perm:[1,0,3,2] row_mask:0xf bank_mask:0xf
	s_waitcnt lgkmcnt(0)
	v_add_f32_e32 v78, v78, v140
	s_nop 1
	v_mov_b32_dpp v140, v78 quad_perm:[2,3,0,1] row_mask:0xf bank_mask:0xf
	s_waitcnt lgkmcnt(0)
	v_add_f32_e32 v78, v78, v140
	s_nop 1
	v_mov_b32_dpp v140, v78 row_shl:4 row_mask:0xf bank_mask:0x5
	s_nop 1
	v_mov_b32_dpp v140, v78 row_shr:4 row_mask:0xf bank_mask:0xa
	s_waitcnt lgkmcnt(0)
	v_add_f32_e32 v78, v78, v140
	s_nop 1
	v_mov_b32_dpp v140, v78 row_ror:8 row_mask:0xf bank_mask:0xf
	s_waitcnt lgkmcnt(0)
	v_add_f32_e32 v78, v78, v140
	v_mov_b32_e32 v140, v78
	s_nop 1
	v_permlane16_swap_b32_e32 v140, v78
	s_waitcnt lgkmcnt(0)
	v_add_f32_e32 v78, v78, v140
	v_mov_b32_e32 v140, v78
	s_nop 1
	v_permlane32_swap_b32_e32 v140, v78
	s_waitcnt lgkmcnt(0)
	v_add_f32_e32 v78, v78, v140
	v_fmamk_f32 v78, v78, 0x3a000000, v148
	v_mul_f32_e32 v140, 0x4f800000, v78
	v_cmp_gt_f32_e32 vcc, s45, v78
	s_nop 1
	v_cndmask_b32_e32 v78, v78, v140, vcc
	v_sqrt_f32_e32 v140, v78
	s_nop 0
	v_add_u32_e32 v141, -1, v140
	v_fma_f32 v206, -v141, v140, v78
	v_cmp_ge_f32_e64 s[0:1], 0, v206
	v_add_u32_e32 v206, 1, v140
	s_nop 0
	v_cndmask_b32_e64 v141, v140, v141, s[0:1]
	v_fma_f32 v140, -v206, v140, v78
	v_cmp_lt_f32_e64 s[0:1], 0, v140
	s_nop 1
	v_cndmask_b32_e64 v140, v141, v206, s[0:1]
	v_mul_f32_e32 v141, 0x37800000, v140
	v_cndmask_b32_e32 v140, v140, v141, vcc
	v_cmp_class_f32_e32 vcc, v78, v149
	s_nop 1
	v_cndmask_b32_e32 v78, v140, v78, vcc
	v_div_scale_f32 v140, s[0:1], v78, v78, 1.0
	v_rcp_f32_e32 v141, v140
	s_lshl_b64 s[0:1], s[8:9], 11
	s_add_u32 s8, s40, s0
	s_addc_u32 s9, s44, s1
	v_fma_f32 v206, -v140, v141, 1.0
	v_fmac_f32_e32 v141, v206, v141
	v_div_scale_f32 v206, vcc, 1.0, v78, 1.0
	v_mul_f32_e32 v207, v206, v141
	v_fma_f32 v208, -v140, v207, v206
	v_fmac_f32_e32 v207, v208, v141
	v_fma_f32 v140, -v140, v207, v206
	v_div_fmas_f32 v140, v140, v141, v207
	v_div_fixup_f32 v78, v140, v78, 1.0
	v_pk_mul_f32 v[134:135], v[134:135], v[78:79] op_sel_hi:[1,0]
	v_pk_mul_f32 v[132:133], v[132:133], v[78:79] op_sel_hi:[1,0]
	v_pk_add_f32 v[140:141], v[204:205], 1.0 op_sel_hi:[1,0]
	v_pk_fma_f32 v[134:135], v[202:203], v[134:135], v[136:137]
	v_pk_fma_f32 v[132:133], v[140:141], v[132:133], v[138:139]
	v_mov_b32_e32 v139, v79
	v_cvt_pk_fp8_f32 v139, v134, v135
	v_cvt_pk_bf16_f32 v140, v134, v135
	v_cvt_pk_bf16_f32 v141, v132, v133
	v_pk_mul_f32 v[130:131], v[130:131], v[78:79] op_sel_hi:[1,0]
	v_cvt_pk_fp8_f32 v139, v132, v133 op_sel:[0,0,1]
	v_lshlrev_b32_e32 v136, 16, v140
	v_sub_f32_e32 v136, v134, v136
	v_and_b32_e32 v137, 0xffff0000, v140
	v_lshlrev_b32_e32 v138, 16, v141
	v_and_b32_e32 v134, 0xffff0000, v141
	v_sub_f32_e32 v137, v135, v137
	v_sub_f32_e32 v138, v132, v138
	v_sub_f32_e32 v134, v133, v134
	v_cvt_pk_bf16_f32 v202, v136, v137
	v_cvt_pk_bf16_f32 v203, v138, v134
	global_store_dword v150, v139, s[8:9]
	global_load_dwordx4 v[132:135], v[212:213], off offset:1024
	s_nop 0
	global_load_dwordx4 v[136:139], v[210:211], off offset:1024
	v_pk_mul_f32 v[128:129], v[128:129], v[78:79] op_sel_hi:[1,0]
	ds_write_b64 v159, v[140:141]
	ds_write_b64 v160, v[202:203]
	v_pk_mul_f32 v[126:127], v[126:127], v[78:79] op_sel_hi:[1,0]
	v_pk_mul_f32 v[124:125], v[124:125], v[78:79] op_sel_hi:[1,0]
	v_pk_mul_f32 v[122:123], v[122:123], v[78:79] op_sel_hi:[1,0]
	v_pk_mul_f32 v[120:121], v[120:121], v[78:79] op_sel_hi:[1,0]
	v_pk_mul_f32 v[118:119], v[118:119], v[78:79] op_sel_hi:[1,0]
	v_pk_mul_f32 v[116:117], v[116:117], v[78:79] op_sel_hi:[1,0]
	v_pk_mul_f32 v[112:113], v[112:113], v[78:79] op_sel_hi:[1,0]
	v_pk_mul_f32 v[110:111], v[110:111], v[78:79] op_sel_hi:[1,0]
	v_pk_mul_f32 v[108:109], v[108:109], v[78:79] op_sel_hi:[1,0]
	v_pk_mul_f32 v[106:107], v[106:107], v[78:79] op_sel_hi:[1,0]
	v_pk_mul_f32 v[104:105], v[104:105], v[78:79] op_sel_hi:[1,0]
	s_add_i32 s4, s4, 3
	s_ashr_i32 s5, s4, 31
	s_waitcnt vmcnt(1)
	v_pk_add_f32 v[134:135], v[134:135], 1.0 op_sel_hi:[1,0]
	v_pk_add_f32 v[132:133], v[132:133], 1.0 op_sel_hi:[1,0]
	s_waitcnt vmcnt(0)
	v_pk_fma_f32 v[128:129], v[134:135], v[128:129], v[138:139]
	v_pk_fma_f32 v[130:131], v[132:133], v[130:131], v[136:137]
	v_mov_b32_e32 v134, v79
	v_cvt_pk_fp8_f32 v134, v130, v131
	v_cvt_pk_bf16_f32 v136, v130, v131
	v_cvt_pk_bf16_f32 v137, v128, v129
	v_cvt_pk_fp8_f32 v134, v128, v129 op_sel:[0,0,1]
	v_lshlrev_b32_e32 v132, 16, v136
	v_and_b32_e32 v133, 0xffff0000, v136
	v_sub_f32_e32 v132, v130, v132
	v_sub_f32_e32 v133, v131, v133
	v_lshlrev_b32_e32 v130, 16, v137
	v_and_b32_e32 v131, 0xffff0000, v137
	v_sub_f32_e32 v130, v128, v130
	v_sub_f32_e32 v128, v129, v131
	v_cvt_pk_bf16_f32 v138, v132, v133
	v_cvt_pk_bf16_f32 v139, v130, v128
	global_store_dword v150, v134, s[8:9] offset:256
	global_load_dwordx4 v[128:131], v[212:213], off offset:2048
	s_nop 0
	global_load_dwordx4 v[132:135], v[210:211], off offset:2048
	ds_write_b64 v161, v[136:137]
	ds_write_b64 v162, v[138:139]
	v_and_b32_e32 v137, 0xffff0000, v102
	v_and_b32_e32 v136, 0xffff0000, v100
	s_waitcnt vmcnt(1)
	v_pk_add_f32 v[130:131], v[130:131], 1.0 op_sel_hi:[1,0]
	v_pk_add_f32 v[128:129], v[128:129], 1.0 op_sel_hi:[1,0]
	s_waitcnt vmcnt(0)
; #define LAS __attribute__((address_space(3)))
; __device__ __forceinline__ unsigned cvt_pk_bf16(float lo, float hi) { unsigned r; asm volatile("v_cvt_pk_bf16_f32 %0, %1, %2" : "=v"(r) : "v"(lo), "v"(hi)); return r; }
; __device__ __forceinline__ unsigned pk4_fp8(float a, float b, float c, float d) { int w = 0; w = __builtin_amdgcn_cvt_pk_fp8_f32(a, b, w, false); w = __builtin_amdgcn_cvt_pk_fp8_f32(c, d, w, true); return (unsigned)w; }
; __device__ __forceinline__ float bf_lo(unsigned w) { return __uint_as_float(w << 16); }
; __device__ __forceinline__ float bf_hi(unsigned w) { return __uint_as_float(w & 0xffff0000u); }
; __device__ __forceinline__ void p6_router(Frame& F) {
;     ...
;                 const int t = ta + q; f32x4 v[8]; float s = 0.f;
; #pragma unroll
;                 for (int j = 0; j < 8; ++j) { const u32x2 zb = zr[q][j]; v[j] = (f32x4){bf_lo(zb.x), bf_hi(zb.x), bf_lo(zb.y), bf_hi(zb.y)}; s += (v[j][0] + v[j][1]) + (v[j][2] + v[j][3]); }
;                 float mean = wave_sum(s) * (1.f / DM), s2 = 0.f;
;     ...
; #pragma unroll
;                 for (int j = 0; j < 8; ++j) { const f32x4 sh = ((const f32x4*)(mod + (size_t)b * 12288 + 6144))[loq + 64 * j], sc = ((const f32x4*)(mod + (size_t)b * 12288 + 8192))[loq + 64 * j];
;                     const f32x4 y = v[j] * rstd * (sc + 1.0f) + sh;
;                     u32x2 wh; wh.x = cvt_pk_bf16(y[0], y[1]); wh.y = cvt_pk_bf16(y[2], y[3]);
;                     const f32x4 yl = {y[0] - bf_lo(wh.x), y[1] - bf_hi(wh.x), y[2] - bf_lo(wh.y), y[3] - bf_hi(wh.y)};
;                     u32x2 wl; wl.x = cvt_pk_bf16(yl[0], yl[1]); wl.y = cvt_pk_bf16(yl[2], yl[3]);
;                     { const int r = 2 * wave + q; LAS unsigned char* rowp = F.lds + r * 4096 + ((((lane >> 1) + 32 * j) ^ r) << 4) + (lane & 1) * 8;
;                       *(LAS u32x2*)rowp = wh; *(LAS u32x2*)(rowp + 65536) = wl; }
;                     U2F[(size_t)t * (DM / 4) + lane + 64 * j] = pk4_fp8(y[0], y[1], y[2], y[3]); }
	v_pk_fma_f32 v[124:125], v[130:131], v[124:125], v[134:135]
	v_pk_fma_f32 v[126:127], v[128:129], v[126:127], v[132:133]
	v_mov_b32_e32 v130, v79
	v_cvt_pk_fp8_f32 v130, v126, v127
	v_cvt_pk_bf16_f32 v132, v126, v127
	v_cvt_pk_bf16_f32 v133, v124, v125
	v_cvt_pk_fp8_f32 v130, v124, v125 op_sel:[0,0,1]
	v_lshlrev_b32_e32 v128, 16, v132
	v_and_b32_e32 v129, 0xffff0000, v132
	v_sub_f32_e32 v128, v126, v128
	v_sub_f32_e32 v129, v127, v129
	v_lshlrev_b32_e32 v126, 16, v133
	v_and_b32_e32 v127, 0xffff0000, v133
	v_sub_f32_e32 v126, v124, v126
	v_sub_f32_e32 v124, v125, v127
	v_cvt_pk_bf16_f32 v134, v128, v129
	v_cvt_pk_bf16_f32 v135, v126, v124
	global_store_dword v150, v130, s[8:9] offset:512
	global_load_dwordx4 v[124:127], v[212:213], off offset:3072
	s_nop 0
	global_load_dwordx4 v[128:131], v[210:211], off offset:3072
	ds_write_b64 v165, v[132:133]
	ds_write_b64 v166, v[134:135]
	v_mov_b32_e32 v132, v79
	v_lshlrev_b32_e32 v135, 16, v102
	v_lshlrev_b32_e32 v134, 16, v100
	v_lshlrev_b32_e32 v133, 16, v103
	s_waitcnt vmcnt(1)
	v_pk_add_f32 v[126:127], v[126:127], 1.0 op_sel_hi:[1,0]
	v_pk_add_f32 v[124:125], v[124:125], 1.0 op_sel_hi:[1,0]
	s_waitcnt vmcnt(0)
	v_pk_fma_f32 v[120:121], v[120:121], v[126:127], v[130:131]
	v_pk_fma_f32 v[122:123], v[122:123], v[124:125], v[128:129]
	v_mov_b32_e32 v126, v79
	v_cvt_pk_fp8_f32 v126, v122, v123
	v_cvt_pk_bf16_f32 v138, v122, v123
	v_cvt_pk_bf16_f32 v139, v120, v121
	v_cvt_pk_fp8_f32 v126, v120, v121 op_sel:[0,0,1]
	v_lshlrev_b32_e32 v124, 16, v138
	v_and_b32_e32 v125, 0xffff0000, v138
	v_sub_f32_e32 v124, v122, v124
	v_sub_f32_e32 v125, v123, v125
	v_lshlrev_b32_e32 v122, 16, v139
	v_and_b32_e32 v123, 0xffff0000, v139
	v_sub_f32_e32 v122, v120, v122
	v_sub_f32_e32 v120, v121, v123
	v_cvt_pk_bf16_f32 v140, v124, v125
	v_cvt_pk_bf16_f32 v141, v122, v120
	v_add_co_u32_e32 v120, vcc, s41, v212
	global_store_dword v150, v126, s[8:9] offset:768
	s_nop 0
	v_addc_co_u32_e32 v121, vcc, 0, v213, vcc
	v_add_co_u32_e32 v122, vcc, s41, v210
	global_load_dwordx4 v[124:127], v[120:121], off
	s_nop 0
	v_addc_co_u32_e32 v123, vcc, 0, v211, vcc
	global_load_dwordx4 v[128:131], v[122:123], off
	ds_write_b64 v155, v[138:139]
	ds_write_b64 v156, v[140:141]
	v_and_b32_e32 v139, 0xffff0000, v103
	v_and_b32_e32 v138, 0xffff0000, v101
	v_and_b32_e32 v211, 0xffff0000, v99
	v_and_b32_e32 v210, 0xffff0000, v98
	s_waitcnt vmcnt(1)
	v_pk_add_f32 v[124:125], v[124:125], 1.0 op_sel_hi:[1,0]
	v_pk_add_f32 v[126:127], v[126:127], 1.0 op_sel_hi:[1,0]
	s_waitcnt vmcnt(0)
	v_pk_fma_f32 v[118:119], v[118:119], v[124:125], v[128:129]
	s_nop 0
	v_cvt_pk_fp8_f32 v132, v118, v119
	v_pk_fma_f32 v[116:117], v[116:117], v[126:127], v[130:131]
	v_cvt_pk_bf16_f32 v140, v118, v119
	v_lshlrev_b32_e32 v131, 16, v99
	v_cvt_pk_fp8_f32 v132, v116, v117 op_sel:[0,0,1]
	v_cvt_pk_bf16_f32 v141, v116, v117
	v_lshlrev_b32_e32 v100, 16, v140
	v_and_b32_e32 v102, 0xffff0000, v140
	v_lshlrev_b32_e32 v124, 16, v141
	v_and_b32_e32 v125, 0xffff0000, v141
	v_sub_f32_e32 v100, v118, v100
	v_sub_f32_e32 v102, v119, v102
	v_sub_f32_e32 v118, v116, v124
	v_sub_f32_e32 v116, v117, v125
	v_cvt_pk_bf16_f32 v160, v100, v102
	v_cvt_pk_bf16_f32 v161, v118, v116
	global_store_dword v150, v132, s[8:9] offset:1024
	global_load_dwordx4 v[202:205], v[122:123], off offset:1024
	global_load_dwordx4 v[206:209], v[120:121], off offset:1024
	v_lshlrev_b32_e32 v132, 16, v101
	v_pk_add_f32 v[100:101], v[134:135], v[136:137]
	v_pk_add_f32 v[102:103], v[132:133], v[138:139]
	v_lshlrev_b32_e32 v130, 16, v98
	v_pk_add_f32 v[100:101], v[100:101], v[102:103]
	v_pk_add_f32 v[98:99], v[130:131], v[210:211]
	v_add_f32_e32 v100, 0, v100
	v_add_f32_e32 v100, v100, v101
	v_lshlrev_b32_e32 v126, 16, v96
	v_and_b32_e32 v127, 0xffff0000, v96
	v_lshlrev_b32_e32 v128, 16, v97
	v_and_b32_e32 v129, 0xffff0000, v97
	v_lshlrev_b32_e32 v101, 16, v94
	v_and_b32_e32 v125, 0xffff0000, v94
	v_lshlrev_b32_e32 v119, 16, v95
	v_and_b32_e32 v117, 0xffff0000, v95
	v_pk_add_f32 v[94:95], v[98:99], v[98:99] op_sel:[0,1] op_sel_hi:[1,0]
	v_add_f32_e32 v118, v126, v127
	v_add_f32_e32 v116, v128, v129
	v_mov_b32_e32 v95, v125
	v_pk_add_f32 v[94:95], v[100:101], v[94:95]
	v_pk_add_f32 v[96:97], v[118:119], v[116:117]
	v_lshlrev_b32_e32 v103, 16, v93
	v_lshlrev_b32_e32 v102, 16, v92
	v_pk_add_f32 v[212:213], v[94:95], v[96:97]
	v_pk_add_f32 v[216:217], v[102:103], v[214:215]
	v_lshlrev_b32_e32 v96, 16, v90
	v_and_b32_e32 v97, 0xffff0000, v90
	v_lshlrev_b32_e32 v98, 16, v91
	v_and_b32_e32 v99, 0xffff0000, v91
	v_lshlrev_b32_e32 v94, 16, v88
	v_and_b32_e32 v95, 0xffff0000, v88
	v_lshlrev_b32_e32 v93, 16, v89
	v_and_b32_e32 v91, 0xffff0000, v89
	v_pk_add_f32 v[88:89], v[212:213], v[212:213] op_sel:[0,1] op_sel_hi:[1,0]
	v_pk_add_f32 v[212:213], v[216:217], v[216:217] op_sel:[0,1] op_sel_hi:[1,0]
	v_add_f32_e32 v92, v96, v97
	v_add_f32_e32 v90, v98, v99
	v_mov_b32_e32 v89, v94
	v_mov_b32_e32 v213, v95
	v_pk_add_f32 v[88:89], v[88:89], v[212:213]
	v_pk_add_f32 v[212:213], v[92:93], v[90:91]
	ds_write_b64 v169, v[140:141]
	ds_write_b64 v171, v[160:161]
	v_pk_add_f32 v[88:89], v[88:89], v[212:213]
	v_mov_b32_e32 v90, v79
	v_add_f32_e32 v88, v88, v89
	s_nop 1
	v_mov_b32_dpp v89, v88 quad_perm:[1,0,3,2] row_mask:0xf bank_mask:0xf
	s_waitcnt lgkmcnt(0)
	v_add_f32_e32 v88, v88, v89
	s_nop 1
	v_mov_b32_dpp v89, v88 quad_perm:[2,3,0,1] row_mask:0xf bank_mask:0xf
	s_waitcnt lgkmcnt(0)
	v_add_f32_e32 v88, v88, v89
	s_nop 1
	v_mov_b32_dpp v89, v88 row_shl:4 row_mask:0xf bank_mask:0x5
	s_nop 1
	v_mov_b32_dpp v89, v88 row_shr:4 row_mask:0xf bank_mask:0xa
	s_waitcnt lgkmcnt(0)
; #define LAS __attribute__((address_space(3)))
; __device__ __forceinline__ unsigned cvt_pk_bf16(float lo, float hi) { unsigned r; asm volatile("v_cvt_pk_bf16_f32 %0, %1, %2" : "=v"(r) : "v"(lo), "v"(hi)); return r; }
; __device__ __forceinline__ unsigned pk4_fp8(float a, float b, float c, float d) { int w = 0; w = __builtin_amdgcn_cvt_pk_fp8_f32(a, b, w, false); w = __builtin_amdgcn_cvt_pk_fp8_f32(c, d, w, true); return (unsigned)w; }
; __device__ __forceinline__ float bf_lo(unsigned w) { return __uint_as_float(w << 16); }
; __device__ __forceinline__ float bf_hi(unsigned w) { return __uint_as_float(w & 0xffff0000u); }
; __device__ __forceinline__ void p6_router(Frame& F) {
;     ...
;                 float mean = wave_sum(s) * (1.f / DM), s2 = 0.f;
; #pragma unroll
;                 for (int j = 0; j < 8; ++j) { v[j] = v[j] - mean; s2 += (v[j][0] * v[j][0] + v[j][1] * v[j][1]) + (v[j][2] * v[j][2] + v[j][3] * v[j][3]); }
;                 float rstd = 1.f / sqrtf(wave_sum(s2) * (1.f / DM) + LN_EPS);
;     ...
; #pragma unroll
;                 for (int j = 0; j < 8; ++j) { const f32x4 sh = ((const f32x4*)(mod + (size_t)b * 12288 + 6144))[loq + 64 * j], sc = ((const f32x4*)(mod + (size_t)b * 12288 + 8192))[loq + 64 * j];
;                     const f32x4 y = v[j] * rstd * (sc + 1.0f) + sh;
;                     u32x2 wh; wh.x = cvt_pk_bf16(y[0], y[1]); wh.y = cvt_pk_bf16(y[2], y[3]);
;                     const f32x4 yl = {y[0] - bf_lo(wh.x), y[1] - bf_hi(wh.x), y[2] - bf_lo(wh.y), y[3] - bf_hi(wh.y)};
;                     u32x2 wl; wl.x = cvt_pk_bf16(yl[0], yl[1]); wl.y = cvt_pk_bf16(yl[2], yl[3]);
;                     { const int r = 2 * wave + q; LAS unsigned char* rowp = F.lds + r * 4096 + ((((lane >> 1) + 32 * j) ^ r) << 4) + (lane & 1) * 8;
;                       *(LAS u32x2*)rowp = wh; *(LAS u32x2*)(rowp + 65536) = wl; }
;                     U2F[(size_t)t * (DM / 4) + lane + 64 * j] = pk4_fp8(y[0], y[1], y[2], y[3]); }
	v_add_f32_e32 v88, v88, v89
	s_nop 1
	v_mov_b32_dpp v89, v88 row_ror:8 row_mask:0xf bank_mask:0xf
	s_waitcnt lgkmcnt(0)
	v_add_f32_e32 v92, v88, v89
	v_pk_mul_f32 v[88:89], v[114:115], v[78:79] op_sel_hi:[1,0]
	v_mov_b32_e32 v100, v92
	s_nop 1
	v_permlane16_swap_b32_e32 v100, v92
	s_waitcnt vmcnt(0)
	v_pk_add_f32 v[140:141], v[206:207], 1.0 op_sel_hi:[1,0]
	s_nop 0
	v_pk_fma_f32 v[88:89], v[88:89], v[140:141], v[202:203]
	v_pk_add_f32 v[114:115], v[208:209], 1.0 op_sel_hi:[1,0]
	v_cvt_pk_fp8_f32 v90, v88, v89
	v_pk_fma_f32 v[112:113], v[112:113], v[114:115], v[204:205]
	v_cvt_pk_bf16_f32 v140, v88, v89
	s_nop 0
	v_cvt_pk_fp8_f32 v90, v112, v113 op_sel:[0,0,1]
	v_cvt_pk_bf16_f32 v141, v112, v113
	v_lshlrev_b32_e32 v114, 16, v140
	v_and_b32_e32 v115, 0xffff0000, v140
	v_lshlrev_b32_e32 v116, 16, v141
	v_and_b32_e32 v118, 0xffff0000, v141
	v_sub_f32_e32 v88, v88, v114
	v_sub_f32_e32 v89, v89, v115
	v_sub_f32_e32 v114, v112, v116
	v_sub_f32_e32 v112, v113, v118
	v_cvt_pk_bf16_f32 v160, v88, v89
	v_cvt_pk_bf16_f32 v161, v114, v112
	global_store_dword v150, v90, s[8:9] offset:1280
	global_load_dwordx4 v[112:115], v[120:121], off offset:2048
	global_load_dwordx4 v[202:205], v[122:123], off offset:2048
	s_waitcnt lgkmcnt(0)
	v_add_f32_e32 v88, v92, v100
	v_mov_b32_e32 v89, v88
	s_nop 1
	v_permlane32_swap_b32_e32 v89, v88
	v_mov_b32_e32 v118, v79
	ds_write_b64 v152, v[140:141]
	ds_write_b64 v153, v[160:161]
	s_waitcnt lgkmcnt(2)
	v_add_f32_e32 v124, v88, v89
	v_fmac_f32_e32 v126, 0xba000000, v124
	v_fmac_f32_e32 v128, 0xba000000, v124
	v_fmac_f32_e32 v96, 0xba000000, v124
	v_fmac_f32_e32 v127, 0xba000000, v124
	v_fmac_f32_e32 v129, 0xba000000, v124
	v_fmac_f32_e32 v101, 0xba000000, v124
	v_fmac_f32_e32 v97, 0xba000000, v124
	v_mul_f32_e32 v90, v126, v126
	v_mul_f32_e32 v92, v128, v128
	v_mul_f32_e32 v100, v96, v96
	v_pk_fma_f32 v[216:217], v[126:127], v[126:127], v[90:91] op_sel_hi:[1,1,0]
	v_pk_fma_f32 v[218:219], v[128:129], v[128:129], v[92:93] op_sel_hi:[1,1,0]
	v_pk_fma_f32 v[224:225], v[96:97], v[96:97], v[100:101] op_sel_hi:[1,1,0]
	v_fmac_f32_e32 v138, 0xba000000, v124
	v_fmac_f32_e32 v136, 0xba000000, v124
	v_fmac_f32_e32 v139, 0xba000000, v124
	v_fmac_f32_e32 v137, 0xba000000, v124
	v_fmac_f32_e32 v210, 0xba000000, v124
	v_fmac_f32_e32 v211, 0xba000000, v124
	v_fmac_f32_e32 v131, 0xba000000, v124
	v_fmac_f32_e32 v132, 0xba000000, v124
	v_fmac_f32_e32 v134, 0xba000000, v124
	v_fmac_f32_e32 v133, 0xba000000, v124
	v_fmac_f32_e32 v135, 0xba000000, v124
	v_fmac_f32_e32 v130, 0xba000000, v124
	v_fmac_f32_e32 v214, 0xba000000, v124
	v_fmac_f32_e32 v215, 0xba000000, v124
	v_fmac_f32_e32 v103, 0xba000000, v124
	v_pk_mul_f32 v[206:207], v[136:137], v[136:137]
	v_pk_mul_f32 v[208:209], v[138:139], v[138:139]
	v_mov_b32_e32 v212, v131
	v_mov_b32_e32 v213, v211
	v_mov_b32_e32 v131, v210
	v_mov_b32_e32 v88, v103
	v_mov_b32_e32 v89, v215
	v_mov_b32_e32 v103, v214
	v_pk_fma_f32 v[206:207], v[134:135], v[134:135], v[206:207]
	v_pk_fma_f32 v[208:209], v[132:133], v[132:133], v[208:209]
	v_pk_mul_f32 v[210:211], v[212:213], v[212:213]
	v_pk_mul_f32 v[214:215], v[130:131], v[130:131]
	v_pk_add_f32 v[206:207], v[206:207], v[208:209]
	v_pk_mov_b32 v[208:209], v[214:215], v[210:211] op_sel:[1,0]
	v_mov_b32_e32 v215, v211
	v_pk_add_f32 v[208:209], v[208:209], v[214:215]
	v_fmac_f32_e32 v117, 0xba000000, v124
	v_fmac_f32_e32 v119, 0xba000000, v124
	v_fmac_f32_e32 v125, 0xba000000, v124
	v_fmac_f32_e32 v102, 0xba000000, v124
	v_pk_add_f32 v[206:207], v[206:207], v[206:207] op_sel_hi:[0,1]
	v_pk_add_f32 v[208:209], v[208:209], v[208:209] op_sel_hi:[0,1]
	v_pk_mul_f32 v[220:221], v[88:89], v[88:89]
	v_pk_mul_f32 v[222:223], v[102:103], v[102:103]
	v_mul_f32_e32 v216, v101, v101
	v_mul_f32_e32 v218, v125, v125
	v_mul_f32_e32 v206, v117, v117
	v_mul_f32_e32 v208, v119, v119
	v_fmac_f32_e32 v98, 0xba000000, v124
	v_pk_mov_b32 v[210:211], v[222:223], v[220:221] op_sel:[1,0]
	v_mov_b32_e32 v223, v221
	v_pk_add_f32 v[214:215], v[216:217], v[218:219]
	v_pk_add_f32 v[206:207], v[208:209], v[206:207]
	v_fmac_f32_e32 v99, 0xba000000, v124
	v_mul_f32_e32 v116, v98, v98
	v_pk_add_f32 v[210:211], v[210:211], v[222:223]
	v_pk_add_f32 v[206:207], v[214:215], v[206:207]
	v_pk_add_f32 v[210:211], v[210:211], v[210:211] op_sel_hi:[0,1]
	v_pk_add_f32 v[206:207], v[206:207], v[206:207] op_sel_hi:[0,1]
	v_fmac_f32_e32 v91, 0xba000000, v124
	v_fmac_f32_e32 v93, 0xba000000, v124
	v_fmac_f32_e32 v95, 0xba000000, v124
	v_fmac_f32_e32 v94, 0xba000000, v124
	s_waitcnt vmcnt(1)
	v_pk_add_f32 v[112:113], v[112:113], 1.0 op_sel_hi:[1,0]
	v_pk_add_f32 v[114:115], v[114:115], 1.0 op_sel_hi:[1,0]
	s_waitcnt vmcnt(0)
	v_pk_fma_f32 v[110:111], v[110:111], v[112:113], v[202:203]
	v_pk_fma_f32 v[108:109], v[108:109], v[114:115], v[204:205]
	v_cvt_pk_fp8_f32 v118, v110, v111
	v_cvt_pk_bf16_f32 v140, v110, v111
	v_cvt_pk_bf16_f32 v141, v108, v109
	v_mul_f32_e32 v224, v94, v94
	v_cvt_pk_fp8_f32 v118, v108, v109 op_sel:[0,0,1]
	v_lshlrev_b32_e32 v90, 16, v140
	v_and_b32_e32 v92, 0xffff0000, v140
	v_lshlrev_b32_e32 v100, 16, v141
	v_and_b32_e32 v112, 0xffff0000, v141
	v_sub_f32_e32 v90, v110, v90
	v_sub_f32_e32 v92, v111, v92
	v_sub_f32_e32 v100, v108, v100
	v_sub_f32_e32 v108, v109, v112
	v_cvt_pk_bf16_f32 v152, v90, v92
	v_cvt_pk_bf16_f32 v153, v100, v108
	global_store_dword v150, v118, s[8:9] offset:1536
	global_load_dwordx4 v[108:111], v[122:123], off offset:3072
	global_load_dwordx4 v[112:115], v[120:121], off offset:3072
	v_pk_fma_f32 v[120:121], v[98:99], v[98:99], v[116:117] op_sel_hi:[1,1,0]
	v_mul_f32_e32 v210, v93, v93
	v_mul_f32_e32 v120, v95, v95
	v_mul_f32_e32 v206, v91, v91
	v_pk_add_f32 v[120:121], v[224:225], v[120:121]
	v_pk_add_f32 v[122:123], v[210:211], v[206:207]
	v_mov_b32_e32 v100, v79
	v_pk_add_f32 v[120:121], v[120:121], v[122:123]
	v_mov_b32_e32 v122, v133
	v_add_f32_e32 v90, v120, v121
	s_nop 1
	v_mov_b32_dpp v92, v90 quad_perm:[1,0,3,2] row_mask:0xf bank_mask:0xf
	v_mov_b32_e32 v120, v135
	v_mov_b32_e32 v135, v136
	ds_write_b64 v163, v[140:141]
	ds_write_b64 v164, v[152:153]
	v_mov_b32_e32 v121, v137
	s_waitcnt lgkmcnt(2)
; __device__ __forceinline__ unsigned cvt_pk_bf16(float lo, float hi) { unsigned r; asm volatile("v_cvt_pk_bf16_f32 %0, %1, %2" : "=v"(r) : "v"(lo), "v"(hi)); return r; }
; __device__ __forceinline__ void p6_router(Frame& F) {
;     ...
;                 for (int j = 0; j < 8; ++j) { v[j] = v[j] - mean; s2 += (v[j][0] * v[j][0] + v[j][1] * v[j][1]) + (v[j][2] * v[j][2] + v[j][3] * v[j][3]); }
;                 float rstd = 1.f / sqrtf(wave_sum(s2) * (1.f / DM) + LN_EPS);
;                 s = 0.f;
; #pragma unroll
;                 for (int j = 0; j < 8; ++j) { v[j] = v[j] * rstd * pw[j] + pb[j]; { u32x2 xb; xb.x = cvt_pk_bf16(v[j][0], v[j][1]); xb.y = cvt_pk_bf16(v[j][2], v[j][3]); ((u32x2*)(X1 + (size_t)t * DM))[lane + 64 * j] = xb; } s += (v[j][0] + v[j][1]) + (v[j][2] + v[j][3]); }
;                 mean = wave_sum(s) * (1.f / DM); s2 = 0.f;
	v_add_f32_e32 v90, v90, v92
	s_nop 1
	v_mov_b32_dpp v92, v90 quad_perm:[2,3,0,1] row_mask:0xf bank_mask:0xf
	v_mov_b32_e32 v123, v139
	s_waitcnt lgkmcnt(0)
	v_add_f32_e32 v90, v90, v92
	s_nop 1
	v_mov_b32_dpp v92, v90 row_shl:4 row_mask:0xf bank_mask:0x5
	s_nop 1
	v_mov_b32_dpp v92, v90 row_shr:4 row_mask:0xf bank_mask:0xa
	s_waitcnt lgkmcnt(0)
	v_add_f32_e32 v90, v90, v92
	s_nop 1
	v_mov_b32_dpp v92, v90 row_ror:8 row_mask:0xf bank_mask:0xf
	s_waitcnt lgkmcnt(0)
	v_add_f32_e32 v90, v90, v92
	v_mov_b32_e32 v92, v90
	s_nop 1
	v_permlane16_swap_b32_e32 v92, v90
	s_waitcnt lgkmcnt(0)
	v_add_f32_e32 v90, v90, v92
	v_mov_b32_e32 v92, v90
	s_nop 1
	v_permlane32_swap_b32_e32 v92, v90
	s_waitcnt lgkmcnt(0)
	v_add_f32_e32 v90, v90, v92
	v_fmamk_f32 v90, v90, 0x3a000000, v148
	v_mul_f32_e32 v92, 0x4f800000, v90
	v_cmp_gt_f32_e32 vcc, s45, v90
	s_waitcnt vmcnt(0)
	v_pk_add_f32 v[112:113], v[112:113], 1.0 op_sel_hi:[1,0]
	v_cndmask_b32_e32 v90, v90, v92, vcc
	v_sqrt_f32_e32 v92, v90
	v_pk_fma_f32 v[106:107], v[106:107], v[112:113], v[108:109]
	v_pk_add_f32 v[114:115], v[114:115], 1.0 op_sel_hi:[1,0]
	v_cvt_pk_fp8_f32 v100, v106, v107
	v_add_u32_e32 v116, -1, v92
	v_add_u32_e32 v118, 1, v92
	v_fma_f32 v124, -v116, v92, v90
	v_fma_f32 v133, -v118, v92, v90
	v_cmp_ge_f32_e64 s[0:1], 0, v124
	v_pk_fma_f32 v[104:105], v[104:105], v[114:115], v[110:111]
	v_cvt_pk_bf16_f32 v108, v106, v107
	s_nop 0
	v_cndmask_b32_e64 v92, v92, v116, s[0:1]
	v_cmp_lt_f32_e64 s[0:1], 0, v133
	v_lshlrev_b32_e32 v78, 16, v108
	v_and_b32_e32 v110, 0xffff0000, v108
	v_cndmask_b32_e64 v92, v92, v118, s[0:1]
	v_mul_f32_e32 v116, 0x37800000, v92
	v_cndmask_b32_e32 v92, v92, v116, vcc
	v_cmp_class_f32_e32 vcc, v90, v149
	v_cvt_pk_bf16_f32 v109, v104, v105
	v_sub_f32_e32 v78, v106, v78
	v_lshlrev_b32_e32 v111, 16, v109
	v_cndmask_b32_e32 v90, v92, v90, vcc
	v_div_scale_f32 v92, s[0:1], v90, v90, 1.0
	v_rcp_f32_e32 v116, v92
	v_div_scale_f32 v118, vcc, 1.0, v90, 1.0
	v_sub_f32_e32 v106, v107, v110
	v_fma_f32 v124, -v92, v116, 1.0
	v_fmac_f32_e32 v116, v124, v116
	v_mul_f32_e32 v124, v118, v116
	v_fma_f32 v136, -v92, v124, v118
	v_fmac_f32_e32 v124, v136, v116
	v_fma_f32 v92, -v92, v124, v118
	v_div_fmas_f32 v92, v92, v116, v124
	v_and_b32_e32 v112, 0xffff0000, v109
	v_sub_f32_e32 v107, v104, v111
	v_cvt_pk_bf16_f32 v106, v78, v106
	v_div_fixup_f32 v78, v92, v90, 1.0
	v_mov_b32_e32 v133, v138
	v_sub_f32_e32 v110, v105, v112
	v_cvt_pk_fp8_f32 v100, v104, v105 op_sel:[0,0,1]
	v_cvt_pk_bf16_f32 v107, v107, v110
	v_pk_mul_f32 v[104:105], v[134:135], v[78:79] op_sel_hi:[1,0]
	ds_write_b64 v157, v[108:109]
	ds_write_b64 v158, v[106:107]
	v_pk_mul_f32 v[106:107], v[132:133], v[78:79] op_sel_hi:[1,0]
	v_pk_fma_f32 v[70:71], v[70:71], v[104:105], v[10:11]
	v_pk_mul_f32 v[10:11], v[120:121], v[78:79] op_sel_hi:[1,0]
	v_pk_fma_f32 v[72:73], v[72:73], v[106:107], v[12:13]
	v_pk_mul_f32 v[12:13], v[122:123], v[78:79] op_sel_hi:[1,0]
	v_pk_fma_f32 v[62:63], v[62:63], v[10:11], v[66:67]
	v_pk_fma_f32 v[64:65], v[64:65], v[12:13], v[68:69]
	v_mov_b32_e32 v10, v62
	v_mov_b32_e32 v11, v70
	v_mov_b32_e32 v12, v63
	v_mov_b32_e32 v13, v71
	v_pk_add_f32 v[10:11], v[10:11], v[12:13]
	v_mov_b32_e32 v12, v65
	v_mov_b32_e32 v13, v73
	v_mov_b32_e32 v66, v64
	v_mov_b32_e32 v67, v72
	v_pk_add_f32 v[12:13], v[12:13], v[66:67]
	v_pk_mul_f32 v[66:67], v[212:213], v[78:79] op_sel_hi:[1,0]
	v_pk_add_f32 v[10:11], v[10:11], v[12:13]
	v_pk_mul_f32 v[12:13], v[130:131], v[78:79] op_sel_hi:[1,0]
	v_pk_fma_f32 v[56:57], v[56:57], v[66:67], v[60:61]
	v_pk_fma_f32 v[54:55], v[54:55], v[12:13], v[58:59]
	v_mov_b32_e32 v13, v57
	v_mov_b32_e32 v12, v54
	v_pk_mov_b32 v[58:59], v[54:55], v[56:57] op_sel:[1,0]
	v_pk_mul_f32 v[60:61], v[128:129], v[78:79] op_sel_hi:[1,0]
	v_pk_add_f32 v[12:13], v[12:13], v[58:59]
	v_pk_mul_f32 v[58:59], v[126:127], v[78:79] op_sel_hi:[1,0]
	v_mov_b32_e32 v124, v101
	v_mov_b32_e32 v116, v119
	v_pk_fma_f32 v[48:49], v[48:49], v[60:61], v[52:53]
	v_pk_fma_f32 v[46:47], v[46:47], v[58:59], v[50:51]
	v_pk_mul_f32 v[58:59], v[124:125], v[78:79] op_sel_hi:[1,0]
	v_pk_mul_f32 v[60:61], v[116:117], v[78:79] op_sel_hi:[1,0]
	v_add_f32_e32 v11, 0, v11
	v_pk_add_f32 v[12:13], v[12:13], v[12:13] op_sel_hi:[0,1]
	v_pk_fma_f32 v[40:41], v[40:41], v[60:61], v[44:45]
	v_pk_fma_f32 v[38:39], v[38:39], v[58:59], v[42:43]
	v_add_f32_e32 v11, v10, v11
	v_add_f32_e32 v51, v46, v47
	v_add_f32_e32 v53, v49, v48
	v_mov_b32_e32 v50, v38
	v_mov_b32_e32 v52, v39
	v_mov_b32_e32 v12, v41
	v_mov_b32_e32 v10, v40
	v_pk_add_f32 v[42:43], v[50:51], v[52:53]
	v_pk_add_f32 v[10:11], v[12:13], v[10:11]
	v_pk_mul_f32 v[12:13], v[88:89], v[78:79] op_sel_hi:[1,0]
	v_pk_add_f32 v[10:11], v[42:43], v[10:11]
	v_pk_fma_f32 v[32:33], v[32:33], v[12:13], v[36:37]
	v_pk_add_f32 v[42:43], v[10:11], v[10:11] op_sel_hi:[0,1]
	v_pk_mul_f32 v[10:11], v[102:103], v[78:79] op_sel_hi:[1,0]
	v_mov_b32_e32 v90, v93
	v_pk_fma_f32 v[30:31], v[30:31], v[10:11], v[34:35]
	v_mov_b32_e32 v11, v33
	v_mov_b32_e32 v10, v30
	v_pk_mov_b32 v[12:13], v[30:31], v[32:33] op_sel:[1,0]
	s_lshl_b64 s[0:1], s[4:5], 12
	v_pk_add_f32 v[10:11], v[10:11], v[12:13]
	v_pk_mul_f32 v[12:13], v[98:99], v[78:79] op_sel_hi:[1,0]
	v_pk_add_f32 v[34:35], v[10:11], v[10:11] op_sel_hi:[0,1]
	v_pk_mul_f32 v[10:11], v[96:97], v[78:79] op_sel_hi:[1,0]
	v_pk_fma_f32 v[24:25], v[24:25], v[12:13], v[28:29]
	v_pk_fma_f32 v[22:23], v[22:23], v[10:11], v[26:27]
	v_pk_mul_f32 v[12:13], v[94:95], v[78:79] op_sel_hi:[1,0]
	v_pk_mul_f32 v[10:11], v[90:91], v[78:79] op_sel_hi:[1,0]
	v_pk_fma_f32 v[12:13], v[14:15], v[12:13], v[18:19]
	v_pk_fma_f32 v[10:11], v[16:17], v[10:11], v[20:21]
	v_add_f32_e32 v27, v22, v23
	v_add_f32_e32 v29, v25, v24
	v_mov_b32_e32 v26, v12
	v_mov_b32_e32 v28, v13
	v_mov_b32_e32 v34, v11
	v_mov_b32_e32 v42, v10
	v_pk_add_f32 v[14:15], v[26:27], v[28:29]
	v_pk_add_f32 v[16:17], v[34:35], v[42:43]
	s_add_u32 s0, s42, s0
	v_pk_add_f32 v[14:15], v[14:15], v[16:17]
	s_addc_u32 s1, s43, s1
	v_add_f32_e32 v15, v14, v15
	s_nop 1
	v_mov_b32_dpp v16, v15 quad_perm:[1,0,3,2] row_mask:0xf bank_mask:0xf
	global_store_dword v150, v100, s[8:9] offset:1792
	v_cvt_pk_bf16_f32 v104, v70, v71
	v_cvt_pk_bf16_f32 v105, v72, v73
	global_store_dwordx2 v146, v[104:105], s[0:1]
	s_waitcnt lgkmcnt(0)
; __device__ __forceinline__ void p6_router(Frame& F) {
;     ...
;                 mean = wave_sum(s) * (1.f / DM); s2 = 0.f;
; #pragma unroll
;                 for (int j = 0; j < 8; ++j) { v[j] = v[j] - mean; s2 += (v[j][0] * v[j][0] + v[j][1] * v[j][1]) + (v[j][2] * v[j][2] + v[j][3] * v[j][3]); }
;                 rstd = 1.f / sqrtf(wave_sum(s2) * (1.f / DM) + LN_EPS);
;                 int loq = lane; asm volatile("" : "+v"(loq));
; #pragma unroll
;                 for (int j = 0; j < 8; ++j) { const f32x4 sh = ((const f32x4*)(mod + (size_t)b * 12288 + 6144))[loq + 64 * j], sc = ((const f32x4*)(mod + (size_t)b * 12288 + 8192))[loq + 64 * j];
	v_add_f32_e32 v16, v15, v16
	s_nop 1
	v_mov_b32_dpp v17, v16 quad_perm:[2,3,0,1] row_mask:0xf bank_mask:0xf
	v_cvt_pk_bf16_f32 v14, v62, v63
	v_cvt_pk_bf16_f32 v15, v64, v65
	global_store_dwordx2 v146, v[14:15], s[0:1] offset:512
	v_cvt_pk_bf16_f32 v14, v54, v55
	s_waitcnt lgkmcnt(0)
	v_add_f32_e32 v16, v16, v17
	s_nop 1
	v_mov_b32_dpp v17, v16 row_shl:4 row_mask:0xf bank_mask:0x5
	s_nop 1
	v_mov_b32_dpp v17, v16 row_shr:4 row_mask:0xf bank_mask:0xa
	v_cvt_pk_bf16_f32 v15, v56, v57
	global_store_dwordx2 v146, v[14:15], s[0:1] offset:1024
	v_cvt_pk_bf16_f32 v14, v46, v47
	v_cvt_pk_bf16_f32 v15, v48, v49
	s_waitcnt lgkmcnt(0)
	v_add_f32_e32 v16, v16, v17
	s_nop 1
	v_mov_b32_dpp v17, v16 row_ror:8 row_mask:0xf bank_mask:0xf
	global_store_dwordx2 v146, v[14:15], s[0:1] offset:1536
	v_cvt_pk_bf16_f32 v14, v38, v39
	v_cvt_pk_bf16_f32 v15, v40, v41
	global_store_dwordx2 v146, v[14:15], s[0:1] offset:2048
	s_waitcnt lgkmcnt(0)
	v_add_f32_e32 v16, v16, v17
	v_mov_b32_e32 v17, v16
	s_nop 1
	v_permlane16_swap_b32_e32 v17, v16
	v_cvt_pk_bf16_f32 v14, v30, v31
	v_cvt_pk_bf16_f32 v15, v32, v33
	global_store_dwordx2 v146, v[14:15], s[0:1] offset:2560
	v_cvt_pk_bf16_f32 v14, v22, v23
	s_waitcnt lgkmcnt(0)
	v_add_f32_e32 v16, v16, v17
	v_mov_b32_e32 v17, v16
	s_nop 1
	v_permlane32_swap_b32_e32 v17, v16
	v_cvt_pk_bf16_f32 v15, v24, v25
	global_store_dwordx2 v146, v[14:15], s[0:1] offset:3072
	v_cvt_pk_bf16_f32 v14, v12, v13
	v_cvt_pk_bf16_f32 v15, v10, v11
	s_waitcnt lgkmcnt(0)
	v_add_f32_e32 v26, v16, v17
	v_fmamk_f32 v71, v26, 0xba000000, v71
	v_fmamk_f32 v63, v26, 0xba000000, v63
	v_fmamk_f32 v73, v26, 0xba000000, v73
	v_fmac_f32_e32 v70, 0xba000000, v26
	v_fmamk_f32 v65, v26, 0xba000000, v65
	v_fmac_f32_e32 v62, 0xba000000, v26
	v_mov_b32_e32 v16, v71
	v_mov_b32_e32 v17, v63
	global_store_dwordx2 v146, v[14:15], s[0:1] offset:3584
	v_fmac_f32_e32 v72, 0xba000000, v26
	v_fmac_f32_e32 v64, 0xba000000, v26
	v_mov_b32_e32 v14, v70
	v_mov_b32_e32 v15, v62
	v_pk_mul_f32 v[16:17], v[16:17], v[16:17]
	v_mov_b32_e32 v18, v73
	v_mov_b32_e32 v19, v65
	v_pk_fma_f32 v[14:15], v[14:15], v[14:15], v[16:17]
	v_mov_b32_e32 v16, v72
	v_mov_b32_e32 v17, v64
	v_pk_mul_f32 v[18:19], v[18:19], v[18:19]
	v_fmamk_f32 v55, v26, 0xba000000, v55
	v_pk_fma_f32 v[16:17], v[16:17], v[16:17], v[18:19]
	v_fmac_f32_e32 v54, 0xba000000, v26
	v_pk_add_f32 v[14:15], v[14:15], v[16:17]
	v_fmamk_f32 v57, v26, 0xba000000, v57
	v_fmac_f32_e32 v56, 0xba000000, v26
	v_pk_add_f32 v[14:15], v[14:15], v[14:15] op_sel_hi:[0,1]
	v_pk_mul_f32 v[16:17], v[56:57], v[56:57]
	v_pk_mul_f32 v[18:19], v[54:55], v[54:55]
	v_fmac_f32_e32 v46, 0xba000000, v26
	v_pk_mov_b32 v[20:21], v[18:19], v[16:17] op_sel:[1,0]
	v_mov_b32_e32 v19, v17
	v_fmamk_f32 v47, v26, 0xba000000, v47
	v_fmac_f32_e32 v48, 0xba000000, v26
	v_mul_f32_e32 v14, v46, v46
	v_pk_add_f32 v[16:17], v[20:21], v[18:19]
	v_fmamk_f32 v49, v26, 0xba000000, v49
	v_pk_fma_f32 v[18:19], v[46:47], v[46:47], v[14:15] op_sel_hi:[1,1,0]
	v_mul_f32_e32 v14, v48, v48
	v_pk_add_f32 v[16:17], v[16:17], v[16:17] op_sel_hi:[0,1]
	v_pk_fma_f32 v[20:21], v[48:49], v[48:49], v[14:15] op_sel_hi:[1,1,0]
	v_fmamk_f32 v41, v26, 0xba000000, v41
	v_fmac_f32_e32 v40, 0xba000000, v26
	v_fmamk_f32 v39, v26, 0xba000000, v39
	v_fmac_f32_e32 v38, 0xba000000, v26
	v_mul_f32_e32 v18, v38, v38
	v_mul_f32_e32 v20, v39, v39
	v_mul_f32_e32 v16, v40, v40
	v_mul_f32_e32 v14, v41, v41
	v_pk_add_f32 v[18:19], v[18:19], v[20:21]
	v_pk_add_f32 v[14:15], v[16:17], v[14:15]
	v_fmamk_f32 v31, v26, 0xba000000, v31
	v_fmac_f32_e32 v30, 0xba000000, v26
	v_fmamk_f32 v33, v26, 0xba000000, v33
	v_fmac_f32_e32 v32, 0xba000000, v26
	v_pk_add_f32 v[14:15], v[18:19], v[14:15]
	v_pk_mul_f32 v[16:17], v[32:33], v[32:33]
	v_pk_mul_f32 v[18:19], v[30:31], v[30:31]
	v_pk_add_f32 v[14:15], v[14:15], v[14:15] op_sel_hi:[0,1]
	v_pk_mov_b32 v[20:21], v[18:19], v[16:17] op_sel:[1,0]
	v_mov_b32_e32 v19, v17
	v_fmac_f32_e32 v22, 0xba000000, v26
	v_pk_add_f32 v[16:17], v[20:21], v[18:19]
	v_fmamk_f32 v23, v26, 0xba000000, v23
	v_fmac_f32_e32 v24, 0xba000000, v26
	v_mul_f32_e32 v14, v22, v22
	v_pk_add_f32 v[34:35], v[16:17], v[16:17] op_sel_hi:[0,1]
	v_fmamk_f32 v25, v26, 0xba000000, v25
	v_pk_fma_f32 v[16:17], v[22:23], v[22:23], v[14:15] op_sel_hi:[1,1,0]
	v_mul_f32_e32 v14, v24, v24
	v_pk_fma_f32 v[18:19], v[24:25], v[24:25], v[14:15] op_sel_hi:[1,1,0]
	v_fmamk_f32 v13, v26, 0xba000000, v13
	v_fmac_f32_e32 v12, 0xba000000, v26
	v_mul_f32_e32 v16, v12, v12
	v_mul_f32_e32 v18, v13, v13
	v_pk_add_f32 v[36:37], v[16:17], v[18:19]
	v_mov_b32_e32 v16, v170
	v_fmamk_f32 v11, v26, 0xba000000, v11
	v_ashrrev_i32_e32 v17, 31, v16
	v_lshlrev_b64 v[18:19], 4, v[16:17]
	v_lshl_add_u64 v[16:17], s[16:17], 0, v[18:19]
	v_fmac_f32_e32 v10, 0xba000000, v26
	v_lshl_add_u64 v[42:43], s[20:21], 0, v[18:19]
	global_load_dwordx4 v[18:21], v[16:17], off
	global_load_dwordx4 v[26:29], v[42:43], off
	v_mul_f32_e32 v34, v10, v10
	v_mul_f32_e32 v14, v11, v11
	v_pk_add_f32 v[14:15], v[34:35], v[14:15]
	s_waitcnt vmcnt(0)
	v_pk_add_f32 v[28:29], v[28:29], 1.0 op_sel_hi:[1,0]
	v_pk_add_f32 v[14:15], v[36:37], v[14:15]
	v_pk_add_f32 v[26:27], v[26:27], 1.0 op_sel_hi:[1,0]
	v_add_f32_e32 v14, v14, v15
	s_nop 1
	v_mov_b32_dpp v15, v14 quad_perm:[1,0,3,2] row_mask:0xf bank_mask:0xf
	s_waitcnt lgkmcnt(0)
	v_add_f32_e32 v14, v14, v15
	s_nop 1
	v_mov_b32_dpp v15, v14 quad_perm:[2,3,0,1] row_mask:0xf bank_mask:0xf
	s_waitcnt lgkmcnt(0)
	v_add_f32_e32 v14, v14, v15
	s_nop 1
	v_mov_b32_dpp v15, v14 row_shl:4 row_mask:0xf bank_mask:0x5
	s_nop 1
	v_mov_b32_dpp v15, v14 row_shr:4 row_mask:0xf bank_mask:0xa
	s_waitcnt lgkmcnt(0)
; #define LAS __attribute__((address_space(3)))
; __device__ __forceinline__ unsigned cvt_pk_bf16(float lo, float hi) { unsigned r; asm volatile("v_cvt_pk_bf16_f32 %0, %1, %2" : "=v"(r) : "v"(lo), "v"(hi)); return r; }
; __device__ __forceinline__ unsigned pk4_fp8(float a, float b, float c, float d) { int w = 0; w = __builtin_amdgcn_cvt_pk_fp8_f32(a, b, w, false); w = __builtin_amdgcn_cvt_pk_fp8_f32(c, d, w, true); return (unsigned)w; }
; __device__ __forceinline__ float bf_lo(unsigned w) { return __uint_as_float(w << 16); }
; __device__ __forceinline__ float bf_hi(unsigned w) { return __uint_as_float(w & 0xffff0000u); }
; __device__ __forceinline__ float wave_sum(float v) {
; #pragma unroll
;     for (int o = 1; o < 64; o <<= 1) v += __shfl_xor(v, o);
;     return v;
; __device__ __forceinline__ void p6_router(Frame& F) {
;     ...
;                 rstd = 1.f / sqrtf(wave_sum(s2) * (1.f / DM) + LN_EPS);
;                 int loq = lane; asm volatile("" : "+v"(loq));
; #pragma unroll
;                 for (int j = 0; j < 8; ++j) { const f32x4 sh = ((const f32x4*)(mod + (size_t)b * 12288 + 6144))[loq + 64 * j], sc = ((const f32x4*)(mod + (size_t)b * 12288 + 8192))[loq + 64 * j];
;                     const f32x4 y = v[j] * rstd * (sc + 1.0f) + sh;
;                     u32x2 wh; wh.x = cvt_pk_bf16(y[0], y[1]); wh.y = cvt_pk_bf16(y[2], y[3]);
;                     const f32x4 yl = {y[0] - bf_lo(wh.x), y[1] - bf_hi(wh.x), y[2] - bf_lo(wh.y), y[3] - bf_hi(wh.y)};
;                     u32x2 wl; wl.x = cvt_pk_bf16(yl[0], yl[1]); wl.y = cvt_pk_bf16(yl[2], yl[3]);
;                     { const int r = 2 * wave + q; LAS unsigned char* rowp = F.lds + r * 4096 + ((((lane >> 1) + 32 * j) ^ r) << 4) + (lane & 1) * 8;
;                       *(LAS u32x2*)rowp = wh; *(LAS u32x2*)(rowp + 65536) = wl; }
;                     U2F[(size_t)t * (DM / 4) + lane + 64 * j] = pk4_fp8(y[0], y[1], y[2], y[3]); }
	v_add_f32_e32 v14, v14, v15
	s_nop 1
	v_mov_b32_dpp v15, v14 row_ror:8 row_mask:0xf bank_mask:0xf
	s_waitcnt lgkmcnt(0)
	v_add_f32_e32 v14, v14, v15
	v_mov_b32_e32 v15, v14
	s_nop 1
	v_permlane16_swap_b32_e32 v15, v14
	s_waitcnt lgkmcnt(0)
	v_add_f32_e32 v14, v14, v15
	v_mov_b32_e32 v15, v14
	s_nop 1
	v_permlane32_swap_b32_e32 v15, v14
	s_waitcnt lgkmcnt(0)
	v_add_f32_e32 v14, v14, v15
	v_fmac_f32_e32 v148, 0x3a000000, v14
	v_mul_f32_e32 v14, 0x4f800000, v148
	v_cmp_gt_f32_e32 vcc, s45, v148
	s_nop 1
	v_cndmask_b32_e32 v14, v148, v14, vcc
	v_sqrt_f32_e32 v15, v14
	s_nop 0
	v_add_u32_e32 v34, -1, v15
	v_fma_f32 v35, -v34, v15, v14
	v_cmp_ge_f32_e64 s[0:1], 0, v35
	v_add_u32_e32 v35, 1, v15
	s_nop 0
	v_cndmask_b32_e64 v34, v15, v34, s[0:1]
	v_fma_f32 v15, -v35, v15, v14
	v_cmp_lt_f32_e64 s[0:1], 0, v15
	s_nop 1
	v_cndmask_b32_e64 v15, v34, v35, s[0:1]
	v_mul_f32_e32 v34, 0x37800000, v15
	v_cndmask_b32_e32 v15, v15, v34, vcc
	v_cmp_class_f32_e32 vcc, v14, v149
	s_nop 1
	v_cndmask_b32_e32 v14, v15, v14, vcc
	v_div_scale_f32 v15, s[0:1], v14, v14, 1.0
	v_rcp_f32_e32 v34, v15
	s_lshl_b64 s[0:1], s[4:5], 11
	s_add_u32 s0, s40, s0
	s_addc_u32 s1, s44, s1
	v_fma_f32 v35, -v15, v34, 1.0
	v_fmac_f32_e32 v34, v35, v34
	v_div_scale_f32 v35, vcc, 1.0, v14, 1.0
	v_mul_f32_e32 v36, v35, v34
	v_fma_f32 v37, -v15, v36, v35
	v_fmac_f32_e32 v36, v37, v34
	v_fma_f32 v15, -v15, v36, v35
	v_div_fmas_f32 v15, v15, v34, v36
	v_div_fixup_f32 v14, v15, v14, 1.0
	v_pk_mul_f32 v[34:35], v[70:71], v[14:15] op_sel_hi:[1,0]
	v_pk_mul_f32 v[36:37], v[72:73], v[14:15] op_sel_hi:[1,0]
	v_pk_fma_f32 v[18:19], v[26:27], v[34:35], v[18:19]
	v_pk_fma_f32 v[20:21], v[28:29], v[36:37], v[20:21]
	v_mov_b32_e32 v28, v79
	v_cvt_pk_fp8_f32 v28, v18, v19
	v_cvt_pk_bf16_f32 v34, v18, v19
	v_cvt_pk_bf16_f32 v35, v20, v21
	v_cvt_pk_fp8_f32 v28, v20, v21 op_sel:[0,0,1]
	v_lshlrev_b32_e32 v15, 16, v34
	v_sub_f32_e32 v15, v18, v15
	v_and_b32_e32 v26, 0xffff0000, v34
	v_lshlrev_b32_e32 v27, 16, v35
	v_and_b32_e32 v18, 0xffff0000, v35
	v_sub_f32_e32 v26, v19, v26
	v_sub_f32_e32 v27, v20, v27
	v_sub_f32_e32 v18, v21, v18
	v_cvt_pk_bf16_f32 v36, v15, v26
	v_cvt_pk_bf16_f32 v37, v27, v18
	global_store_dword v150, v28, s[0:1]
	global_load_dwordx4 v[18:21], v[42:43], off offset:1024
	s_nop 0
	global_load_dwordx4 v[26:29], v[16:17], off offset:1024
	ds_write_b64 v172, v[34:35]
	ds_write_b64 v173, v[36:37]
	v_pk_mul_f32 v[34:35], v[62:63], v[14:15] op_sel_hi:[1,0]
	v_pk_mul_f32 v[36:37], v[64:65], v[14:15] op_sel_hi:[1,0]
	s_waitcnt vmcnt(1)
	v_pk_add_f32 v[18:19], v[18:19], 1.0 op_sel_hi:[1,0]
	s_waitcnt vmcnt(0)
	v_pk_fma_f32 v[18:19], v[18:19], v[34:35], v[26:27]
	v_mov_b32_e32 v27, v79
	v_cvt_pk_fp8_f32 v27, v18, v19
	v_pk_add_f32 v[20:21], v[20:21], 1.0 op_sel_hi:[1,0]
	v_cvt_pk_bf16_f32 v34, v18, v19
	s_nop 0
	v_pk_fma_f32 v[20:21], v[20:21], v[36:37], v[28:29]
	v_lshlrev_b32_e32 v15, 16, v34
	v_cvt_pk_fp8_f32 v27, v20, v21 op_sel:[0,0,1]
	v_and_b32_e32 v26, 0xffff0000, v34
	v_cvt_pk_bf16_f32 v35, v20, v21
	v_sub_f32_e32 v15, v18, v15
	v_sub_f32_e32 v26, v19, v26
	v_lshlrev_b32_e32 v18, 16, v35
	v_and_b32_e32 v19, 0xffff0000, v35
	v_sub_f32_e32 v18, v20, v18
	v_sub_f32_e32 v19, v21, v19
	v_cvt_pk_bf16_f32 v36, v15, v26
	v_cvt_pk_bf16_f32 v37, v18, v19
	global_store_dword v150, v27, s[0:1] offset:256
	global_load_dwordx4 v[18:21], v[42:43], off offset:2048
	s_nop 0
	global_load_dwordx4 v[26:29], v[16:17], off offset:2048
	ds_write_b64 v174, v[34:35]
	ds_write_b64 v175, v[36:37]
	v_pk_mul_f32 v[34:35], v[54:55], v[14:15] op_sel_hi:[1,0]
	v_pk_mul_f32 v[36:37], v[56:57], v[14:15] op_sel_hi:[1,0]
	s_waitcnt vmcnt(1)
	v_pk_add_f32 v[18:19], v[18:19], 1.0 op_sel_hi:[1,0]
	s_waitcnt vmcnt(0)
	v_pk_fma_f32 v[18:19], v[18:19], v[34:35], v[26:27]
	v_mov_b32_e32 v27, v79
	v_cvt_pk_fp8_f32 v27, v18, v19
	v_pk_add_f32 v[20:21], v[20:21], 1.0 op_sel_hi:[1,0]
	v_cvt_pk_bf16_f32 v34, v18, v19
	s_nop 0
	v_pk_fma_f32 v[20:21], v[20:21], v[36:37], v[28:29]
	v_lshlrev_b32_e32 v15, 16, v34
	v_cvt_pk_fp8_f32 v27, v20, v21 op_sel:[0,0,1]
	v_and_b32_e32 v26, 0xffff0000, v34
	v_cvt_pk_bf16_f32 v35, v20, v21
	v_sub_f32_e32 v15, v18, v15
	v_sub_f32_e32 v26, v19, v26
	v_lshlrev_b32_e32 v18, 16, v35
	v_and_b32_e32 v19, 0xffff0000, v35
	v_sub_f32_e32 v18, v20, v18
	v_sub_f32_e32 v19, v21, v19
	v_cvt_pk_bf16_f32 v36, v15, v26
	v_cvt_pk_bf16_f32 v37, v18, v19
	global_store_dword v150, v27, s[0:1] offset:512
	global_load_dwordx4 v[18:21], v[42:43], off offset:3072
	s_nop 0
	global_load_dwordx4 v[26:29], v[16:17], off offset:3072
	v_mov_b32_e32 v15, v79
	v_pk_mul_f32 v[44:45], v[46:47], v[14:15] op_sel_hi:[1,0]
	v_pk_mul_f32 v[46:47], v[48:49], v[14:15] op_sel_hi:[1,0]
	v_add_co_u32_e32 v42, vcc, s41, v42
	ds_write_b64 v167, v[34:35]
	ds_write_b64 v168, v[36:37]
	v_addc_co_u32_e32 v43, vcc, 0, v43, vcc
	s_waitcnt vmcnt(1)
	v_pk_add_f32 v[18:19], v[18:19], 1.0 op_sel_hi:[1,0]
	s_waitcnt vmcnt(0)
	v_pk_fma_f32 v[18:19], v[44:45], v[18:19], v[26:27]
	v_pk_add_f32 v[20:21], v[20:21], 1.0 op_sel_hi:[1,0]
	v_cvt_pk_fp8_f32 v15, v18, v19
	v_pk_fma_f32 v[20:21], v[46:47], v[20:21], v[28:29]
	v_cvt_pk_bf16_f32 v34, v18, v19
	v_add_co_u32_e32 v44, vcc, s41, v16
	v_cvt_pk_fp8_f32 v15, v20, v21 op_sel:[0,0,1]
	v_cvt_pk_bf16_f32 v35, v20, v21
	v_lshlrev_b32_e32 v26, 16, v34
	v_and_b32_e32 v27, 0xffff0000, v34
	v_lshlrev_b32_e32 v28, 16, v35
	v_and_b32_e32 v29, 0xffff0000, v35
	v_sub_f32_e32 v18, v18, v26
	v_sub_f32_e32 v19, v19, v27
	v_sub_f32_e32 v26, v20, v28
	v_sub_f32_e32 v20, v21, v29
	v_cvt_pk_bf16_f32 v36, v18, v19
	v_cvt_pk_bf16_f32 v37, v26, v20
	global_store_dword v150, v15, s[0:1] offset:768
	global_load_dwordx4 v[18:21], v[42:43], off
	v_addc_co_u32_e32 v45, vcc, 0, v17, vcc
	global_load_dwordx4 v[26:29], v[44:45], off
	v_mov_b32_e32 v15, v79
	v_pk_mul_f32 v[16:17], v[38:39], v[14:15] op_sel_hi:[1,0]
	v_pk_mul_f32 v[38:39], v[40:41], v[14:15] op_sel_hi:[1,0]
	ds_write_b64 v176, v[34:35]
	ds_write_b64 v177, v[36:37]
	s_waitcnt vmcnt(1)
; #define LAS __attribute__((address_space(3)))
; __device__ __forceinline__ unsigned cvt_pk_bf16(float lo, float hi) { unsigned r; asm volatile("v_cvt_pk_bf16_f32 %0, %1, %2" : "=v"(r) : "v"(lo), "v"(hi)); return r; }
; __device__ __forceinline__ unsigned pk4_fp8(float a, float b, float c, float d) { int w = 0; w = __builtin_amdgcn_cvt_pk_fp8_f32(a, b, w, false); w = __builtin_amdgcn_cvt_pk_fp8_f32(c, d, w, true); return (unsigned)w; }
; __device__ __forceinline__ float bf_lo(unsigned w) { return __uint_as_float(w << 16); }
; __device__ __forceinline__ void p6_router(Frame& F) {
;     ...
; #pragma unroll
;                 for (int j = 0; j < 8; ++j) { const f32x4 sh = ((const f32x4*)(mod + (size_t)b * 12288 + 6144))[loq + 64 * j], sc = ((const f32x4*)(mod + (size_t)b * 12288 + 8192))[loq + 64 * j];
;                     const f32x4 y = v[j] * rstd * (sc + 1.0f) + sh;
;                     u32x2 wh; wh.x = cvt_pk_bf16(y[0], y[1]); wh.y = cvt_pk_bf16(y[2], y[3]);
;                     const f32x4 yl = {y[0] - bf_lo(wh.x), y[1] - bf_hi(wh.x), y[2] - bf_lo(wh.y), y[3] - bf_hi(wh.y)};
;                     u32x2 wl; wl.x = cvt_pk_bf16(yl[0], yl[1]); wl.y = cvt_pk_bf16(yl[2], yl[3]);
;                     { const int r = 2 * wave + q; LAS unsigned char* rowp = F.lds + r * 4096 + ((((lane >> 1) + 32 * j) ^ r) << 4) + (lane & 1) * 8;
;                       *(LAS u32x2*)rowp = wh; *(LAS u32x2*)(rowp + 65536) = wl; }
;                     U2F[(size_t)t * (DM / 4) + lane + 64 * j] = pk4_fp8(y[0], y[1], y[2], y[3]); }
;             }
;             __builtin_amdgcn_sched_barrier(0);
;             bf16x8 bh[2][2], bl[2][2]; f32x4 cur[2] = {(f32x4){0.f, 0.f, 0.f, 0.f}, (f32x4){0.f, 0.f, 0.f, 0.f}};
;             const bf16_t* wbh = WRH + (size_t)fr * DM + wave * 256 + fq * 8; const bf16_t* wbl = WRL + (size_t)fr * DM + wave * 256 + fq * 8;
; #pragma unroll
;             for (int n = 0; n < 2; ++n) { bh[0][n] = *(const bf16x8*)(wbh + (size_t)(16 * n) * DM); bl[0][n] = *(const bf16x8*)(wbl + (size_t)(16 * n) * DM); }
;             if (rp == 0) {
; #pragma unroll
;                 for (int q = 0; q < 2; ++q)
; #pragma unroll
;                     for (int j = 0; j < 8; ++j) zr[q][j] = ((const u32x2*)(ZB + (size_t)(ta + 2 + q) * DM))[lane + 64 * j];
;             }
;             __syncthreads();
	v_pk_add_f32 v[18:19], v[18:19], 1.0 op_sel_hi:[1,0]
	v_pk_add_f32 v[20:21], v[20:21], 1.0 op_sel_hi:[1,0]
	s_waitcnt vmcnt(0)
	v_pk_fma_f32 v[16:17], v[16:17], v[18:19], v[26:27]
	s_nop 0
	v_cvt_pk_fp8_f32 v15, v16, v17
	v_pk_fma_f32 v[20:21], v[38:39], v[20:21], v[28:29]
	v_cvt_pk_bf16_f32 v34, v16, v17
	s_nop 0
	v_cvt_pk_fp8_f32 v15, v20, v21 op_sel:[0,0,1]
	v_cvt_pk_bf16_f32 v35, v20, v21
	v_lshlrev_b32_e32 v18, 16, v34
	v_and_b32_e32 v19, 0xffff0000, v34
	v_lshlrev_b32_e32 v26, 16, v35
	v_and_b32_e32 v27, 0xffff0000, v35
	v_sub_f32_e32 v16, v16, v18
	v_sub_f32_e32 v17, v17, v19
	v_sub_f32_e32 v18, v20, v26
	v_sub_f32_e32 v19, v21, v27
	v_cvt_pk_bf16_f32 v20, v16, v17
	v_cvt_pk_bf16_f32 v21, v18, v19
	global_store_dword v150, v15, s[0:1] offset:1024
	global_load_dwordx4 v[16:19], v[42:43], off offset:1024
	global_load_dwordx4 v[26:29], v[44:45], off offset:1024
	v_mov_b32_e32 v15, v79
	v_pk_mul_f32 v[30:31], v[30:31], v[14:15] op_sel_hi:[1,0]
	v_pk_mul_f32 v[32:33], v[32:33], v[14:15] op_sel_hi:[1,0]
	ds_write_b64 v178, v[34:35]
	ds_write_b64 v179, v[20:21]
	s_waitcnt vmcnt(1)
	v_pk_add_f32 v[16:17], v[16:17], 1.0 op_sel_hi:[1,0]
	s_waitcnt vmcnt(0)
	v_pk_fma_f32 v[16:17], v[30:31], v[16:17], v[26:27]
	v_pk_add_f32 v[18:19], v[18:19], 1.0 op_sel_hi:[1,0]
	v_cvt_pk_fp8_f32 v15, v16, v17
	v_pk_fma_f32 v[18:19], v[32:33], v[18:19], v[28:29]
	v_cvt_pk_bf16_f32 v20, v16, v17
	s_nop 0
	v_cvt_pk_fp8_f32 v15, v18, v19 op_sel:[0,0,1]
	v_cvt_pk_bf16_f32 v21, v18, v19
	v_lshlrev_b32_e32 v26, 16, v20
	v_and_b32_e32 v27, 0xffff0000, v20
	v_lshlrev_b32_e32 v28, 16, v21
	v_and_b32_e32 v29, 0xffff0000, v21
	v_sub_f32_e32 v16, v16, v26
	v_sub_f32_e32 v17, v17, v27
	v_sub_f32_e32 v26, v18, v28
	v_sub_f32_e32 v18, v19, v29
	v_cvt_pk_bf16_f32 v30, v16, v17
	v_cvt_pk_bf16_f32 v31, v26, v18
	global_store_dword v150, v15, s[0:1] offset:1280
	global_load_dwordx4 v[16:19], v[42:43], off offset:2048
	global_load_dwordx4 v[26:29], v[44:45], off offset:2048
	v_mov_b32_e32 v15, v79
	v_pk_mul_f32 v[22:23], v[22:23], v[14:15] op_sel_hi:[1,0]
	v_pk_mul_f32 v[24:25], v[24:25], v[14:15] op_sel_hi:[1,0]
	ds_write_b64 v180, v[20:21]
	ds_write_b64 v181, v[30:31]
	s_waitcnt vmcnt(1)
	v_pk_add_f32 v[16:17], v[16:17], 1.0 op_sel_hi:[1,0]
	s_waitcnt vmcnt(0)
	v_pk_fma_f32 v[16:17], v[22:23], v[16:17], v[26:27]
	v_pk_add_f32 v[18:19], v[18:19], 1.0 op_sel_hi:[1,0]
	v_cvt_pk_fp8_f32 v15, v16, v17
	v_pk_fma_f32 v[18:19], v[24:25], v[18:19], v[28:29]
	v_cvt_pk_bf16_f32 v24, v16, v17
	s_nop 0
	v_cvt_pk_fp8_f32 v15, v18, v19 op_sel:[0,0,1]
	v_cvt_pk_bf16_f32 v25, v18, v19
	v_lshlrev_b32_e32 v20, 16, v24
	v_and_b32_e32 v21, 0xffff0000, v24
	v_lshlrev_b32_e32 v22, 16, v25
	v_and_b32_e32 v23, 0xffff0000, v25
	v_sub_f32_e32 v16, v16, v20
	v_sub_f32_e32 v17, v17, v21
	v_sub_f32_e32 v20, v18, v22
	v_sub_f32_e32 v18, v19, v23
	v_cvt_pk_bf16_f32 v26, v16, v17
	v_cvt_pk_bf16_f32 v27, v20, v18
	global_store_dword v150, v15, s[0:1] offset:1536
	global_load_dwordx4 v[16:19], v[42:43], off offset:3072
	global_load_dwordx4 v[20:23], v[44:45], off offset:3072
	v_pk_mul_f32 v[12:13], v[12:13], v[14:15] op_sel_hi:[1,0]
	v_pk_mul_f32 v[10:11], v[10:11], v[14:15] op_sel_hi:[1,0]
	ds_write_b64 v184, v[24:25]
	ds_write_b64 v185, v[26:27]
	s_waitcnt vmcnt(1)
	v_pk_add_f32 v[16:17], v[16:17], 1.0 op_sel_hi:[1,0]
	s_waitcnt vmcnt(0)
	v_pk_fma_f32 v[12:13], v[12:13], v[16:17], v[20:21]
	v_pk_add_f32 v[14:15], v[18:19], 1.0 op_sel_hi:[1,0]
	v_cvt_pk_fp8_f32 v79, v12, v13
	v_pk_fma_f32 v[10:11], v[10:11], v[14:15], v[22:23]
	v_cvt_pk_bf16_f32 v14, v12, v13
	s_nop 0
	v_cvt_pk_fp8_f32 v79, v10, v11 op_sel:[0,0,1]
	v_lshlrev_b32_e32 v16, 16, v14
	v_and_b32_e32 v17, 0xffff0000, v14
	v_cvt_pk_bf16_f32 v15, v10, v11
	v_sub_f32_e32 v12, v12, v16
	v_lshlrev_b32_e32 v18, 16, v15
	v_and_b32_e32 v19, 0xffff0000, v15
	v_sub_f32_e32 v13, v13, v17
	v_sub_f32_e32 v16, v10, v18
	v_sub_f32_e32 v17, v11, v19
	v_cvt_pk_bf16_f32 v12, v12, v13
	v_cvt_pk_bf16_f32 v13, v16, v17
	ds_write_b64 v182, v[14:15]
	ds_write_b64 v183, v[12:13]
	global_store_dword v150, v79, s[0:1] offset:1792
	global_load_dwordx4 v[10:13], v[84:85], off
	global_load_dwordx4 v[14:17], v[74:75], off
	global_load_dwordx4 v[18:21], v[86:87], off
	global_load_dwordx4 v[22:25], v[76:77], off
	s_waitcnt lgkmcnt(0)
	s_barrier
; #define LAS __attribute__((address_space(3)))
; __device__ __forceinline__ void p6_router(Frame& F) {
;     ...
; #pragma unroll
;             for (int ks = 0; ks < 8; ++ks) {
;                 if (ks < 7) {
; #pragma unroll
;                     for (int n = 0; n < 2; ++n) { bh[(ks + 1) & 1][n] = *(const bf16x8*)(wbh + (size_t)(16 * n) * DM + (ks + 1) * 32); bl[(ks + 1) & 1][n] = *(const bf16x8*)(wbl + (size_t)(16 * n) * DM + (ks + 1) * 32); }
;                 }
;                 const LAS unsigned char* ap = F.lds + fr * 4096 + (((wave * 32 + ks * 4 + fq) ^ fr) << 4);
;                 const bf16x8 ah = *(const LAS bf16x8*)ap, al = *(const LAS bf16x8*)(ap + 65536);
; #pragma unroll
;                 for (int n = 0; n < 2; ++n) {
;                     cur[n] = __builtin_amdgcn_mfma_f32_16x16x32_bf16(ah, bh[ks & 1][n], cur[n], 0, 0, 0);
;                     cur[n] = __builtin_amdgcn_mfma_f32_16x16x32_bf16(ah, bl[ks & 1][n], cur[n], 0, 0, 0);
;                     cur[n] = __builtin_amdgcn_mfma_f32_16x16x32_bf16(al, bh[ks & 1][n], cur[n], 0, 0, 0);
;                 }
;                 __builtin_amdgcn_sched_barrier(0);
;             }
;             accp[0] = cur[0]; accp[1] = cur[1];
;             __syncthreads();
;         };
;         pass(0, acc[0]); pass(1, acc[1]);
;     }
;     LAS float* red = (LAS float*)F.lds;
;     LAS float* lg = red + 8 * 1024;
;     LAS int* aE = (LAS int*)(lg + 1024); LAS int* aP = aE + 128; LAS float* aW = (LAS float*)(aP + 128);
; #pragma unroll
;     for (int a = 0; a < 2; ++a)
; #pragma unroll
;         for (int n = 0; n < 2; ++n)
; #pragma unroll
;             for (int i = 0; i < 4; ++i) { const int m = 4 * fq + i; red[wave * 1024 + (4 * (m >> 1) + 2 * a + (m & 1)) * 32 + 16 * n + fr] = acc[a][n][i]; }
;     __syncthreads();
;     for (int i = tid; i < 1024; i += 512) { float s = F.in[I_BR][i & 31];
	ds_read_b128 v[26:29], v186
	ds_read_b128 v[30:33], v187
	s_waitcnt vmcnt(3) lgkmcnt(1)
	v_mfma_f32_16x16x32_bf16 v[34:37], v[26:29], v[10:13], 0
	s_waitcnt vmcnt(2)
	v_mfma_f32_16x16x32_bf16 v[38:41], v[26:29], v[14:17], 0
	s_waitcnt vmcnt(1)
	v_mfma_f32_16x16x32_bf16 v[18:21], v[26:29], v[18:21], v[34:37]
	s_waitcnt vmcnt(0)
	v_mfma_f32_16x16x32_bf16 v[22:25], v[26:29], v[22:25], v[38:41]
	global_load_dwordx4 v[26:29], v[80:81], off offset:64
	s_nop 0
	global_load_dwordx4 v[34:37], v[82:83], off offset:64
	s_waitcnt lgkmcnt(0)
	v_mfma_f32_16x16x32_bf16 v[10:13], v[30:33], v[10:13], v[18:21]
	s_nop 2
	global_load_dwordx4 v[18:21], v[74:75], off offset:64
	global_load_dwordx4 v[38:41], v[76:77], off offset:64
	v_mfma_f32_16x16x32_bf16 v[14:17], v[30:33], v[14:17], v[22:25]
	s_nop 2
	ds_read_b128 v[22:25], v188
	ds_read_b128 v[30:33], v189
	s_waitcnt vmcnt(3) lgkmcnt(1)
	v_mfma_f32_16x16x32_bf16 v[10:13], v[22:25], v[26:29], v[10:13]
	s_waitcnt vmcnt(1)
	v_mfma_f32_16x16x32_bf16 v[14:17], v[22:25], v[18:21], v[14:17]
	v_mfma_f32_16x16x32_bf16 v[10:13], v[22:25], v[34:37], v[10:13]
	s_waitcnt lgkmcnt(0)
	v_mfma_f32_16x16x32_bf16 v[10:13], v[30:33], v[26:29], v[10:13]
	global_load_dwordx4 v[26:29], v[80:81], off offset:128
	global_load_dwordx4 v[34:37], v[82:83], off offset:128
	s_waitcnt vmcnt(2)
	v_mfma_f32_16x16x32_bf16 v[14:17], v[22:25], v[38:41], v[14:17]
	global_load_dwordx4 v[22:25], v[74:75], off offset:128
	global_load_dwordx4 v[38:41], v[76:77], off offset:128
	v_mfma_f32_16x16x32_bf16 v[14:17], v[30:33], v[18:21], v[14:17]
	ds_read_b128 v[18:21], v190
	ds_read_b128 v[30:33], v191
	s_waitcnt vmcnt(3) lgkmcnt(1)
	v_mfma_f32_16x16x32_bf16 v[10:13], v[18:21], v[26:29], v[10:13]
	s_waitcnt vmcnt(1)
	v_mfma_f32_16x16x32_bf16 v[14:17], v[18:21], v[22:25], v[14:17]
	v_mfma_f32_16x16x32_bf16 v[10:13], v[18:21], v[34:37], v[10:13]
	s_waitcnt lgkmcnt(0)
	v_mfma_f32_16x16x32_bf16 v[10:13], v[30:33], v[26:29], v[10:13]
	global_load_dwordx4 v[26:29], v[80:81], off offset:192
	global_load_dwordx4 v[34:37], v[82:83], off offset:192
	s_waitcnt vmcnt(2)
	v_mfma_f32_16x16x32_bf16 v[14:17], v[18:21], v[38:41], v[14:17]
	global_load_dwordx4 v[18:21], v[74:75], off offset:192
	global_load_dwordx4 v[38:41], v[76:77], off offset:192
	v_mfma_f32_16x16x32_bf16 v[14:17], v[30:33], v[22:25], v[14:17]
	ds_read_b128 v[22:25], v192
	ds_read_b128 v[30:33], v193
	s_waitcnt vmcnt(3) lgkmcnt(1)
	v_mfma_f32_16x16x32_bf16 v[10:13], v[22:25], v[26:29], v[10:13]
	s_waitcnt vmcnt(1)
	v_mfma_f32_16x16x32_bf16 v[14:17], v[22:25], v[18:21], v[14:17]
	v_mfma_f32_16x16x32_bf16 v[10:13], v[22:25], v[34:37], v[10:13]
	s_waitcnt lgkmcnt(0)
	v_mfma_f32_16x16x32_bf16 v[10:13], v[30:33], v[26:29], v[10:13]
	global_load_dwordx4 v[26:29], v[80:81], off offset:256
	global_load_dwordx4 v[34:37], v[82:83], off offset:256
	s_waitcnt vmcnt(2)
	v_mfma_f32_16x16x32_bf16 v[14:17], v[22:25], v[38:41], v[14:17]
	global_load_dwordx4 v[22:25], v[74:75], off offset:256
	global_load_dwordx4 v[38:41], v[76:77], off offset:256
	v_mfma_f32_16x16x32_bf16 v[14:17], v[30:33], v[18:21], v[14:17]
	ds_read_b128 v[18:21], v194
	ds_read_b128 v[30:33], v195
	s_waitcnt vmcnt(3) lgkmcnt(1)
	v_mfma_f32_16x16x32_bf16 v[10:13], v[18:21], v[26:29], v[10:13]
	s_waitcnt vmcnt(1)
	v_mfma_f32_16x16x32_bf16 v[14:17], v[18:21], v[22:25], v[14:17]
	v_mfma_f32_16x16x32_bf16 v[10:13], v[18:21], v[34:37], v[10:13]
	s_waitcnt lgkmcnt(0)
	v_mfma_f32_16x16x32_bf16 v[10:13], v[30:33], v[26:29], v[10:13]
	global_load_dwordx4 v[26:29], v[80:81], off offset:320
	global_load_dwordx4 v[34:37], v[82:83], off offset:320
	s_waitcnt vmcnt(2)
	v_mfma_f32_16x16x32_bf16 v[14:17], v[18:21], v[38:41], v[14:17]
	global_load_dwordx4 v[18:21], v[74:75], off offset:320
	global_load_dwordx4 v[38:41], v[76:77], off offset:320
	v_mfma_f32_16x16x32_bf16 v[14:17], v[30:33], v[22:25], v[14:17]
	ds_read_b128 v[22:25], v196
	ds_read_b128 v[30:33], v197
	s_waitcnt vmcnt(3) lgkmcnt(1)
	v_mfma_f32_16x16x32_bf16 v[10:13], v[22:25], v[26:29], v[10:13]
	s_waitcnt vmcnt(1)
	v_mfma_f32_16x16x32_bf16 v[14:17], v[22:25], v[18:21], v[14:17]
	v_mfma_f32_16x16x32_bf16 v[10:13], v[22:25], v[34:37], v[10:13]
	s_waitcnt lgkmcnt(0)
	v_mfma_f32_16x16x32_bf16 v[10:13], v[30:33], v[26:29], v[10:13]
	global_load_dwordx4 v[26:29], v[80:81], off offset:384
	global_load_dwordx4 v[34:37], v[82:83], off offset:384
	s_waitcnt vmcnt(2)
	v_mfma_f32_16x16x32_bf16 v[14:17], v[22:25], v[38:41], v[14:17]
	global_load_dwordx4 v[22:25], v[74:75], off offset:384
	global_load_dwordx4 v[38:41], v[76:77], off offset:384
	v_mfma_f32_16x16x32_bf16 v[14:17], v[30:33], v[18:21], v[14:17]
	ds_read_b128 v[18:21], v199
	ds_read_b128 v[30:33], v201
	s_waitcnt vmcnt(3) lgkmcnt(1)
	v_mfma_f32_16x16x32_bf16 v[10:13], v[18:21], v[26:29], v[10:13]
	s_waitcnt vmcnt(1)
	v_mfma_f32_16x16x32_bf16 v[14:17], v[18:21], v[22:25], v[14:17]
	v_mfma_f32_16x16x32_bf16 v[10:13], v[18:21], v[34:37], v[10:13]
	s_waitcnt lgkmcnt(0)
	v_mfma_f32_16x16x32_bf16 v[10:13], v[30:33], v[26:29], v[10:13]
	global_load_dwordx4 v[26:29], v[80:81], off offset:448
	global_load_dwordx4 v[34:37], v[82:83], off offset:448
	s_waitcnt vmcnt(2)
	v_mfma_f32_16x16x32_bf16 v[14:17], v[18:21], v[38:41], v[14:17]
	global_load_dwordx4 v[18:21], v[74:75], off offset:448
	global_load_dwordx4 v[38:41], v[76:77], off offset:448
	v_mfma_f32_16x16x32_bf16 v[14:17], v[30:33], v[22:25], v[14:17]
	ds_read_b128 v[22:25], v198
	ds_read_b128 v[30:33], v200
	s_waitcnt vmcnt(3) lgkmcnt(1)
	v_mfma_f32_16x16x32_bf16 v[10:13], v[22:25], v[26:29], v[10:13]
	s_waitcnt vmcnt(1)
	v_mfma_f32_16x16x32_bf16 v[14:17], v[22:25], v[18:21], v[14:17]
	v_mfma_f32_16x16x32_bf16 v[10:13], v[22:25], v[34:37], v[10:13]
	s_waitcnt vmcnt(0)
	v_mfma_f32_16x16x32_bf16 v[14:17], v[22:25], v[38:41], v[14:17]
	s_waitcnt lgkmcnt(0)
	v_mfma_f32_16x16x32_bf16 v[10:13], v[30:33], v[26:29], v[10:13]
	v_mfma_f32_16x16x32_bf16 v[14:17], v[30:33], v[18:21], v[14:17]
	s_lshl_b32 s0, s46, 12
	v_lshlrev_b32_e32 v18, 10, v154
	s_add_i32 s0, s0, 0
	v_lshlrev_b32_e32 v19, 2, v151
	v_add3_u32 v18, s0, v18, v19
	s_barrier
	ds_write2_b32 v18, v2, v6 offset1:16
	ds_write2_b32 v18, v3, v7 offset0:32 offset1:48
	ds_write2_b32 v18, v4, v8 offset0:128 offset1:144
	ds_write2_b32 v18, v5, v9 offset0:160 offset1:176
	ds_write2_b32 v18, v10, v14 offset0:64 offset1:80
	ds_write2_b32 v18, v11, v15 offset0:96 offset1:112
	ds_write2_b32 v18, v12, v16 offset0:192 offset1:208
	ds_write2_b32 v18, v13, v17 offset0:224 offset1:240
	v_and_b32_e32 v5, 31, v0
	v_lshlrev_b32_e32 v2, 2, v5
	s_waitcnt lgkmcnt(0)
	s_barrier
	global_load_dword v2, v2, s[14:15]
	v_or_b32_e32 v3, 0xfffffe00, v0
	v_lshl_add_u32 v4, v0, 2, 0
	s_mov_b64 s[0:1], 0

; __device__ __forceinline__ float bf_lo(unsigned w) { return __uint_as_float(w << 16); }
; __device__ __forceinline__ float bf_hi(unsigned w) { return __uint_as_float(w & 0xffff0000u); }
; __device__ __forceinline__ void p9_final(Frame& F) {
;     ...
;     for (int t = gw; t < NTOK; t += NGW) {
;         const int b = t >> 12;
;         const i32x4 ae = ae_n, ap = ap_n; const f32x4 aw = aw_n;
;         { const int tn = (t + NGW < NTOK) ? t + NGW : t;
;           ae_n = ((const i32x4*)(F.ws + WS_ASG_E))[tn]; ap_n = ((const i32x4*)(F.ws + WS_ASG_P))[tn]; aw_n = ((const f32x4*)(F.ws + WS_ASG_W))[tn]; }
;         const u32x2* yr[4];
; #pragma unroll
;         for (int k = 0; k < 4; ++k) yr[k] = (const u32x2*)(Y + ((size_t)tab[352 + ae[k]] * 256 + ap[k]) * DM) + lane;
;         u32x2 q[4][8]; f32x4 x1[8];
; #pragma unroll
;         for (int k = 0; k < 4; ++k)
; #pragma unroll
;             for (int j = 0; j < 8; ++j) q[k][j] = yr[k][64 * j];
; #pragma unroll
;         for (int j = 0; j < 8; ++j) { const u32x2 xb = ((const u32x2*)(X1 + (size_t)t * DM))[lane + 64 * j]; x1[j] = (f32x4){bf_lo(xb.x), bf_hi(xb.x), bf_lo(xb.y), bf_hi(xb.y)}; }
.LBB0_1211:
	global_load_dwordx2 v[50:51], v[48:49], off
	global_load_dwordx2 v[52:53], v[48:49], off offset:512
	global_load_dwordx2 v[54:55], v[48:49], off offset:1024
	global_load_dwordx2 v[56:57], v[48:49], off offset:1536
	global_load_dwordx2 v[58:59], v[48:49], off offset:2048
	global_load_dwordx2 v[60:61], v[48:49], off offset:2560
	global_load_dwordx2 v[62:63], v[48:49], off offset:3072
	global_load_dwordx2 v[64:65], v[48:49], off offset:3584
	s_add_i32 s28, s14, s4
	s_cmpk_lt_i32 s28, 0x2000
	s_cselect_b64 s[24:25], -1, 0
	v_lshlrev_b32_e32 v4, 2, v4
	v_lshlrev_b32_e32 v6, 2, v6
	s_and_b64 s[30:31], s[24:25], exec
	v_lshlrev_b32_e32 v5, 2, v5
	v_lshlrev_b32_e32 v7, 2, v7
	v_add_u32_e32 v4, s5, v4
	v_add_u32_e32 v8, s5, v6
	s_cselect_b32 s30, s28, s14
	global_load_dwordx4 v[16:19], v[26:27], off
	global_load_dwordx4 v[20:23], v[28:29], off
	v_add_u32_e32 v5, s5, v5
	v_add_u32_e32 v7, s5, v7
	ds_read_b32 v4, v4
	ds_read_b32 v6, v5
	ds_read_b32 v8, v8
	ds_read_b32 v10, v7
	s_ashr_i32 s31, s30, 31
	s_lshl_b64 s[30:31], s[30:31], 4
	s_add_u32 s36, s34, s30
	s_waitcnt lgkmcnt(3)
	v_ashrrev_i32_e32 v5, 31, v4
	s_waitcnt lgkmcnt(2)
	v_ashrrev_i32_e32 v7, 31, v6
	s_addc_u32 s37, s35, s31
	v_lshlrev_b64 v[12:13], 20, v[4:5]
	v_lshlrev_b64 v[14:15], 20, v[6:7]
	global_load_dwordx4 v[4:7], v25, s[36:37]
	s_add_u32 s36, s27, s30
	s_addc_u32 s37, s33, s31
	s_add_u32 s30, s13, s30
	s_mov_b32 s16, s0
	s_waitcnt lgkmcnt(1)
	v_ashrrev_i32_e32 v9, 31, v8
	s_waitcnt lgkmcnt(0)
	v_ashrrev_i32_e32 v11, 31, v10
	s_addc_u32 s31, s26, s31
	s_ashr_i32 s17, s0, 31
	s_mov_b32 s18, s1
	s_mov_b32 s20, s2
	s_mov_b32 s22, s3
	v_lshlrev_b64 v[8:9], 20, v[8:9]
	v_lshlrev_b64 v[10:11], 20, v[10:11]
	v_lshl_add_u64 v[84:85], s[6:7], 0, v[12:13]
	s_ashr_i32 s19, s1, 31
	s_ashr_i32 s21, s2, 31
	s_ashr_i32 s23, s3, 31
	s_lshl_b64 s[0:1], s[16:17], 12
	v_lshl_add_u64 v[86:87], s[6:7], 0, v[14:15]
	v_lshl_add_u64 v[88:89], s[6:7], 0, v[8:9]
	v_lshl_add_u64 v[90:91], s[6:7], 0, v[10:11]
	s_lshl_b64 s[2:3], s[18:19], 12
	s_lshl_b64 s[16:17], s[20:21], 12
	s_lshl_b64 s[18:19], s[22:23], 12
	v_lshl_add_u64 v[84:85], v[84:85], 0, s[0:1]
	v_lshlrev_b32_e32 v81, 3, v170
	v_lshl_add_u64 v[86:87], v[86:87], 0, s[2:3]
	v_lshl_add_u64 v[88:89], v[88:89], 0, s[16:17]
	v_lshl_add_u64 v[90:91], v[90:91], 0, s[18:19]
	v_readfirstlane_b32 s0, v84
	v_readfirstlane_b32 s1, v85
	global_load_dwordx4 v[8:11], v25, s[36:37]
	global_load_dwordx4 v[12:15], v25, s[30:31]
	v_readfirstlane_b32 s2, v86
	v_readfirstlane_b32 s3, v87
	v_readfirstlane_b32 s16, v88
	v_readfirstlane_b32 s17, v89
	v_readfirstlane_b32 s18, v90
	v_readfirstlane_b32 s19, v91
	global_load_dwordx2 v[102:103], v81, s[0:1]
	global_load_dwordx2 v[104:105], v81, s[2:3]
	s_nop 0
	global_load_dwordx2 v[106:107], v81, s[16:17]
	s_nop 0
	global_load_dwordx2 v[108:109], v81, s[18:19]
	global_load_dwordx2 v[110:111], v81, s[0:1] offset:512
	global_load_dwordx2 v[112:113], v81, s[0:1] offset:1024
	global_load_dwordx2 v[114:115], v81, s[0:1] offset:1536
	global_load_dwordx2 v[116:117], v81, s[2:3] offset:512
	global_load_dwordx2 v[118:119], v81, s[16:17] offset:512
	global_load_dwordx2 v[120:121], v81, s[0:1] offset:2048
	global_load_dwordx2 v[122:123], v81, s[0:1] offset:2560
	global_load_dwordx2 v[124:125], v81, s[0:1] offset:3072
	global_load_dwordx2 v[126:127], v81, s[0:1] offset:3584
	global_load_dwordx2 v[128:129], v81, s[18:19] offset:512
	global_load_dwordx2 v[130:131], v81, s[2:3] offset:1024
	global_load_dwordx2 v[132:133], v81, s[2:3] offset:1536
	global_load_dwordx2 v[134:135], v81, s[2:3] offset:2048
	global_load_dwordx2 v[136:137], v81, s[2:3] offset:2560
	global_load_dwordx2 v[138:139], v81, s[2:3] offset:3072
	global_load_dwordx2 v[140:141], v81, s[2:3] offset:3584
	global_load_dwordx2 v[142:143], v81, s[16:17] offset:1024
	global_load_dwordx2 v[144:145], v81, s[16:17] offset:1536
	global_load_dwordx2 v[146:147], v81, s[16:17] offset:2048
	global_load_dwordx2 v[148:149], v81, s[16:17] offset:2560
	global_load_dwordx2 v[150:151], v81, s[16:17] offset:3072
	global_load_dwordx2 v[152:153], v81, s[16:17] offset:3584
	global_load_dwordx2 v[154:155], v81, s[18:19] offset:1024
	global_load_dwordx2 v[156:157], v81, s[18:19] offset:1536
	global_load_dwordx2 v[158:159], v81, s[18:19] offset:2048
	global_load_dwordx2 v[160:161], v81, s[18:19] offset:2560
	global_load_dwordx2 v[162:163], v81, s[18:19] offset:3072
	global_load_dwordx2 v[164:165], v81, s[18:19] offset:3584
	s_ashr_i32 s14, s14, 12
	s_mul_hi_i32 s20, s14, 0xc000
	s_mul_i32 s14, s14, 0xc000
	s_add_u32 s14, s82, s14
	s_addc_u32 s20, s83, s20
	s_add_u32 s0, s14, 0x10a000
	v_lshlrev_b32_e32 v82, 4, v170
	s_addc_u32 s1, s20, 0
	s_waitcnt vmcnt(44)
	v_lshlrev_b32_e32 v166, 16, v50
	v_and_b32_e32 v167, 0xffff0000, v50
	v_lshlrev_b32_e32 v168, 16, v51
	v_and_b32_e32 v169, 0xffff0000, v51
	s_waitcnt vmcnt(40)
	v_lshlrev_b32_e32 v184, 16, v58
	v_and_b32_e32 v185, 0xffff0000, v58
	v_lshlrev_b32_e32 v186, 16, v59
	v_and_b32_e32 v187, 0xffff0000, v59
	v_lshlrev_b32_e32 v176, 16, v54
	v_and_b32_e32 v177, 0xffff0000, v54
	v_lshlrev_b32_e32 v178, 16, v55
	v_and_b32_e32 v179, 0xffff0000, v55
	s_waitcnt vmcnt(39)
	v_lshlrev_b32_e32 v188, 16, v60
	v_and_b32_e32 v189, 0xffff0000, v60
	v_lshlrev_b32_e32 v190, 16, v61
	v_and_b32_e32 v191, 0xffff0000, v61
	v_lshlrev_b32_e32 v172, 16, v52
	v_and_b32_e32 v173, 0xffff0000, v52
	v_lshlrev_b32_e32 v174, 16, v53
	v_and_b32_e32 v175, 0xffff0000, v53
	v_lshlrev_b32_e32 v180, 16, v56
	v_and_b32_e32 v181, 0xffff0000, v56
	v_lshlrev_b32_e32 v182, 16, v57
	v_and_b32_e32 v183, 0xffff0000, v57
	global_load_dwordx4 v[82:85], v82, s[0:1]
	s_nop 0
	global_load_dwordx4 v[86:89], v72, s[0:1]
	global_load_dwordx4 v[90:93], v73, s[0:1]
	global_load_dwordx4 v[94:97], v74, s[0:1]
	global_load_dwordx4 v[98:101], v75, s[0:1]
	v_mov_b32_e32 v24, v3
	s_waitcnt vmcnt(43)
; __device__ __forceinline__ float bf_lo(unsigned w) { return __uint_as_float(w << 16); }
; __device__ __forceinline__ float bf_hi(unsigned w) { return __uint_as_float(w & 0xffff0000u); }
; __device__ __forceinline__ void p9_final(Frame& F) {
;     ...
;         for (int j = 0; j < 8; ++j) { const u32x2 xb = ((const u32x2*)(X1 + (size_t)t * DM))[lane + 64 * j]; x1[j] = (f32x4){bf_lo(xb.x), bf_hi(xb.x), bf_lo(xb.y), bf_hi(xb.y)}; }
;         float s = 0.f; f32x4 v[8];
; #pragma unroll
;         for (int j = 0; j < 8; ++j) { f32x4 y = {0.f, 0.f, 0.f, 0.f};
; #pragma unroll
;             for (int k = 0; k < 4; ++k) { const float w = aw[k]; y[0] += w * bf_lo(q[k][j].x); y[1] += w * bf_hi(q[k][j].x); y[2] += w * bf_lo(q[k][j].y); y[3] += w * bf_hi(q[k][j].y); }
	v_lshlrev_b32_e32 v192, 16, v62
	v_and_b32_e32 v193, 0xffff0000, v62
	v_lshlrev_b32_e32 v62, 16, v63
	v_and_b32_e32 v63, 0xffff0000, v63
	s_waitcnt vmcnt(42)
	v_lshlrev_b32_e32 v194, 16, v64
	v_and_b32_e32 v195, 0xffff0000, v64
	v_lshlrev_b32_e32 v64, 16, v65
	v_and_b32_e32 v65, 0xffff0000, v65
	v_lshl_add_u64 v[48:49], v[48:49], 0, s[10:11]
	s_mov_b32 s14, s28
	s_waitcnt vmcnt(36)
	v_lshlrev_b32_e32 v50, 16, v102
	v_and_b32_e32 v51, 0xffff0000, v102
	v_lshlrev_b32_e32 v54, 16, v103
	v_and_b32_e32 v55, 0xffff0000, v103
	s_waitcnt vmcnt(32)
	v_lshlrev_b32_e32 v58, 16, v110
	v_and_b32_e32 v59, 0xffff0000, v110
	v_lshlrev_b32_e32 v110, 16, v111
	s_waitcnt vmcnt(29)
	v_lshlrev_b32_e32 v60, 16, v116
	v_and_b32_e32 v61, 0xffff0000, v116
	v_and_b32_e32 v111, 0xffff0000, v111
	v_lshlrev_b32_e32 v200, 16, v112
	v_and_b32_e32 v201, 0xffff0000, v112
	v_pk_fma_f32 v[58:59], v[0:1], v[58:59], 0 op_sel_hi:[0,1,0]
	v_lshlrev_b32_e32 v52, 16, v104
	v_and_b32_e32 v53, 0xffff0000, v104
	v_lshlrev_b32_e32 v56, 16, v105
	v_and_b32_e32 v57, 0xffff0000, v105
	v_lshlrev_b32_e32 v116, 16, v117
	v_and_b32_e32 v117, 0xffff0000, v117
	s_waitcnt vmcnt(22)
	v_lshlrev_b32_e32 v202, 16, v130
	v_and_b32_e32 v203, 0xffff0000, v130
	v_pk_fma_f32 v[50:51], v[0:1], v[50:51], 0 op_sel_hi:[0,1,0]
	v_pk_fma_f32 v[54:55], v[0:1], v[54:55], 0 op_sel_hi:[0,1,0]
	v_pk_fma_f32 v[252:253], v[0:1], v[60:61], v[58:59] op_sel:[1,0,0]
	v_pk_fma_f32 v[58:59], v[0:1], v[110:111], 0 op_sel_hi:[0,1,0]
	v_pk_fma_f32 v[60:61], v[0:1], v[200:201], 0 op_sel_hi:[0,1,0]
	v_pk_fma_f32 v[248:249], v[0:1], v[52:53], v[50:51] op_sel:[1,0,0]
	global_load_dwordx4 v[50:53], v76, s[0:1]
	v_pk_fma_f32 v[250:251], v[0:1], v[56:57], v[54:55] op_sel:[1,0,0]
	global_load_dwordx4 v[54:57], v77, s[0:1]
	v_pk_fma_f32 v[110:111], v[0:1], v[116:117], v[58:59] op_sel:[1,0,0]
	v_pk_fma_f32 v[116:117], v[0:1], v[202:203], v[60:61] op_sel:[1,0,0]
	global_load_dwordx4 v[58:61], v78, s[0:1]
	v_lshlrev_b32_e32 v112, 16, v113
	v_and_b32_e32 v113, 0xffff0000, v113
	v_lshlrev_b32_e32 v208, 16, v114
	v_and_b32_e32 v209, 0xffff0000, v114
	v_lshlrev_b32_e32 v114, 16, v115
	v_and_b32_e32 v115, 0xffff0000, v115
	v_lshlrev_b32_e32 v216, 16, v120
	v_and_b32_e32 v217, 0xffff0000, v120
	v_lshlrev_b32_e32 v120, 16, v121
	v_and_b32_e32 v121, 0xffff0000, v121
	v_lshlrev_b32_e32 v224, 16, v122
	v_and_b32_e32 v225, 0xffff0000, v122
	v_lshlrev_b32_e32 v122, 16, v123
	v_and_b32_e32 v123, 0xffff0000, v123
	v_lshlrev_b32_e32 v232, 16, v124
	v_and_b32_e32 v233, 0xffff0000, v124
	v_lshlrev_b32_e32 v124, 16, v125
	v_and_b32_e32 v125, 0xffff0000, v125
	v_lshlrev_b32_e32 v240, 16, v126
	v_and_b32_e32 v241, 0xffff0000, v126
	v_lshlrev_b32_e32 v126, 16, v127
	v_and_b32_e32 v127, 0xffff0000, v127
	v_lshlrev_b32_e32 v196, 16, v106
	v_and_b32_e32 v197, 0xffff0000, v106
	v_lshlrev_b32_e32 v102, 16, v107
	v_and_b32_e32 v103, 0xffff0000, v107
	v_lshlrev_b32_e32 v106, 16, v118
	v_and_b32_e32 v107, 0xffff0000, v118
	v_lshlrev_b32_e32 v118, 16, v119
	v_and_b32_e32 v119, 0xffff0000, v119
	v_lshlrev_b32_e32 v130, 16, v131
	v_and_b32_e32 v131, 0xffff0000, v131
	s_waitcnt vmcnt(24)
	v_lshlrev_b32_e32 v210, 16, v132
	v_and_b32_e32 v211, 0xffff0000, v132
	v_lshlrev_b32_e32 v132, 16, v133
	v_and_b32_e32 v133, 0xffff0000, v133
	s_waitcnt vmcnt(23)
	v_lshlrev_b32_e32 v218, 16, v134
	v_and_b32_e32 v219, 0xffff0000, v134
	v_lshlrev_b32_e32 v134, 16, v135
	v_and_b32_e32 v135, 0xffff0000, v135
	s_waitcnt vmcnt(22)
	v_lshlrev_b32_e32 v226, 16, v136
	v_and_b32_e32 v227, 0xffff0000, v136
	v_lshlrev_b32_e32 v136, 16, v137
	v_and_b32_e32 v137, 0xffff0000, v137
	s_waitcnt vmcnt(21)
	v_lshlrev_b32_e32 v234, 16, v138
	v_and_b32_e32 v235, 0xffff0000, v138
	v_lshlrev_b32_e32 v138, 16, v139
	v_and_b32_e32 v139, 0xffff0000, v139
	s_waitcnt vmcnt(20)
	v_lshlrev_b32_e32 v242, 16, v140
	v_and_b32_e32 v243, 0xffff0000, v140
	v_lshlrev_b32_e32 v140, 16, v141
	v_and_b32_e32 v141, 0xffff0000, v141
	v_pk_fma_f32 v[112:113], v[0:1], v[112:113], 0 op_sel_hi:[0,1,0]
	v_pk_fma_f32 v[200:201], v[0:1], v[208:209], 0 op_sel_hi:[0,1,0]
	v_pk_fma_f32 v[114:115], v[0:1], v[114:115], 0 op_sel_hi:[0,1,0]
	v_pk_fma_f32 v[202:203], v[0:1], v[216:217], 0 op_sel_hi:[0,1,0]
	v_pk_fma_f32 v[120:121], v[0:1], v[120:121], 0 op_sel_hi:[0,1,0]
	v_pk_fma_f32 v[208:209], v[0:1], v[224:225], 0 op_sel_hi:[0,1,0]
	v_pk_fma_f32 v[122:123], v[0:1], v[122:123], 0 op_sel_hi:[0,1,0]
	v_pk_fma_f32 v[216:217], v[0:1], v[232:233], 0 op_sel_hi:[0,1,0]
	v_pk_fma_f32 v[124:125], v[0:1], v[124:125], 0 op_sel_hi:[0,1,0]
	v_pk_fma_f32 v[224:225], v[0:1], v[240:241], 0 op_sel_hi:[0,1,0]
	v_pk_fma_f32 v[126:127], v[0:1], v[126:127], 0 op_sel_hi:[0,1,0]
	v_lshlrev_b32_e32 v198, 16, v108
	v_and_b32_e32 v199, 0xffff0000, v108
	v_lshlrev_b32_e32 v104, 16, v109
	v_and_b32_e32 v105, 0xffff0000, v109
	v_lshlrev_b32_e32 v108, 16, v128
	v_and_b32_e32 v109, 0xffff0000, v128
	v_lshlrev_b32_e32 v128, 16, v129
	v_and_b32_e32 v129, 0xffff0000, v129
	s_waitcnt vmcnt(19)
	v_lshlrev_b32_e32 v204, 16, v142
	v_and_b32_e32 v205, 0xffff0000, v142
	v_lshlrev_b32_e32 v142, 16, v143
	v_and_b32_e32 v143, 0xffff0000, v143
	s_waitcnt vmcnt(18)
	v_lshlrev_b32_e32 v212, 16, v144
	v_and_b32_e32 v213, 0xffff0000, v144
	v_lshlrev_b32_e32 v144, 16, v145
	v_and_b32_e32 v145, 0xffff0000, v145
	s_waitcnt vmcnt(17)
	v_lshlrev_b32_e32 v220, 16, v146
	v_and_b32_e32 v221, 0xffff0000, v146
	v_lshlrev_b32_e32 v146, 16, v147
	v_and_b32_e32 v147, 0xffff0000, v147
	s_waitcnt vmcnt(16)
	v_lshlrev_b32_e32 v228, 16, v148
	v_and_b32_e32 v229, 0xffff0000, v148
	v_lshlrev_b32_e32 v148, 16, v149
	v_and_b32_e32 v149, 0xffff0000, v149
	s_waitcnt vmcnt(15)
; __device__ __forceinline__ float bf_lo(unsigned w) { return __uint_as_float(w << 16); }
; __device__ __forceinline__ float bf_hi(unsigned w) { return __uint_as_float(w & 0xffff0000u); }
; __device__ __forceinline__ void p9_final(Frame& F) {
;     ...
;         for (int j = 0; j < 8; ++j) { f32x4 y = {0.f, 0.f, 0.f, 0.f};
; #pragma unroll
;             for (int k = 0; k < 4; ++k) { const float w = aw[k]; y[0] += w * bf_lo(q[k][j].x); y[1] += w * bf_hi(q[k][j].x); y[2] += w * bf_lo(q[k][j].y); y[3] += w * bf_hi(q[k][j].y); }
;             v[j] = x1[j] * DN_ALPHA + ((const f32x4*)(mod + (size_t)b * 12288 + 10240))[lane + 64 * j] * y; s += (v[j][0] + v[j][1]) + (v[j][2] + v[j][3]); }
	v_lshlrev_b32_e32 v236, 16, v150
	v_and_b32_e32 v237, 0xffff0000, v150
	v_lshlrev_b32_e32 v150, 16, v151
	v_and_b32_e32 v151, 0xffff0000, v151
	s_waitcnt vmcnt(14)
	v_lshlrev_b32_e32 v244, 16, v152
	v_and_b32_e32 v245, 0xffff0000, v152
	v_lshlrev_b32_e32 v152, 16, v153
	v_and_b32_e32 v153, 0xffff0000, v153
	v_pk_fma_f32 v[112:113], v[0:1], v[130:131], v[112:113] op_sel:[1,0,0]
	v_pk_fma_f32 v[130:131], v[0:1], v[210:211], v[200:201] op_sel:[1,0,0]
	v_pk_fma_f32 v[114:115], v[0:1], v[132:133], v[114:115] op_sel:[1,0,0]
	v_pk_fma_f32 v[132:133], v[0:1], v[218:219], v[202:203] op_sel:[1,0,0]
	v_pk_fma_f32 v[120:121], v[0:1], v[134:135], v[120:121] op_sel:[1,0,0]
	v_pk_fma_f32 v[134:135], v[0:1], v[226:227], v[208:209] op_sel:[1,0,0]
	v_pk_fma_f32 v[122:123], v[0:1], v[136:137], v[122:123] op_sel:[1,0,0]
	v_pk_fma_f32 v[136:137], v[0:1], v[234:235], v[216:217] op_sel:[1,0,0]
	v_pk_fma_f32 v[124:125], v[0:1], v[138:139], v[124:125] op_sel:[1,0,0]
	v_pk_fma_f32 v[138:139], v[0:1], v[242:243], v[224:225] op_sel:[1,0,0]
	v_pk_fma_f32 v[0:1], v[0:1], v[140:141], v[126:127] op_sel:[1,0,0]
	v_pk_fma_f32 v[126:127], v[2:3], v[196:197], v[248:249] op_sel_hi:[0,1,1]
	v_pk_fma_f32 v[102:103], v[2:3], v[102:103], v[250:251] op_sel_hi:[0,1,1]
	v_pk_fma_f32 v[106:107], v[2:3], v[106:107], v[252:253] op_sel_hi:[0,1,1]
	v_pk_fma_f32 v[110:111], v[2:3], v[118:119], v[110:111] op_sel_hi:[0,1,1]
	s_waitcnt vmcnt(13)
	v_lshlrev_b32_e32 v206, 16, v154
	v_and_b32_e32 v207, 0xffff0000, v154
	v_lshlrev_b32_e32 v154, 16, v155
	v_and_b32_e32 v155, 0xffff0000, v155
	s_waitcnt vmcnt(12)
	v_lshlrev_b32_e32 v214, 16, v156
	v_and_b32_e32 v215, 0xffff0000, v156
	v_lshlrev_b32_e32 v156, 16, v157
	v_and_b32_e32 v157, 0xffff0000, v157
	s_waitcnt vmcnt(11)
	v_lshlrev_b32_e32 v222, 16, v158
	v_and_b32_e32 v223, 0xffff0000, v158
	v_lshlrev_b32_e32 v158, 16, v159
	v_and_b32_e32 v159, 0xffff0000, v159
	s_waitcnt vmcnt(10)
	v_lshlrev_b32_e32 v230, 16, v160
	v_and_b32_e32 v231, 0xffff0000, v160
	v_lshlrev_b32_e32 v160, 16, v161
	v_and_b32_e32 v161, 0xffff0000, v161
	s_waitcnt vmcnt(9)
	v_lshlrev_b32_e32 v238, 16, v162
	v_and_b32_e32 v239, 0xffff0000, v162
	v_lshlrev_b32_e32 v162, 16, v163
	v_and_b32_e32 v163, 0xffff0000, v163
	s_waitcnt vmcnt(8)
	v_lshlrev_b32_e32 v246, 16, v164
	v_and_b32_e32 v247, 0xffff0000, v164
	v_lshlrev_b32_e32 v164, 16, v165
	v_and_b32_e32 v165, 0xffff0000, v165
	v_pk_fma_f32 v[116:117], v[2:3], v[204:205], v[116:117] op_sel_hi:[0,1,1]
	v_pk_fma_f32 v[112:113], v[2:3], v[142:143], v[112:113] op_sel_hi:[0,1,1]
	v_pk_fma_f32 v[118:119], v[2:3], v[212:213], v[130:131] op_sel_hi:[0,1,1]
	v_pk_fma_f32 v[114:115], v[2:3], v[144:145], v[114:115] op_sel_hi:[0,1,1]
	v_pk_fma_f32 v[130:131], v[2:3], v[220:221], v[132:133] op_sel_hi:[0,1,1]
	v_pk_fma_f32 v[120:121], v[2:3], v[146:147], v[120:121] op_sel_hi:[0,1,1]
	v_pk_fma_f32 v[132:133], v[2:3], v[228:229], v[134:135] op_sel_hi:[0,1,1]
	v_pk_fma_f32 v[122:123], v[2:3], v[148:149], v[122:123] op_sel_hi:[0,1,1]
	v_pk_fma_f32 v[134:135], v[2:3], v[236:237], v[136:137] op_sel_hi:[0,1,1]
	v_pk_fma_f32 v[124:125], v[2:3], v[150:151], v[124:125] op_sel_hi:[0,1,1]
	v_pk_fma_f32 v[136:137], v[2:3], v[244:245], v[138:139] op_sel_hi:[0,1,1]
	v_pk_fma_f32 v[0:1], v[2:3], v[152:153], v[0:1] op_sel_hi:[0,1,1]
	v_pk_fma_f32 v[2:3], v[24:25], v[198:199], v[126:127] op_sel_hi:[0,1,1]
	v_pk_fma_f32 v[102:103], v[24:25], v[104:105], v[102:103] op_sel_hi:[0,1,1]
	v_pk_fma_f32 v[104:105], v[24:25], v[108:109], v[106:107] op_sel_hi:[0,1,1]
	v_pk_fma_f32 v[106:107], v[24:25], v[128:129], v[110:111] op_sel_hi:[0,1,1]
	v_pk_fma_f32 v[108:109], v[24:25], v[206:207], v[116:117] op_sel_hi:[0,1,1]
	v_pk_fma_f32 v[110:111], v[24:25], v[154:155], v[112:113] op_sel_hi:[0,1,1]
	v_pk_fma_f32 v[112:113], v[24:25], v[214:215], v[118:119] op_sel_hi:[0,1,1]
	v_pk_fma_f32 v[114:115], v[24:25], v[156:157], v[114:115] op_sel_hi:[0,1,1]
	v_pk_fma_f32 v[116:117], v[24:25], v[222:223], v[130:131] op_sel_hi:[0,1,1]
	v_pk_fma_f32 v[118:119], v[24:25], v[158:159], v[120:121] op_sel_hi:[0,1,1]
	v_pk_fma_f32 v[122:123], v[24:25], v[160:161], v[122:123] op_sel_hi:[0,1,1]
	v_pk_fma_f32 v[124:125], v[24:25], v[162:163], v[124:125] op_sel_hi:[0,1,1]
	v_pk_fma_f32 v[0:1], v[24:25], v[164:165], v[0:1] op_sel_hi:[0,1,1]
	s_waitcnt vmcnt(7)
	v_pk_mul_f32 v[2:3], v[2:3], v[82:83]
	v_pk_mul_f32 v[82:83], v[102:103], v[84:85]
	s_waitcnt vmcnt(6)
	v_pk_mul_f32 v[84:85], v[104:105], v[86:87]
	v_pk_mul_f32 v[86:87], v[106:107], v[88:89]
	v_pk_fma_f32 v[126:127], v[24:25], v[238:239], v[134:135] op_sel_hi:[0,1,1]
	v_pk_fma_f32 v[128:129], v[24:25], v[246:247], v[136:137] op_sel_hi:[0,1,1]
	s_waitcnt vmcnt(5)
	v_pk_mul_f32 v[88:89], v[108:109], v[90:91]
	v_pk_mul_f32 v[90:91], v[110:111], v[92:93]
	s_waitcnt vmcnt(4)
	v_pk_mul_f32 v[92:93], v[112:113], v[94:95]
	v_pk_mul_f32 v[94:95], v[114:115], v[96:97]
	s_waitcnt vmcnt(3)
	v_pk_mul_f32 v[96:97], v[116:117], v[98:99]
	v_pk_mul_f32 v[98:99], v[118:119], v[100:101]
	s_waitcnt vmcnt(2)
	v_pk_mul_f32 v[52:53], v[122:123], v[52:53]
	s_waitcnt vmcnt(1)
	v_pk_mul_f32 v[102:103], v[124:125], v[56:57]
	s_waitcnt vmcnt(0)
; __device__ __forceinline__ float wave_sum(float v) {
; #pragma unroll
;     for (int o = 1; o < 64; o <<= 1) v += __shfl_xor(v, o);
;     return v;
; __device__ __forceinline__ void p9_final(Frame& F) {
;     ...
;             v[j] = x1[j] * DN_ALPHA + ((const f32x4*)(mod + (size_t)b * 12288 + 10240))[lane + 64 * j] * y; s += (v[j][0] + v[j][1]) + (v[j][2] + v[j][3]); }
;         const float mean = wave_sum(s) * (1.f / DM); float s2 = 0.f;
; #pragma unroll
;         for (int j = 0; j < 8; ++j) { v[j] = v[j] - mean; s2 += (v[j][0] * v[j][0] + v[j][1] * v[j][1]) + (v[j][2] * v[j][2] + v[j][3] * v[j][3]); }
	v_pk_mul_f32 v[106:107], v[0:1], v[60:61]
	v_pk_fma_f32 v[82:83], v[168:169], s[12:13], v[82:83] op_sel_hi:[1,0,1]
	v_pk_fma_f32 v[108:109], v[166:167], s[12:13], v[2:3] op_sel_hi:[1,0,1]
	v_pk_fma_f32 v[86:87], v[174:175], s[12:13], v[86:87] op_sel_hi:[1,0,1]
	v_pk_fma_f32 v[84:85], v[172:173], s[12:13], v[84:85] op_sel_hi:[1,0,1]
	v_pk_mul_f32 v[100:101], v[126:127], v[54:55]
	v_pk_mul_f32 v[104:105], v[128:129], v[58:59]
	v_pk_fma_f32 v[90:91], v[178:179], s[12:13], v[90:91] op_sel_hi:[1,0,1]
	v_pk_fma_f32 v[88:89], v[176:177], s[12:13], v[88:89] op_sel_hi:[1,0,1]
	v_pk_fma_f32 v[60:61], v[186:187], s[12:13], v[98:99] op_sel_hi:[1,0,1]
	v_pk_fma_f32 v[58:59], v[184:185], s[12:13], v[96:97] op_sel_hi:[1,0,1]
	v_pk_fma_f32 v[56:57], v[190:191], s[12:13], v[52:53] op_sel_hi:[1,0,1]
	v_pk_fma_f32 v[2:3], v[62:63], s[12:13], v[102:103] op_sel_hi:[1,0,1]
	v_pk_fma_f32 v[52:53], v[64:65], s[12:13], v[106:107] op_sel_hi:[1,0,1]
	v_mov_b32_e32 v62, v108
	v_mov_b32_e32 v63, v84
	v_mov_b32_e32 v64, v109
	v_mov_b32_e32 v65, v85
	v_mov_b32_e32 v96, v82
	v_mov_b32_e32 v97, v86
	v_mov_b32_e32 v98, v83
	v_mov_b32_e32 v99, v87
	v_pk_fma_f32 v[0:1], v[192:193], s[12:13], v[100:101] op_sel_hi:[1,0,1]
	v_pk_mov_b32 v[100:101], v[88:89], v[90:91] op_sel:[1,0]
	v_mov_b32_e32 v102, v88
	v_mov_b32_e32 v103, v91
	v_pk_add_f32 v[62:63], v[62:63], v[64:65]
	v_pk_add_f32 v[64:65], v[96:97], v[98:99]
	v_pk_fma_f32 v[120:121], v[24:25], v[230:231], v[132:133] op_sel_hi:[0,1,1]
	v_pk_add_f32 v[96:97], v[100:101], v[102:103]
	v_pk_add_f32 v[62:63], v[62:63], v[64:65]
	v_pk_mul_f32 v[50:51], v[120:121], v[50:51]
	v_pk_fma_f32 v[94:95], v[182:183], s[12:13], v[94:95] op_sel_hi:[1,0,1]
	v_pk_fma_f32 v[92:93], v[180:181], s[12:13], v[92:93] op_sel_hi:[1,0,1]
	v_pk_add_f32 v[64:65], v[96:97], v[96:97] op_sel:[0,1] op_sel_hi:[1,0]
	v_add_f32_e32 v24, 0, v62
	v_pk_fma_f32 v[54:55], v[188:189], s[12:13], v[50:51] op_sel_hi:[1,0,1]
	v_pk_fma_f32 v[50:51], v[194:195], s[12:13], v[104:105] op_sel_hi:[1,0,1]
	v_add_f32_e32 v104, v92, v93
	v_add_f32_e32 v106, v94, v95
	v_mov_b32_e32 v111, v58
	v_mov_b32_e32 v105, v60
	v_mov_b32_e32 v107, v61
	v_mov_b32_e32 v65, v59
	v_add_f32_e32 v110, v24, v63
	v_pk_mov_b32 v[112:113], v[54:55], v[56:57] op_sel:[1,0]
	v_mov_b32_e32 v114, v54
	v_mov_b32_e32 v115, v57
	v_pk_add_f32 v[98:99], v[104:105], v[106:107]
	v_pk_add_f32 v[62:63], v[110:111], v[64:65]
	v_pk_add_f32 v[100:101], v[112:113], v[114:115]
	v_pk_add_f32 v[62:63], v[62:63], v[98:99]
	v_pk_add_f32 v[96:97], v[100:101], v[100:101] op_sel:[0,1] op_sel_hi:[1,0]
	v_pk_add_f32 v[62:63], v[62:63], v[62:63] op_sel:[0,1] op_sel_hi:[1,0]
	v_add_f32_e32 v116, v0, v1
	v_add_f32_e32 v118, v2, v3
	v_mov_b32_e32 v117, v52
	v_mov_b32_e32 v119, v53
	v_mov_b32_e32 v97, v51
	v_mov_b32_e32 v63, v50
	v_pk_add_f32 v[102:103], v[116:117], v[118:119]
	v_pk_add_f32 v[62:63], v[62:63], v[96:97]
	v_readfirstlane_b32 s2, v10
	v_pk_add_f32 v[62:63], v[62:63], v[102:103]
	v_readfirstlane_b32 s3, v11
	v_add_f32_e32 v24, v62, v63
	s_nop 1
	v_mov_b32_dpp v62, v24 quad_perm:[1,0,3,2] row_mask:0xf bank_mask:0xf
	s_waitcnt lgkmcnt(0)
	v_add_f32_e32 v24, v24, v62
	s_nop 1
	v_mov_b32_dpp v62, v24 quad_perm:[2,3,0,1] row_mask:0xf bank_mask:0xf
	s_waitcnt lgkmcnt(0)
	v_add_f32_e32 v24, v24, v62
	s_nop 1
	v_mov_b32_dpp v62, v24 row_shl:4 row_mask:0xf bank_mask:0x5
	s_nop 1
	v_mov_b32_dpp v62, v24 row_shr:4 row_mask:0xf bank_mask:0xa
	s_waitcnt lgkmcnt(0)
	v_add_f32_e32 v24, v24, v62
	s_nop 1
	v_mov_b32_dpp v62, v24 row_ror:8 row_mask:0xf bank_mask:0xf
	s_waitcnt lgkmcnt(0)
	v_add_f32_e32 v24, v24, v62
	v_mov_b32_e32 v62, v24
	s_nop 1
	v_permlane16_swap_b32_e32 v62, v24
	s_waitcnt lgkmcnt(0)
	v_add_f32_e32 v24, v24, v62
	v_mov_b32_e32 v62, v24
	s_nop 1
	v_permlane32_swap_b32_e32 v62, v24
	s_waitcnt lgkmcnt(0)
	v_add_f32_e32 v24, v24, v62
	v_fmamk_f32 v83, v24, 0xba000000, v83
	v_fmamk_f32 v109, v24, 0xba000000, v109
	v_fmamk_f32 v87, v24, 0xba000000, v87
	v_fmamk_f32 v85, v24, 0xba000000, v85
	v_fmac_f32_e32 v82, 0xba000000, v24
	v_fmac_f32_e32 v108, 0xba000000, v24
	v_fmac_f32_e32 v86, 0xba000000, v24
	v_fmac_f32_e32 v84, 0xba000000, v24
	v_fmamk_f32 v89, v24, 0xba000000, v89
	v_fmac_f32_e32 v88, 0xba000000, v24
	v_fmamk_f32 v91, v24, 0xba000000, v91
	v_fmac_f32_e32 v90, 0xba000000, v24
	v_mov_b32_e32 v64, v109
	v_mov_b32_e32 v65, v85
	v_mov_b32_e32 v98, v83
	v_mov_b32_e32 v99, v87
	v_mov_b32_e32 v62, v108
	v_mov_b32_e32 v63, v84
	v_mov_b32_e32 v96, v82
	v_mov_b32_e32 v97, v86
	v_pk_mul_f32 v[100:101], v[90:91], v[90:91]
	v_pk_mul_f32 v[102:103], v[88:89], v[88:89]
	v_pk_mul_f32 v[64:65], v[64:65], v[64:65]
	v_pk_mul_f32 v[98:99], v[98:99], v[98:99]
	v_fmac_f32_e32 v92, 0xba000000, v24
	v_fmac_f32_e32 v94, 0xba000000, v24
	v_pk_mov_b32 v[116:117], v[102:103], v[100:101] op_sel:[1,0]
	v_mov_b32_e32 v103, v101
	v_pk_fma_f32 v[62:63], v[62:63], v[62:63], v[64:65]
	v_pk_fma_f32 v[64:65], v[96:97], v[96:97], v[98:99]
	v_fmamk_f32 v93, v24, 0xba000000, v93
	v_fmamk_f32 v95, v24, 0xba000000, v95
	v_fmamk_f32 v61, v24, 0xba000000, v61
	v_fmac_f32_e32 v60, 0xba000000, v24
	v_fmamk_f32 v59, v24, 0xba000000, v59
	v_fmac_f32_e32 v58, 0xba000000, v24
	v_fmamk_f32 v55, v24, 0xba000000, v55
	v_fmac_f32_e32 v54, 0xba000000, v24
	v_fmamk_f32 v57, v24, 0xba000000, v57
	v_fmac_f32_e32 v56, 0xba000000, v24
	v_fmamk_f32 v1, v24, 0xba000000, v1
	v_fmac_f32_e32 v0, 0xba000000, v24
	v_fmamk_f32 v3, v24, 0xba000000, v3
	v_fmac_f32_e32 v2, 0xba000000, v24
	v_fmamk_f32 v53, v24, 0xba000000, v53
	v_fmac_f32_e32 v52, 0xba000000, v24
	v_fmamk_f32 v51, v24, 0xba000000, v51
	v_fmac_f32_e32 v50, 0xba000000, v24
	v_mul_f32_e32 v24, v92, v92
; __device__ __forceinline__ float wave_sum(float v) {
; #pragma unroll
;     for (int o = 1; o < 64; o <<= 1) v += __shfl_xor(v, o);
;     return v;
; __device__ __forceinline__ void p9_final(Frame& F) {
;     ...
;         for (int j = 0; j < 8; ++j) { v[j] = v[j] - mean; s2 += (v[j][0] * v[j][0] + v[j][1] * v[j][1]) + (v[j][2] * v[j][2] + v[j][3] * v[j][3]); }
;         const float rstd = 1.f / sqrtf(wave_sum(s2) * (1.f / DM) + LN_EPS);
; #pragma unroll
;         for (int j = 0; j < 8; ++j) __builtin_nontemporal_store(v[j] * rstd * ((const f32x4*)F.in[I_LN2W])[lane + 64 * j] + ((const f32x4*)F.in[I_LN2B])[lane + 64 * j], (f32x4*)(F.out + (size_t)t * DM) + lane + 64 * j);
	v_mul_f32_e32 v104, v94, v94
	v_pk_add_f32 v[96:97], v[116:117], v[102:103]
	v_pk_add_f32 v[62:63], v[62:63], v[64:65]
	v_pk_fma_f32 v[100:101], v[92:93], v[92:93], v[24:25] op_sel_hi:[1,1,0]
	v_pk_fma_f32 v[104:105], v[94:95], v[94:95], v[104:105] op_sel_hi:[1,1,0]
	v_pk_add_f32 v[64:65], v[96:97], v[96:97] op_sel_hi:[0,1]
	v_pk_add_f32 v[62:63], v[62:63], v[62:63] op_sel_hi:[0,1]
	v_pk_mul_f32 v[106:107], v[56:57], v[56:57]
	v_pk_mul_f32 v[110:111], v[54:55], v[54:55]
	v_mul_f32_e32 v100, v58, v58
	v_mul_f32_e32 v104, v59, v59
	v_mul_f32_e32 v64, v60, v60
	v_mul_f32_e32 v62, v61, v61
	v_pk_mov_b32 v[118:119], v[110:111], v[106:107] op_sel:[1,0]
	v_mov_b32_e32 v111, v107
	v_pk_add_f32 v[96:97], v[100:101], v[104:105]
	v_pk_add_f32 v[62:63], v[64:65], v[62:63]
	v_mul_f32_e32 v112, v0, v0
	v_mul_f32_e32 v114, v2, v2
	v_pk_add_f32 v[98:99], v[118:119], v[110:111]
	v_pk_add_f32 v[62:63], v[96:97], v[62:63]
	v_pk_fma_f32 v[106:107], v[0:1], v[0:1], v[112:113] op_sel_hi:[1,1,0]
	v_pk_fma_f32 v[112:113], v[2:3], v[2:3], v[114:115] op_sel_hi:[1,1,0]
	v_pk_add_f32 v[98:99], v[98:99], v[98:99] op_sel_hi:[0,1]
	v_pk_add_f32 v[62:63], v[62:63], v[62:63] op_sel_hi:[0,1]
	v_mul_f32_e32 v106, v50, v50
	v_mul_f32_e32 v112, v51, v51
	v_mul_f32_e32 v98, v52, v52
	v_mul_f32_e32 v62, v53, v53
	v_pk_add_f32 v[100:101], v[106:107], v[112:113]
	v_pk_add_f32 v[62:63], v[98:99], v[62:63]
	s_nop 0
	v_pk_add_f32 v[62:63], v[100:101], v[62:63]
	s_nop 0
	v_add_f32_e32 v24, v62, v63
	s_nop 1
	v_mov_b32_dpp v62, v24 quad_perm:[1,0,3,2] row_mask:0xf bank_mask:0xf
	s_waitcnt lgkmcnt(0)
	v_add_f32_e32 v24, v24, v62
	s_nop 1
	v_mov_b32_dpp v62, v24 quad_perm:[2,3,0,1] row_mask:0xf bank_mask:0xf
	s_waitcnt lgkmcnt(0)
	v_add_f32_e32 v24, v24, v62
	s_nop 1
	v_mov_b32_dpp v62, v24 row_shl:4 row_mask:0xf bank_mask:0x5
	s_nop 1
	v_mov_b32_dpp v62, v24 row_shr:4 row_mask:0xf bank_mask:0xa
	s_waitcnt lgkmcnt(0)
	v_add_f32_e32 v24, v24, v62
	s_nop 1
	v_mov_b32_dpp v62, v24 row_ror:8 row_mask:0xf bank_mask:0xf
	s_waitcnt lgkmcnt(0)
	v_add_f32_e32 v24, v24, v62
	v_mov_b32_e32 v62, v24
	s_nop 1
	v_permlane16_swap_b32_e32 v62, v24
	s_waitcnt lgkmcnt(0)
	v_add_f32_e32 v24, v24, v62
	v_mov_b32_e32 v62, v24
	s_nop 1
	v_permlane32_swap_b32_e32 v62, v24
	s_waitcnt lgkmcnt(0)
	v_add_f32_e32 v24, v24, v62
	v_fmamk_f32 v24, v24, 0x3a000000, v79
	v_mul_f32_e32 v62, 0x4f800000, v24
	v_cmp_gt_f32_e32 vcc, s15, v24
	s_nop 1
	v_cndmask_b32_e32 v24, v24, v62, vcc
	v_sqrt_f32_e32 v62, v24
	s_nop 0
	v_add_u32_e32 v63, -1, v62
	v_add_u32_e32 v64, 1, v62
	v_fma_f32 v65, -v63, v62, v24
	v_fma_f32 v81, -v64, v62, v24
	v_cmp_ge_f32_e64 s[0:1], 0, v65
	s_nop 1
	v_cndmask_b32_e64 v62, v62, v63, s[0:1]
	v_cmp_lt_f32_e64 s[0:1], 0, v81
	s_nop 1
	v_cndmask_b32_e64 v62, v62, v64, s[0:1]
	v_mul_f32_e32 v63, 0x37800000, v62
	v_cndmask_b32_e32 v62, v62, v63, vcc
	v_cmp_class_f32_e32 vcc, v24, v80
	s_nop 1
	v_cndmask_b32_e32 v24, v62, v24, vcc
	v_div_scale_f32 v62, s[0:1], v24, v24, 1.0
	v_rcp_f32_e32 v64, v62
	v_div_scale_f32 v63, vcc, 1.0, v24, 1.0
	v_readfirstlane_b32 s0, v8
	v_fma_f32 v65, -v62, v64, 1.0
	v_fmac_f32_e32 v64, v65, v64
	v_mul_f32_e32 v65, v63, v64
	v_fma_f32 v81, -v62, v65, v63
	v_fmac_f32_e32 v65, v81, v64
	v_fma_f32 v62, -v62, v65, v63
	v_div_fmas_f32 v62, v62, v64, v65
	v_div_fixup_f32 v24, v62, v24, 1.0
	v_pk_mul_f32 v[62:63], v[108:109], v[24:25] op_sel_hi:[1,0]
	v_pk_mul_f32 v[64:65], v[82:83], v[24:25] op_sel_hi:[1,0]
	v_pk_fma_f32 v[16:17], v[16:17], v[62:63], v[20:21]
	v_pk_fma_f32 v[18:19], v[18:19], v[64:65], v[22:23]
	global_store_dwordx4 v[46:47], v[16:19], off offset:-4096 nt
	global_load_dwordx4 v[16:19], v[26:27], off offset:1024
	s_nop 0
	global_load_dwordx4 v[20:23], v[28:29], off offset:1024
	v_pk_mul_f32 v[62:63], v[86:87], v[24:25] op_sel_hi:[1,0]
	v_pk_mul_f32 v[64:65], v[84:85], v[24:25] op_sel_hi:[1,0]
	v_pk_mul_f32 v[60:61], v[60:61], v[24:25] op_sel_hi:[1,0]
	v_pk_mul_f32 v[58:59], v[58:59], v[24:25] op_sel_hi:[1,0]
	v_pk_mul_f32 v[56:57], v[56:57], v[24:25] op_sel_hi:[1,0]
	v_pk_mul_f32 v[54:55], v[54:55], v[24:25] op_sel_hi:[1,0]
	v_pk_mul_f32 v[2:3], v[2:3], v[24:25] op_sel_hi:[1,0]
	v_pk_mul_f32 v[0:1], v[0:1], v[24:25] op_sel_hi:[1,0]
	v_readfirstlane_b32 s1, v9
	v_pk_mul_f32 v[10:11], v[52:53], v[24:25] op_sel_hi:[1,0]
	v_pk_mul_f32 v[8:9], v[50:51], v[24:25] op_sel_hi:[1,0]
	s_and_b64 vcc, s[24:25], exec
	s_waitcnt vmcnt(0)
	v_pk_fma_f32 v[16:17], v[16:17], v[64:65], v[20:21]
	v_pk_fma_f32 v[18:19], v[18:19], v[62:63], v[22:23]
	global_store_dwordx4 v[46:47], v[16:19], off offset:-3072 nt
	global_load_dwordx4 v[16:19], v[26:27], off offset:2048
	s_nop 0
	global_load_dwordx4 v[20:23], v[28:29], off offset:2048
	v_pk_mul_f32 v[62:63], v[90:91], v[24:25] op_sel_hi:[1,0]
	v_pk_mul_f32 v[64:65], v[88:89], v[24:25] op_sel_hi:[1,0]
	s_waitcnt vmcnt(0)
	v_pk_fma_f32 v[18:19], v[18:19], v[62:63], v[22:23]
	v_pk_fma_f32 v[16:17], v[16:17], v[64:65], v[20:21]
	global_store_dwordx4 v[46:47], v[16:19], off offset:-2048 nt
	global_load_dwordx4 v[16:19], v[26:27], off offset:3072
	s_nop 0
	global_load_dwordx4 v[20:23], v[28:29], off offset:3072
	v_pk_mul_f32 v[62:63], v[94:95], v[24:25] op_sel_hi:[1,0]
	v_pk_mul_f32 v[64:65], v[92:93], v[24:25] op_sel_hi:[1,0]
	s_waitcnt vmcnt(0)
	v_pk_fma_f32 v[18:19], v[18:19], v[62:63], v[22:23]
	v_pk_fma_f32 v[16:17], v[16:17], v[64:65], v[20:21]
	global_store_dwordx4 v[46:47], v[16:19], off offset:-1024 nt
	global_load_dwordx4 v[16:19], v[30:31], off
	s_nop 0
	global_load_dwordx4 v[20:23], v[32:33], off
	s_waitcnt vmcnt(0)
	v_pk_fma_f32 v[16:17], v[16:17], v[58:59], v[20:21]
	v_pk_fma_f32 v[18:19], v[18:19], v[60:61], v[22:23]
	global_store_dwordx4 v[46:47], v[16:19], off nt
	global_load_dwordx4 v[16:19], v[34:35], off
	s_nop 0
	global_load_dwordx4 v[20:23], v[36:37], off
	s_waitcnt vmcnt(0)
	v_pk_fma_f32 v[16:17], v[54:55], v[16:17], v[20:21]
	v_pk_fma_f32 v[18:19], v[56:57], v[18:19], v[22:23]
	global_store_dwordx4 v[46:47], v[16:19], off offset:1024 nt
	global_load_dwordx4 v[16:19], v[38:39], off
	s_nop 0
	global_load_dwordx4 v[20:23], v[40:41], off
	s_waitcnt vmcnt(0)
	v_pk_fma_f32 v[0:1], v[0:1], v[16:17], v[20:21]
	v_pk_fma_f32 v[2:3], v[2:3], v[18:19], v[22:23]
	global_store_dwordx4 v[46:47], v[0:3], off offset:2048 nt
	global_load_dwordx4 v[16:19], v[42:43], off
	global_load_dwordx4 v[20:23], v[44:45], off
	v_mov_b64_e32 v[0:1], v[12:13]
	v_mov_b64_e32 v[2:3], v[14:15]
	s_waitcnt vmcnt(0)
	v_pk_fma_f32 v[8:9], v[8:9], v[16:17], v[20:21]
	v_pk_fma_f32 v[10:11], v[10:11], v[18:19], v[22:23]
	global_store_dwordx4 v[46:47], v[8:11], off offset:3072 nt
	v_lshl_add_u64 v[46:47], v[46:47], 0, s[8:9]
	s_cbranch_vccnz .LBB0_1211
